# speedup vs baseline: 1.0008x; 1.0008x over previous
.Lscan_loop_a_st:
	ds_read_b64 v[128:129], v106 offset:96
	ds_read_b64 v[130:131], v106 offset:104
	ds_read_b64 v[132:133], v106 offset:112
	s_waitcnt vmcnt(8)
	global_load_dwordx4 v[146:149], v[196:197], off
	global_load_dwordx4 v[150:153], v[196:197], off offset:512
	global_load_dwordx4 v[154:157], v[196:197], off offset:1024
	v_lshl_add_u64 v[196:197], v[196:197], 0, s[42:43]
	s_waitcnt lgkmcnt(3)
	v_mfma_f32_16x16x128_f8f6f4 v[134:137], v[122:127], v[2:7], 0 cbsz:2 blgp:2
	v_mfma_f32_16x16x128_f8f6f4 v[138:141], v[122:127], v[14:19], 0 cbsz:2 blgp:2
	v_mfma_f32_16x16x128_f8f6f4 v[142:145], v[122:127], v[26:31], v[188:191] cbsz:2 blgp:2
	v_mfma_f32_16x16x128_f8f6f4 v[204:207], v[122:127], v[38:43], 0 cbsz:2 blgp:2
	v_mfma_f32_16x16x128_f8f6f4 v[208:211], v[122:127], v[50:55], 0 cbsz:2 blgp:2
	v_mfma_f32_16x16x128_f8f6f4 v[212:215], v[122:127], v[62:67], v[188:191] cbsz:2 blgp:2
	s_waitcnt lgkmcnt(0)
	v_mfma_f32_16x16x128_f8f6f4 v[134:137], v[128:133], v[8:13], v[134:137] cbsz:2 blgp:2
	v_mfma_f32_16x16x128_f8f6f4 v[204:207], v[128:133], v[44:49], v[204:207] cbsz:2 blgp:2
	v_mfma_f32_16x16x128_f8f6f4 v[138:141], v[128:133], v[20:25], v[138:141] cbsz:2 blgp:2
	v_mfma_f32_16x16x128_f8f6f4 v[208:211], v[128:133], v[56:61], v[208:211] cbsz:2 blgp:2
	v_mfma_f32_16x16x128_f8f6f4 v[142:145], v[128:133], v[32:37], v[142:145] cbsz:2 blgp:2
	v_mfma_f32_16x16x128_f8f6f4 v[212:215], v[128:133], v[68:73], v[212:215] cbsz:2 blgp:2
	v_cndmask_b32_e64 v158, v134, v204, s[4:5]
	v_cndmask_b32_e64 v159, v138, v208, s[4:5]
	v_fma_mix_f32 v158, v158, v1, v82 op_sel_hi:[0,0,1]
	v_fma_mix_f32 v159, v159, v99, v74 op_sel_hi:[0,0,1]
	v_exp_f32_e32 v158, v158
	v_exp_f32_e32 v159, v159
	v_fma_f32 v158, v158, v186, v186
	v_add_f32_e32 v159, 1.0, v159
	v_rcp_f32_e32 v158, v158
	v_rcp_f32_e32 v159, v159
	v_cndmask_b32_e64 v160, v142, v212, s[4:5]
	v_fma_mix_f32 v161, v158, v160, v78 op_sel_hi:[0,0,1]
	v_exp_f32_e32 v161, v161
	s_add_u32 s48, s48, s40
	v_add_f32_e32 v161, 1.0, v161
	v_rcp_f32_e32 v161, v161
	s_addc_u32 s49, s49, s41
	v_fma_f32 v162, v161, -2.0, 1.0
	v_sub_f32_e32 v163, v176, v162
	v_fma_f32 v176, v159, v163, v162
	v_fma_f32 v164, |v176|, s16, v117
	v_fma_f32 v165, |v176|, s17, v118
	v_fma_f32 v166, |v176|, s18, v119
	v_lshrrev_b32_e32 v167, 26, v176
	v_min3_u32 v164, v164, v165, v166
	v_bfi_b32 v168, 31, v164, v167
	s_nop 1
	v_mul_u32_u24_dpp v170, v168, v180 quad_perm:[1,2,3,3] row_mask:0xf bank_mask:0xf bound_ctrl:1
	v_mad_u32_u24 v171, v168, v181, v170
	ds_write_b8_d16_hi v184, v171 offset:416
	global_store_short_d16_hi v185, v176, s[48:49]
	s_waitcnt lgkmcnt(0)
	s_barrier
	ds_read_b64 v[122:123], v106 offset:416
	ds_read_b64 v[124:125], v106 offset:424
	ds_read_b64 v[126:127], v106 offset:432
	s_barrier
	ds_read_b64 v[128:129], v106 offset:512
	ds_read_b64 v[130:131], v106 offset:520
	ds_read_b64 v[132:133], v106 offset:528
	s_waitcnt lgkmcnt(3)
	v_mfma_f32_16x16x128_f8f6f4 v[134:137], v[122:127], v[2:7], 0 cbsz:2 blgp:2
	v_mfma_f32_16x16x128_f8f6f4 v[138:141], v[122:127], v[14:19], 0 cbsz:2 blgp:2
	v_mfma_f32_16x16x128_f8f6f4 v[142:145], v[122:127], v[26:31], v[188:191] cbsz:2 blgp:2
	v_mfma_f32_16x16x128_f8f6f4 v[204:207], v[122:127], v[38:43], 0 cbsz:2 blgp:2
	v_mfma_f32_16x16x128_f8f6f4 v[208:211], v[122:127], v[50:55], 0 cbsz:2 blgp:2
	v_mfma_f32_16x16x128_f8f6f4 v[212:215], v[122:127], v[62:67], v[188:191] cbsz:2 blgp:2
	s_waitcnt lgkmcnt(0)
	v_mfma_f32_16x16x128_f8f6f4 v[134:137], v[128:133], v[8:13], v[134:137] cbsz:2 blgp:2
	v_mfma_f32_16x16x128_f8f6f4 v[204:207], v[128:133], v[44:49], v[204:207] cbsz:2 blgp:2
	v_mfma_f32_16x16x128_f8f6f4 v[138:141], v[128:133], v[20:25], v[138:141] cbsz:2 blgp:2
	v_mfma_f32_16x16x128_f8f6f4 v[208:211], v[128:133], v[56:61], v[208:211] cbsz:2 blgp:2
	v_mfma_f32_16x16x128_f8f6f4 v[142:145], v[128:133], v[32:37], v[142:145] cbsz:2 blgp:2
	v_mfma_f32_16x16x128_f8f6f4 v[212:215], v[128:133], v[68:73], v[212:215] cbsz:2 blgp:2
	v_cndmask_b32_e64 v158, v134, v204, s[4:5]
	v_cndmask_b32_e64 v159, v138, v208, s[4:5]
	v_fma_mix_f32 v158, v158, v1, v82 op_sel:[0,0,1] op_sel_hi:[0,0,1]
	v_fma_mix_f32 v159, v159, v99, v74 op_sel:[0,0,1] op_sel_hi:[0,0,1]
	v_exp_f32_e32 v158, v158
	v_exp_f32_e32 v159, v159
	v_fma_f32 v158, v158, v186, v186
	v_add_f32_e32 v159, 1.0, v159
	v_rcp_f32_e32 v158, v158
	v_rcp_f32_e32 v159, v159
	v_cndmask_b32_e64 v160, v142, v212, s[4:5]
	v_fma_mix_f32 v161, v158, v160, v78 op_sel:[0,0,1] op_sel_hi:[0,0,1]
	v_exp_f32_e32 v161, v161
	s_add_u32 s48, s48, s40
	v_add_f32_e32 v161, 1.0, v161
	v_rcp_f32_e32 v161, v161
	s_addc_u32 s49, s49, s41
	v_fma_f32 v162, v161, -2.0, 1.0
	v_sub_f32_e32 v163, v176, v162
	v_fma_f32 v176, v159, v163, v162
	v_fma_f32 v164, |v176|, s16, v117
	v_fma_f32 v165, |v176|, s17, v118
	v_fma_f32 v166, |v176|, s18, v119
	v_lshrrev_b32_e32 v167, 26, v176
	v_min3_u32 v164, v164, v165, v166
	v_bfi_b32 v168, 31, v164, v167
	s_nop 1
	v_mul_u32_u24_dpp v170, v168, v180 quad_perm:[1,2,3,3] row_mask:0xf bank_mask:0xf bound_ctrl:1
	v_mad_u32_u24 v171, v168, v181, v170
	ds_write_b8_d16_hi v184, v171
	global_store_short_d16_hi v185, v176, s[48:49]
	s_waitcnt lgkmcnt(0)
	s_barrier
	ds_read_b64 v[122:123], v106 offset:0
	ds_read_b64 v[124:125], v106 offset:8
	ds_read_b64 v[126:127], v106 offset:16
	s_barrier
	ds_read_b64 v[128:129], v106 offset:96
	ds_read_b64 v[130:131], v106 offset:104
	ds_read_b64 v[132:133], v106 offset:112
	s_waitcnt lgkmcnt(3)
	v_mfma_f32_16x16x128_f8f6f4 v[134:137], v[122:127], v[2:7], 0 cbsz:2 blgp:2
	v_mfma_f32_16x16x128_f8f6f4 v[138:141], v[122:127], v[14:19], 0 cbsz:2 blgp:2
	v_mfma_f32_16x16x128_f8f6f4 v[142:145], v[122:127], v[26:31], v[188:191] cbsz:2 blgp:2
	v_mfma_f32_16x16x128_f8f6f4 v[204:207], v[122:127], v[38:43], 0 cbsz:2 blgp:2
	v_mfma_f32_16x16x128_f8f6f4 v[208:211], v[122:127], v[50:55], 0 cbsz:2 blgp:2
	v_mfma_f32_16x16x128_f8f6f4 v[212:215], v[122:127], v[62:67], v[188:191] cbsz:2 blgp:2
	s_waitcnt lgkmcnt(0)
	v_mfma_f32_16x16x128_f8f6f4 v[134:137], v[128:133], v[8:13], v[134:137] cbsz:2 blgp:2
	v_mfma_f32_16x16x128_f8f6f4 v[204:207], v[128:133], v[44:49], v[204:207] cbsz:2 blgp:2
	v_mfma_f32_16x16x128_f8f6f4 v[138:141], v[128:133], v[20:25], v[138:141] cbsz:2 blgp:2
	v_mfma_f32_16x16x128_f8f6f4 v[208:211], v[128:133], v[56:61], v[208:211] cbsz:2 blgp:2
	v_mfma_f32_16x16x128_f8f6f4 v[142:145], v[128:133], v[32:37], v[142:145] cbsz:2 blgp:2
	v_mfma_f32_16x16x128_f8f6f4 v[212:215], v[128:133], v[68:73], v[212:215] cbsz:2 blgp:2
	v_cndmask_b32_e64 v158, v134, v204, s[4:5]
	v_cndmask_b32_e64 v159, v138, v208, s[4:5]
	v_fma_mix_f32 v158, v158, v1, v83 op_sel_hi:[0,0,1]
	v_fma_mix_f32 v159, v159, v99, v75 op_sel_hi:[0,0,1]
	v_exp_f32_e32 v158, v158
	v_exp_f32_e32 v159, v159
	v_fma_f32 v158, v158, v186, v186
	v_add_f32_e32 v159, 1.0, v159
	v_rcp_f32_e32 v158, v158
	v_rcp_f32_e32 v159, v159
	v_cndmask_b32_e64 v160, v142, v212, s[4:5]
	v_fma_mix_f32 v161, v158, v160, v79 op_sel_hi:[0,0,1]
	v_exp_f32_e32 v161, v161
	s_add_u32 s48, s48, s40
	v_add_f32_e32 v161, 1.0, v161
	v_rcp_f32_e32 v161, v161
	s_addc_u32 s49, s49, s41
	v_fma_f32 v162, v161, -2.0, 1.0
	v_sub_f32_e32 v163, v176, v162
	v_fma_f32 v176, v159, v163, v162
	v_fma_f32 v164, |v176|, s16, v117
	v_fma_f32 v165, |v176|, s17, v118
	v_fma_f32 v166, |v176|, s18, v119
	v_lshrrev_b32_e32 v167, 26, v176
	v_min3_u32 v164, v164, v165, v166
	v_bfi_b32 v168, 31, v164, v167
	s_nop 1
	v_mul_u32_u24_dpp v170, v168, v180 quad_perm:[1,2,3,3] row_mask:0xf bank_mask:0xf bound_ctrl:1
	v_mad_u32_u24 v171, v168, v181, v170
	ds_write_b8_d16_hi v184, v171 offset:416
	global_store_short_d16_hi v185, v176, s[48:49]
	s_waitcnt lgkmcnt(0)
	s_barrier
	ds_read_b64 v[122:123], v106 offset:416
	ds_read_b64 v[124:125], v106 offset:424
	ds_read_b64 v[126:127], v106 offset:432
	s_barrier
	ds_read_b64 v[128:129], v106 offset:512
	ds_read_b64 v[130:131], v106 offset:520
	ds_read_b64 v[132:133], v106 offset:528
	s_waitcnt lgkmcnt(3)
	v_mfma_f32_16x16x128_f8f6f4 v[134:137], v[122:127], v[2:7], 0 cbsz:2 blgp:2
	v_mfma_f32_16x16x128_f8f6f4 v[138:141], v[122:127], v[14:19], 0 cbsz:2 blgp:2
	v_mfma_f32_16x16x128_f8f6f4 v[142:145], v[122:127], v[26:31], v[188:191] cbsz:2 blgp:2
	v_mfma_f32_16x16x128_f8f6f4 v[204:207], v[122:127], v[38:43], 0 cbsz:2 blgp:2
	v_mfma_f32_16x16x128_f8f6f4 v[208:211], v[122:127], v[50:55], 0 cbsz:2 blgp:2
	v_mfma_f32_16x16x128_f8f6f4 v[212:215], v[122:127], v[62:67], v[188:191] cbsz:2 blgp:2
	s_waitcnt lgkmcnt(0)
	v_mfma_f32_16x16x128_f8f6f4 v[134:137], v[128:133], v[8:13], v[134:137] cbsz:2 blgp:2
	v_mfma_f32_16x16x128_f8f6f4 v[204:207], v[128:133], v[44:49], v[204:207] cbsz:2 blgp:2
	v_mfma_f32_16x16x128_f8f6f4 v[138:141], v[128:133], v[20:25], v[138:141] cbsz:2 blgp:2
	v_mfma_f32_16x16x128_f8f6f4 v[208:211], v[128:133], v[56:61], v[208:211] cbsz:2 blgp:2
	v_mfma_f32_16x16x128_f8f6f4 v[142:145], v[128:133], v[32:37], v[142:145] cbsz:2 blgp:2
	v_mfma_f32_16x16x128_f8f6f4 v[212:215], v[128:133], v[68:73], v[212:215] cbsz:2 blgp:2
	v_cndmask_b32_e64 v158, v134, v204, s[4:5]
	v_cndmask_b32_e64 v159, v138, v208, s[4:5]
	v_fma_mix_f32 v158, v158, v1, v83 op_sel:[0,0,1] op_sel_hi:[0,0,1]
	v_fma_mix_f32 v159, v159, v99, v75 op_sel:[0,0,1] op_sel_hi:[0,0,1]
	v_exp_f32_e32 v158, v158
	v_exp_f32_e32 v159, v159
	v_fma_f32 v158, v158, v186, v186
	v_add_f32_e32 v159, 1.0, v159
	v_rcp_f32_e32 v158, v158
	v_rcp_f32_e32 v159, v159
	v_cndmask_b32_e64 v160, v142, v212, s[4:5]
	v_fma_mix_f32 v161, v158, v160, v79 op_sel:[0,0,1] op_sel_hi:[0,0,1]
	v_exp_f32_e32 v161, v161
	s_add_u32 s48, s48, s40
	v_add_f32_e32 v161, 1.0, v161
	v_rcp_f32_e32 v161, v161
	s_addc_u32 s49, s49, s41
	v_fma_f32 v162, v161, -2.0, 1.0
	v_sub_f32_e32 v163, v176, v162
	v_fma_f32 v176, v159, v163, v162
	v_fma_f32 v164, |v176|, s16, v117
	v_fma_f32 v165, |v176|, s17, v118
	v_fma_f32 v166, |v176|, s18, v119
	v_lshrrev_b32_e32 v167, 26, v176
	v_min3_u32 v164, v164, v165, v166
	v_bfi_b32 v168, 31, v164, v167
	s_nop 1
	v_mul_u32_u24_dpp v170, v168, v180 quad_perm:[1,2,3,3] row_mask:0xf bank_mask:0xf bound_ctrl:1
	v_mad_u32_u24 v171, v168, v181, v170
	ds_write_b8_d16_hi v184, v171
	global_store_short_d16_hi v185, v176, s[48:49]
	s_waitcnt lgkmcnt(0)
	s_barrier
	ds_read_b64 v[122:123], v106 offset:0
	ds_read_b64 v[124:125], v106 offset:8
	ds_read_b64 v[126:127], v106 offset:16
	s_barrier
	ds_read_b64 v[128:129], v106 offset:96
	ds_read_b64 v[130:131], v106 offset:104
	ds_read_b64 v[132:133], v106 offset:112
	s_waitcnt lgkmcnt(3)
	v_mfma_f32_16x16x128_f8f6f4 v[134:137], v[122:127], v[2:7], 0 cbsz:2 blgp:2
	v_mfma_f32_16x16x128_f8f6f4 v[138:141], v[122:127], v[14:19], 0 cbsz:2 blgp:2
	v_mfma_f32_16x16x128_f8f6f4 v[142:145], v[122:127], v[26:31], v[188:191] cbsz:2 blgp:2
	v_mfma_f32_16x16x128_f8f6f4 v[204:207], v[122:127], v[38:43], 0 cbsz:2 blgp:2
	v_mfma_f32_16x16x128_f8f6f4 v[208:211], v[122:127], v[50:55], 0 cbsz:2 blgp:2
	v_mfma_f32_16x16x128_f8f6f4 v[212:215], v[122:127], v[62:67], v[188:191] cbsz:2 blgp:2
	s_waitcnt lgkmcnt(0)
	v_mfma_f32_16x16x128_f8f6f4 v[134:137], v[128:133], v[8:13], v[134:137] cbsz:2 blgp:2
	v_mfma_f32_16x16x128_f8f6f4 v[204:207], v[128:133], v[44:49], v[204:207] cbsz:2 blgp:2
	v_mfma_f32_16x16x128_f8f6f4 v[138:141], v[128:133], v[20:25], v[138:141] cbsz:2 blgp:2
	v_mfma_f32_16x16x128_f8f6f4 v[208:211], v[128:133], v[56:61], v[208:211] cbsz:2 blgp:2
	v_mfma_f32_16x16x128_f8f6f4 v[142:145], v[128:133], v[32:37], v[142:145] cbsz:2 blgp:2
	v_mfma_f32_16x16x128_f8f6f4 v[212:215], v[128:133], v[68:73], v[212:215] cbsz:2 blgp:2
	v_cndmask_b32_e64 v158, v134, v204, s[4:5]
	v_cndmask_b32_e64 v159, v138, v208, s[4:5]
	v_fma_mix_f32 v158, v158, v1, v84 op_sel_hi:[0,0,1]
	v_fma_mix_f32 v159, v159, v99, v76 op_sel_hi:[0,0,1]
	v_exp_f32_e32 v158, v158
	v_exp_f32_e32 v159, v159
	v_fma_f32 v158, v158, v186, v186
	v_add_f32_e32 v159, 1.0, v159
	v_rcp_f32_e32 v158, v158
	v_rcp_f32_e32 v159, v159
	v_cndmask_b32_e64 v160, v142, v212, s[4:5]
	v_fma_mix_f32 v161, v158, v160, v80 op_sel_hi:[0,0,1]
	v_exp_f32_e32 v161, v161
	s_add_u32 s48, s48, s40
	v_add_f32_e32 v161, 1.0, v161
	v_rcp_f32_e32 v161, v161
	s_addc_u32 s49, s49, s41
	v_fma_f32 v162, v161, -2.0, 1.0
	v_sub_f32_e32 v163, v176, v162
	v_fma_f32 v176, v159, v163, v162
	v_fma_f32 v164, |v176|, s16, v117
	v_fma_f32 v165, |v176|, s17, v118
	v_fma_f32 v166, |v176|, s18, v119
	v_lshrrev_b32_e32 v167, 26, v176
	v_min3_u32 v164, v164, v165, v166
	v_bfi_b32 v168, 31, v164, v167
	s_nop 1
	v_mul_u32_u24_dpp v170, v168, v180 quad_perm:[1,2,3,3] row_mask:0xf bank_mask:0xf bound_ctrl:1
	v_mad_u32_u24 v171, v168, v181, v170
	ds_write_b8_d16_hi v184, v171 offset:416
	global_store_short_d16_hi v185, v176, s[48:49]
	s_waitcnt lgkmcnt(0)
	s_barrier
	ds_read_b64 v[122:123], v106 offset:416
	ds_read_b64 v[124:125], v106 offset:424
	ds_read_b64 v[126:127], v106 offset:432
	s_barrier
	ds_read_b64 v[128:129], v106 offset:512
	ds_read_b64 v[130:131], v106 offset:520
	ds_read_b64 v[132:133], v106 offset:528
	s_waitcnt lgkmcnt(3)
	v_mfma_f32_16x16x128_f8f6f4 v[134:137], v[122:127], v[2:7], 0 cbsz:2 blgp:2
	v_mfma_f32_16x16x128_f8f6f4 v[138:141], v[122:127], v[14:19], 0 cbsz:2 blgp:2
	v_mfma_f32_16x16x128_f8f6f4 v[142:145], v[122:127], v[26:31], v[188:191] cbsz:2 blgp:2
	v_mfma_f32_16x16x128_f8f6f4 v[204:207], v[122:127], v[38:43], 0 cbsz:2 blgp:2
	v_mfma_f32_16x16x128_f8f6f4 v[208:211], v[122:127], v[50:55], 0 cbsz:2 blgp:2
	v_mfma_f32_16x16x128_f8f6f4 v[212:215], v[122:127], v[62:67], v[188:191] cbsz:2 blgp:2
	s_waitcnt lgkmcnt(0)
	v_mfma_f32_16x16x128_f8f6f4 v[134:137], v[128:133], v[8:13], v[134:137] cbsz:2 blgp:2
	v_mfma_f32_16x16x128_f8f6f4 v[204:207], v[128:133], v[44:49], v[204:207] cbsz:2 blgp:2
	v_mfma_f32_16x16x128_f8f6f4 v[138:141], v[128:133], v[20:25], v[138:141] cbsz:2 blgp:2
	v_mfma_f32_16x16x128_f8f6f4 v[208:211], v[128:133], v[56:61], v[208:211] cbsz:2 blgp:2
	v_mfma_f32_16x16x128_f8f6f4 v[142:145], v[128:133], v[32:37], v[142:145] cbsz:2 blgp:2
	v_mfma_f32_16x16x128_f8f6f4 v[212:215], v[128:133], v[68:73], v[212:215] cbsz:2 blgp:2
	v_cndmask_b32_e64 v158, v134, v204, s[4:5]
	v_cndmask_b32_e64 v159, v138, v208, s[4:5]
	v_fma_mix_f32 v158, v158, v1, v84 op_sel:[0,0,1] op_sel_hi:[0,0,1]
	v_fma_mix_f32 v159, v159, v99, v76 op_sel:[0,0,1] op_sel_hi:[0,0,1]
	v_exp_f32_e32 v158, v158
	v_exp_f32_e32 v159, v159
	v_fma_f32 v158, v158, v186, v186
	v_add_f32_e32 v159, 1.0, v159
	v_rcp_f32_e32 v158, v158
	v_rcp_f32_e32 v159, v159
	v_cndmask_b32_e64 v160, v142, v212, s[4:5]
	v_fma_mix_f32 v161, v158, v160, v80 op_sel:[0,0,1] op_sel_hi:[0,0,1]
	v_exp_f32_e32 v161, v161
	s_add_u32 s48, s48, s40
	v_add_f32_e32 v161, 1.0, v161
	v_rcp_f32_e32 v161, v161
	s_addc_u32 s49, s49, s41
	v_fma_f32 v162, v161, -2.0, 1.0
	v_sub_f32_e32 v163, v176, v162
	v_fma_f32 v176, v159, v163, v162
	v_fma_f32 v164, |v176|, s16, v117
	v_fma_f32 v165, |v176|, s17, v118
	v_fma_f32 v166, |v176|, s18, v119
	v_lshrrev_b32_e32 v167, 26, v176
	v_min3_u32 v164, v164, v165, v166
	v_bfi_b32 v168, 31, v164, v167
	s_nop 1
	v_mul_u32_u24_dpp v170, v168, v180 quad_perm:[1,2,3,3] row_mask:0xf bank_mask:0xf bound_ctrl:1
	v_mad_u32_u24 v171, v168, v181, v170
	ds_write_b8_d16_hi v184, v171
	global_store_short_d16_hi v185, v176, s[48:49]
	s_waitcnt lgkmcnt(0)
	s_barrier
	ds_read_b64 v[122:123], v106 offset:0
	ds_read_b64 v[124:125], v106 offset:8
	ds_read_b64 v[126:127], v106 offset:16
	s_barrier
	ds_read_b64 v[128:129], v106 offset:96
	ds_read_b64 v[130:131], v106 offset:104
	ds_read_b64 v[132:133], v106 offset:112
	s_waitcnt lgkmcnt(3)
	v_mfma_f32_16x16x128_f8f6f4 v[134:137], v[122:127], v[2:7], 0 cbsz:2 blgp:2
	v_mfma_f32_16x16x128_f8f6f4 v[138:141], v[122:127], v[14:19], 0 cbsz:2 blgp:2
	v_mfma_f32_16x16x128_f8f6f4 v[142:145], v[122:127], v[26:31], v[188:191] cbsz:2 blgp:2
	v_mfma_f32_16x16x128_f8f6f4 v[204:207], v[122:127], v[38:43], 0 cbsz:2 blgp:2
	v_mfma_f32_16x16x128_f8f6f4 v[208:211], v[122:127], v[50:55], 0 cbsz:2 blgp:2
	v_mfma_f32_16x16x128_f8f6f4 v[212:215], v[122:127], v[62:67], v[188:191] cbsz:2 blgp:2
	s_waitcnt lgkmcnt(0)
	v_mfma_f32_16x16x128_f8f6f4 v[134:137], v[128:133], v[8:13], v[134:137] cbsz:2 blgp:2
	v_mfma_f32_16x16x128_f8f6f4 v[204:207], v[128:133], v[44:49], v[204:207] cbsz:2 blgp:2
	v_mfma_f32_16x16x128_f8f6f4 v[138:141], v[128:133], v[20:25], v[138:141] cbsz:2 blgp:2
	v_mfma_f32_16x16x128_f8f6f4 v[208:211], v[128:133], v[56:61], v[208:211] cbsz:2 blgp:2
	v_mfma_f32_16x16x128_f8f6f4 v[142:145], v[128:133], v[32:37], v[142:145] cbsz:2 blgp:2
	v_mfma_f32_16x16x128_f8f6f4 v[212:215], v[128:133], v[68:73], v[212:215] cbsz:2 blgp:2
	v_cndmask_b32_e64 v158, v134, v204, s[4:5]
	v_cndmask_b32_e64 v159, v138, v208, s[4:5]
	v_fma_mix_f32 v158, v158, v1, v85 op_sel_hi:[0,0,1]
	v_fma_mix_f32 v159, v159, v99, v77 op_sel_hi:[0,0,1]
	v_exp_f32_e32 v158, v158
	v_exp_f32_e32 v159, v159
	v_fma_f32 v158, v158, v186, v186
	v_add_f32_e32 v159, 1.0, v159
	v_rcp_f32_e32 v158, v158
	v_rcp_f32_e32 v159, v159
	v_cndmask_b32_e64 v160, v142, v212, s[4:5]
	v_fma_mix_f32 v161, v158, v160, v81 op_sel_hi:[0,0,1]
	v_exp_f32_e32 v161, v161
	s_add_u32 s48, s48, s40
	v_add_f32_e32 v161, 1.0, v161
	v_rcp_f32_e32 v161, v161
	s_addc_u32 s49, s49, s41
	v_fma_f32 v162, v161, -2.0, 1.0
	v_sub_f32_e32 v163, v176, v162
	v_fma_f32 v176, v159, v163, v162
	v_fma_f32 v164, |v176|, s16, v117
	v_fma_f32 v165, |v176|, s17, v118
	v_fma_f32 v166, |v176|, s18, v119
	v_lshrrev_b32_e32 v167, 26, v176
	v_min3_u32 v164, v164, v165, v166
	v_bfi_b32 v168, 31, v164, v167
	s_nop 1
	v_mul_u32_u24_dpp v170, v168, v180 quad_perm:[1,2,3,3] row_mask:0xf bank_mask:0xf bound_ctrl:1
	v_mad_u32_u24 v171, v168, v181, v170
	ds_write_b8_d16_hi v184, v171 offset:416
	global_store_short_d16_hi v185, v176, s[48:49]
	s_waitcnt lgkmcnt(0)
	s_barrier
	ds_read_b64 v[122:123], v106 offset:416
	ds_read_b64 v[124:125], v106 offset:424
	ds_read_b64 v[126:127], v106 offset:432
	s_barrier
	ds_read_b64 v[128:129], v106 offset:512
	ds_read_b64 v[130:131], v106 offset:520
	ds_read_b64 v[132:133], v106 offset:528
	s_waitcnt lgkmcnt(3)
	v_mfma_f32_16x16x128_f8f6f4 v[134:137], v[122:127], v[2:7], 0 cbsz:2 blgp:2
	v_mfma_f32_16x16x128_f8f6f4 v[138:141], v[122:127], v[14:19], 0 cbsz:2 blgp:2
	v_mfma_f32_16x16x128_f8f6f4 v[142:145], v[122:127], v[26:31], v[188:191] cbsz:2 blgp:2
	v_mfma_f32_16x16x128_f8f6f4 v[204:207], v[122:127], v[38:43], 0 cbsz:2 blgp:2
	v_mfma_f32_16x16x128_f8f6f4 v[208:211], v[122:127], v[50:55], 0 cbsz:2 blgp:2
	v_mfma_f32_16x16x128_f8f6f4 v[212:215], v[122:127], v[62:67], v[188:191] cbsz:2 blgp:2
	s_waitcnt lgkmcnt(0)
	v_mfma_f32_16x16x128_f8f6f4 v[134:137], v[128:133], v[8:13], v[134:137] cbsz:2 blgp:2
	v_mfma_f32_16x16x128_f8f6f4 v[204:207], v[128:133], v[44:49], v[204:207] cbsz:2 blgp:2
	v_mfma_f32_16x16x128_f8f6f4 v[138:141], v[128:133], v[20:25], v[138:141] cbsz:2 blgp:2
	v_mfma_f32_16x16x128_f8f6f4 v[208:211], v[128:133], v[56:61], v[208:211] cbsz:2 blgp:2
	v_mfma_f32_16x16x128_f8f6f4 v[142:145], v[128:133], v[32:37], v[142:145] cbsz:2 blgp:2
	v_mfma_f32_16x16x128_f8f6f4 v[212:215], v[128:133], v[68:73], v[212:215] cbsz:2 blgp:2
	v_cndmask_b32_e64 v158, v134, v204, s[4:5]
	v_cndmask_b32_e64 v159, v138, v208, s[4:5]
	v_fma_mix_f32 v158, v158, v1, v85 op_sel:[0,0,1] op_sel_hi:[0,0,1]
	v_fma_mix_f32 v159, v159, v99, v77 op_sel:[0,0,1] op_sel_hi:[0,0,1]
	v_exp_f32_e32 v158, v158
	v_exp_f32_e32 v159, v159
	v_fma_f32 v158, v158, v186, v186
	v_add_f32_e32 v159, 1.0, v159
	v_rcp_f32_e32 v158, v158
	v_rcp_f32_e32 v159, v159
	v_cndmask_b32_e64 v160, v142, v212, s[4:5]
	v_fma_mix_f32 v161, v158, v160, v81 op_sel:[0,0,1] op_sel_hi:[0,0,1]
	v_exp_f32_e32 v161, v161
	s_add_u32 s48, s48, s40
	v_add_f32_e32 v161, 1.0, v161
	v_rcp_f32_e32 v161, v161
	s_addc_u32 s49, s49, s41
	v_fma_f32 v162, v161, -2.0, 1.0
	v_sub_f32_e32 v163, v176, v162
	v_fma_f32 v176, v159, v163, v162
	v_fma_f32 v164, |v176|, s16, v117
	v_fma_f32 v165, |v176|, s17, v118
	v_fma_f32 v166, |v176|, s18, v119
	v_lshrrev_b32_e32 v167, 26, v176
	v_min3_u32 v164, v164, v165, v166
	v_bfi_b32 v168, 31, v164, v167
	s_nop 1
	v_mul_u32_u24_dpp v170, v168, v180 quad_perm:[1,2,3,3] row_mask:0xf bank_mask:0xf bound_ctrl:1
	v_mad_u32_u24 v171, v168, v181, v170
	ds_write_b8_d16_hi v184, v171
	global_store_short_d16_hi v185, v176, s[48:49]
	s_waitcnt lgkmcnt(0)
	s_barrier
	ds_read_b64 v[122:123], v106 offset:0
	ds_read_b64 v[124:125], v106 offset:8
	ds_read_b64 v[126:127], v106 offset:16
	s_barrier
	ds_read_b64 v[128:129], v106 offset:96
	ds_read_b64 v[130:131], v106 offset:104
	ds_read_b64 v[132:133], v106 offset:112
	s_waitcnt vmcnt(8)
	global_load_dwordx4 v[82:85], v[196:197], off
	global_load_dwordx4 v[74:77], v[196:197], off offset:512
	global_load_dwordx4 v[78:81], v[196:197], off offset:1024
	v_lshl_add_u64 v[196:197], v[196:197], 0, s[42:43]
	s_waitcnt lgkmcnt(3)
	v_mfma_f32_16x16x128_f8f6f4 v[134:137], v[122:127], v[2:7], 0 cbsz:2 blgp:2
	v_mfma_f32_16x16x128_f8f6f4 v[138:141], v[122:127], v[14:19], 0 cbsz:2 blgp:2
	v_mfma_f32_16x16x128_f8f6f4 v[142:145], v[122:127], v[26:31], v[188:191] cbsz:2 blgp:2
	v_mfma_f32_16x16x128_f8f6f4 v[204:207], v[122:127], v[38:43], 0 cbsz:2 blgp:2
	v_mfma_f32_16x16x128_f8f6f4 v[208:211], v[122:127], v[50:55], 0 cbsz:2 blgp:2
	v_mfma_f32_16x16x128_f8f6f4 v[212:215], v[122:127], v[62:67], v[188:191] cbsz:2 blgp:2
	s_waitcnt lgkmcnt(0)
	v_mfma_f32_16x16x128_f8f6f4 v[134:137], v[128:133], v[8:13], v[134:137] cbsz:2 blgp:2
	v_mfma_f32_16x16x128_f8f6f4 v[204:207], v[128:133], v[44:49], v[204:207] cbsz:2 blgp:2
	v_mfma_f32_16x16x128_f8f6f4 v[138:141], v[128:133], v[20:25], v[138:141] cbsz:2 blgp:2
	v_mfma_f32_16x16x128_f8f6f4 v[208:211], v[128:133], v[56:61], v[208:211] cbsz:2 blgp:2
	v_mfma_f32_16x16x128_f8f6f4 v[142:145], v[128:133], v[32:37], v[142:145] cbsz:2 blgp:2
	v_mfma_f32_16x16x128_f8f6f4 v[212:215], v[128:133], v[68:73], v[212:215] cbsz:2 blgp:2
	v_cndmask_b32_e64 v158, v134, v204, s[4:5]
	v_cndmask_b32_e64 v159, v138, v208, s[4:5]
	v_fma_mix_f32 v158, v158, v1, v146 op_sel_hi:[0,0,1]
	v_fma_mix_f32 v159, v159, v99, v150 op_sel_hi:[0,0,1]
	v_exp_f32_e32 v158, v158
	v_exp_f32_e32 v159, v159
	v_fma_f32 v158, v158, v186, v186
	v_add_f32_e32 v159, 1.0, v159
	v_rcp_f32_e32 v158, v158
	v_rcp_f32_e32 v159, v159
	v_cndmask_b32_e64 v160, v142, v212, s[4:5]
	v_fma_mix_f32 v161, v158, v160, v154 op_sel_hi:[0,0,1]
	v_exp_f32_e32 v161, v161
	s_add_u32 s48, s48, s40
	v_add_f32_e32 v161, 1.0, v161
	v_rcp_f32_e32 v161, v161
	s_addc_u32 s49, s49, s41
	v_fma_f32 v162, v161, -2.0, 1.0
	v_sub_f32_e32 v163, v176, v162
	v_fma_f32 v176, v159, v163, v162
	v_fma_f32 v164, |v176|, s16, v117
	v_fma_f32 v165, |v176|, s17, v118
	v_fma_f32 v166, |v176|, s18, v119
	v_lshrrev_b32_e32 v167, 26, v176
	v_min3_u32 v164, v164, v165, v166
	v_bfi_b32 v168, 31, v164, v167
	s_nop 1
	v_mul_u32_u24_dpp v170, v168, v180 quad_perm:[1,2,3,3] row_mask:0xf bank_mask:0xf bound_ctrl:1
	v_mad_u32_u24 v171, v168, v181, v170
	ds_write_b8_d16_hi v184, v171 offset:416
	global_store_short_d16_hi v185, v176, s[48:49]
	s_waitcnt lgkmcnt(0)
	s_barrier
	ds_read_b64 v[122:123], v106 offset:416
	ds_read_b64 v[124:125], v106 offset:424
	ds_read_b64 v[126:127], v106 offset:432
	s_barrier
	ds_read_b64 v[128:129], v106 offset:512
	ds_read_b64 v[130:131], v106 offset:520
	ds_read_b64 v[132:133], v106 offset:528
	s_waitcnt lgkmcnt(3)
	v_mfma_f32_16x16x128_f8f6f4 v[134:137], v[122:127], v[2:7], 0 cbsz:2 blgp:2
	v_mfma_f32_16x16x128_f8f6f4 v[138:141], v[122:127], v[14:19], 0 cbsz:2 blgp:2
	v_mfma_f32_16x16x128_f8f6f4 v[142:145], v[122:127], v[26:31], v[188:191] cbsz:2 blgp:2
	v_mfma_f32_16x16x128_f8f6f4 v[204:207], v[122:127], v[38:43], 0 cbsz:2 blgp:2
	v_mfma_f32_16x16x128_f8f6f4 v[208:211], v[122:127], v[50:55], 0 cbsz:2 blgp:2
	v_mfma_f32_16x16x128_f8f6f4 v[212:215], v[122:127], v[62:67], v[188:191] cbsz:2 blgp:2
	s_waitcnt lgkmcnt(0)
	v_mfma_f32_16x16x128_f8f6f4 v[134:137], v[128:133], v[8:13], v[134:137] cbsz:2 blgp:2
	v_mfma_f32_16x16x128_f8f6f4 v[204:207], v[128:133], v[44:49], v[204:207] cbsz:2 blgp:2
	v_mfma_f32_16x16x128_f8f6f4 v[138:141], v[128:133], v[20:25], v[138:141] cbsz:2 blgp:2
	v_mfma_f32_16x16x128_f8f6f4 v[208:211], v[128:133], v[56:61], v[208:211] cbsz:2 blgp:2
	v_mfma_f32_16x16x128_f8f6f4 v[142:145], v[128:133], v[32:37], v[142:145] cbsz:2 blgp:2
	v_mfma_f32_16x16x128_f8f6f4 v[212:215], v[128:133], v[68:73], v[212:215] cbsz:2 blgp:2
	v_cndmask_b32_e64 v158, v134, v204, s[4:5]
	v_cndmask_b32_e64 v159, v138, v208, s[4:5]
	v_fma_mix_f32 v158, v158, v1, v146 op_sel:[0,0,1] op_sel_hi:[0,0,1]
	v_fma_mix_f32 v159, v159, v99, v150 op_sel:[0,0,1] op_sel_hi:[0,0,1]
	v_exp_f32_e32 v158, v158
	v_exp_f32_e32 v159, v159
	v_fma_f32 v158, v158, v186, v186
	v_add_f32_e32 v159, 1.0, v159
	v_rcp_f32_e32 v158, v158
	v_rcp_f32_e32 v159, v159
	v_cndmask_b32_e64 v160, v142, v212, s[4:5]
	v_fma_mix_f32 v161, v158, v160, v154 op_sel:[0,0,1] op_sel_hi:[0,0,1]
	v_exp_f32_e32 v161, v161
	s_add_u32 s48, s48, s40
	v_add_f32_e32 v161, 1.0, v161
	v_rcp_f32_e32 v161, v161
	s_addc_u32 s49, s49, s41
	v_fma_f32 v162, v161, -2.0, 1.0
	v_sub_f32_e32 v163, v176, v162
	v_fma_f32 v176, v159, v163, v162
	v_fma_f32 v164, |v176|, s16, v117
	v_fma_f32 v165, |v176|, s17, v118
	v_fma_f32 v166, |v176|, s18, v119
	v_lshrrev_b32_e32 v167, 26, v176
	v_min3_u32 v164, v164, v165, v166
	v_bfi_b32 v168, 31, v164, v167
	s_nop 1
	v_mul_u32_u24_dpp v170, v168, v180 quad_perm:[1,2,3,3] row_mask:0xf bank_mask:0xf bound_ctrl:1
	v_mad_u32_u24 v171, v168, v181, v170
	ds_write_b8_d16_hi v184, v171
	global_store_short_d16_hi v185, v176, s[48:49]
	s_waitcnt lgkmcnt(0)
	s_barrier
	ds_read_b64 v[122:123], v106 offset:0
	ds_read_b64 v[124:125], v106 offset:8
	ds_read_b64 v[126:127], v106 offset:16
	s_barrier
	ds_read_b64 v[128:129], v106 offset:96
	ds_read_b64 v[130:131], v106 offset:104
	ds_read_b64 v[132:133], v106 offset:112
	s_waitcnt lgkmcnt(3)
	v_mfma_f32_16x16x128_f8f6f4 v[134:137], v[122:127], v[2:7], 0 cbsz:2 blgp:2
	v_mfma_f32_16x16x128_f8f6f4 v[138:141], v[122:127], v[14:19], 0 cbsz:2 blgp:2
	v_mfma_f32_16x16x128_f8f6f4 v[142:145], v[122:127], v[26:31], v[188:191] cbsz:2 blgp:2
	v_mfma_f32_16x16x128_f8f6f4 v[204:207], v[122:127], v[38:43], 0 cbsz:2 blgp:2
	v_mfma_f32_16x16x128_f8f6f4 v[208:211], v[122:127], v[50:55], 0 cbsz:2 blgp:2
	v_mfma_f32_16x16x128_f8f6f4 v[212:215], v[122:127], v[62:67], v[188:191] cbsz:2 blgp:2
	s_waitcnt lgkmcnt(0)
	v_mfma_f32_16x16x128_f8f6f4 v[134:137], v[128:133], v[8:13], v[134:137] cbsz:2 blgp:2
	v_mfma_f32_16x16x128_f8f6f4 v[204:207], v[128:133], v[44:49], v[204:207] cbsz:2 blgp:2
	v_mfma_f32_16x16x128_f8f6f4 v[138:141], v[128:133], v[20:25], v[138:141] cbsz:2 blgp:2
	v_mfma_f32_16x16x128_f8f6f4 v[208:211], v[128:133], v[56:61], v[208:211] cbsz:2 blgp:2
	v_mfma_f32_16x16x128_f8f6f4 v[142:145], v[128:133], v[32:37], v[142:145] cbsz:2 blgp:2
	v_mfma_f32_16x16x128_f8f6f4 v[212:215], v[128:133], v[68:73], v[212:215] cbsz:2 blgp:2
	v_cndmask_b32_e64 v158, v134, v204, s[4:5]
	v_cndmask_b32_e64 v159, v138, v208, s[4:5]
	v_fma_mix_f32 v158, v158, v1, v147 op_sel_hi:[0,0,1]
	v_fma_mix_f32 v159, v159, v99, v151 op_sel_hi:[0,0,1]
	v_exp_f32_e32 v158, v158
	v_exp_f32_e32 v159, v159
	v_fma_f32 v158, v158, v186, v186
	v_add_f32_e32 v159, 1.0, v159
	v_rcp_f32_e32 v158, v158
	v_rcp_f32_e32 v159, v159
	v_cndmask_b32_e64 v160, v142, v212, s[4:5]
	v_fma_mix_f32 v161, v158, v160, v155 op_sel_hi:[0,0,1]
	v_exp_f32_e32 v161, v161
	s_add_u32 s48, s48, s40
	v_add_f32_e32 v161, 1.0, v161
	v_rcp_f32_e32 v161, v161
	s_addc_u32 s49, s49, s41
	v_fma_f32 v162, v161, -2.0, 1.0
	v_sub_f32_e32 v163, v176, v162
	v_fma_f32 v176, v159, v163, v162
	v_fma_f32 v164, |v176|, s16, v117
	v_fma_f32 v165, |v176|, s17, v118
	v_fma_f32 v166, |v176|, s18, v119
	v_lshrrev_b32_e32 v167, 26, v176
	v_min3_u32 v164, v164, v165, v166
	v_bfi_b32 v168, 31, v164, v167
	s_nop 1
	v_mul_u32_u24_dpp v170, v168, v180 quad_perm:[1,2,3,3] row_mask:0xf bank_mask:0xf bound_ctrl:1
	v_mad_u32_u24 v171, v168, v181, v170
	ds_write_b8_d16_hi v184, v171 offset:416
	global_store_short_d16_hi v185, v176, s[48:49]
	s_waitcnt lgkmcnt(0)
	s_barrier
	ds_read_b64 v[122:123], v106 offset:416
	ds_read_b64 v[124:125], v106 offset:424
	ds_read_b64 v[126:127], v106 offset:432
	s_barrier
	ds_read_b64 v[128:129], v106 offset:512
	ds_read_b64 v[130:131], v106 offset:520
	ds_read_b64 v[132:133], v106 offset:528
	s_waitcnt lgkmcnt(3)
	v_mfma_f32_16x16x128_f8f6f4 v[134:137], v[122:127], v[2:7], 0 cbsz:2 blgp:2
	v_mfma_f32_16x16x128_f8f6f4 v[138:141], v[122:127], v[14:19], 0 cbsz:2 blgp:2
	v_mfma_f32_16x16x128_f8f6f4 v[142:145], v[122:127], v[26:31], v[188:191] cbsz:2 blgp:2
	v_mfma_f32_16x16x128_f8f6f4 v[204:207], v[122:127], v[38:43], 0 cbsz:2 blgp:2
	v_mfma_f32_16x16x128_f8f6f4 v[208:211], v[122:127], v[50:55], 0 cbsz:2 blgp:2
	v_mfma_f32_16x16x128_f8f6f4 v[212:215], v[122:127], v[62:67], v[188:191] cbsz:2 blgp:2
	s_waitcnt lgkmcnt(0)
	v_mfma_f32_16x16x128_f8f6f4 v[134:137], v[128:133], v[8:13], v[134:137] cbsz:2 blgp:2
	v_mfma_f32_16x16x128_f8f6f4 v[204:207], v[128:133], v[44:49], v[204:207] cbsz:2 blgp:2
	v_mfma_f32_16x16x128_f8f6f4 v[138:141], v[128:133], v[20:25], v[138:141] cbsz:2 blgp:2
	v_mfma_f32_16x16x128_f8f6f4 v[208:211], v[128:133], v[56:61], v[208:211] cbsz:2 blgp:2
	v_mfma_f32_16x16x128_f8f6f4 v[142:145], v[128:133], v[32:37], v[142:145] cbsz:2 blgp:2
	v_mfma_f32_16x16x128_f8f6f4 v[212:215], v[128:133], v[68:73], v[212:215] cbsz:2 blgp:2
	v_cndmask_b32_e64 v158, v134, v204, s[4:5]
	v_cndmask_b32_e64 v159, v138, v208, s[4:5]
	v_fma_mix_f32 v158, v158, v1, v147 op_sel:[0,0,1] op_sel_hi:[0,0,1]
	v_fma_mix_f32 v159, v159, v99, v151 op_sel:[0,0,1] op_sel_hi:[0,0,1]
	v_exp_f32_e32 v158, v158
	v_exp_f32_e32 v159, v159
	v_fma_f32 v158, v158, v186, v186
	v_add_f32_e32 v159, 1.0, v159
	v_rcp_f32_e32 v158, v158
	v_rcp_f32_e32 v159, v159
	v_cndmask_b32_e64 v160, v142, v212, s[4:5]
	v_fma_mix_f32 v161, v158, v160, v155 op_sel:[0,0,1] op_sel_hi:[0,0,1]
	v_exp_f32_e32 v161, v161
	s_add_u32 s48, s48, s40
	v_add_f32_e32 v161, 1.0, v161
	v_rcp_f32_e32 v161, v161
	s_addc_u32 s49, s49, s41
	v_fma_f32 v162, v161, -2.0, 1.0
	v_sub_f32_e32 v163, v176, v162
	v_fma_f32 v176, v159, v163, v162
	v_fma_f32 v164, |v176|, s16, v117
	v_fma_f32 v165, |v176|, s17, v118
	v_fma_f32 v166, |v176|, s18, v119
	v_lshrrev_b32_e32 v167, 26, v176
	v_min3_u32 v164, v164, v165, v166
	v_bfi_b32 v168, 31, v164, v167
	s_nop 1
	v_mul_u32_u24_dpp v170, v168, v180 quad_perm:[1,2,3,3] row_mask:0xf bank_mask:0xf bound_ctrl:1
	v_mad_u32_u24 v171, v168, v181, v170
	ds_write_b8_d16_hi v184, v171
	global_store_short_d16_hi v185, v176, s[48:49]
	s_waitcnt lgkmcnt(0)
	s_barrier
	ds_read_b64 v[122:123], v106 offset:0
	ds_read_b64 v[124:125], v106 offset:8
	ds_read_b64 v[126:127], v106 offset:16
	s_barrier
	ds_read_b64 v[128:129], v106 offset:96
	ds_read_b64 v[130:131], v106 offset:104
	ds_read_b64 v[132:133], v106 offset:112
	s_waitcnt lgkmcnt(3)
	v_mfma_f32_16x16x128_f8f6f4 v[134:137], v[122:127], v[2:7], 0 cbsz:2 blgp:2
	v_mfma_f32_16x16x128_f8f6f4 v[138:141], v[122:127], v[14:19], 0 cbsz:2 blgp:2
	v_mfma_f32_16x16x128_f8f6f4 v[142:145], v[122:127], v[26:31], v[188:191] cbsz:2 blgp:2
	v_mfma_f32_16x16x128_f8f6f4 v[204:207], v[122:127], v[38:43], 0 cbsz:2 blgp:2
	v_mfma_f32_16x16x128_f8f6f4 v[208:211], v[122:127], v[50:55], 0 cbsz:2 blgp:2
	v_mfma_f32_16x16x128_f8f6f4 v[212:215], v[122:127], v[62:67], v[188:191] cbsz:2 blgp:2
	s_waitcnt lgkmcnt(0)
	v_mfma_f32_16x16x128_f8f6f4 v[134:137], v[128:133], v[8:13], v[134:137] cbsz:2 blgp:2
	v_mfma_f32_16x16x128_f8f6f4 v[204:207], v[128:133], v[44:49], v[204:207] cbsz:2 blgp:2
	v_mfma_f32_16x16x128_f8f6f4 v[138:141], v[128:133], v[20:25], v[138:141] cbsz:2 blgp:2
	v_mfma_f32_16x16x128_f8f6f4 v[208:211], v[128:133], v[56:61], v[208:211] cbsz:2 blgp:2
	v_mfma_f32_16x16x128_f8f6f4 v[142:145], v[128:133], v[32:37], v[142:145] cbsz:2 blgp:2
	v_mfma_f32_16x16x128_f8f6f4 v[212:215], v[128:133], v[68:73], v[212:215] cbsz:2 blgp:2
	v_cndmask_b32_e64 v158, v134, v204, s[4:5]
	v_cndmask_b32_e64 v159, v138, v208, s[4:5]
	v_fma_mix_f32 v158, v158, v1, v148 op_sel_hi:[0,0,1]
	v_fma_mix_f32 v159, v159, v99, v152 op_sel_hi:[0,0,1]
	v_exp_f32_e32 v158, v158
	v_exp_f32_e32 v159, v159
	v_fma_f32 v158, v158, v186, v186
	v_add_f32_e32 v159, 1.0, v159
	v_rcp_f32_e32 v158, v158
	v_rcp_f32_e32 v159, v159
	v_cndmask_b32_e64 v160, v142, v212, s[4:5]
	v_fma_mix_f32 v161, v158, v160, v156 op_sel_hi:[0,0,1]
	v_exp_f32_e32 v161, v161
	s_add_u32 s48, s48, s40
	v_add_f32_e32 v161, 1.0, v161
	v_rcp_f32_e32 v161, v161
	s_addc_u32 s49, s49, s41
	v_fma_f32 v162, v161, -2.0, 1.0
	v_sub_f32_e32 v163, v176, v162
	v_fma_f32 v176, v159, v163, v162
	v_fma_f32 v164, |v176|, s16, v117
	v_fma_f32 v165, |v176|, s17, v118
	v_fma_f32 v166, |v176|, s18, v119
	v_lshrrev_b32_e32 v167, 26, v176
	v_min3_u32 v164, v164, v165, v166
	v_bfi_b32 v168, 31, v164, v167
	s_nop 1
	v_mul_u32_u24_dpp v170, v168, v180 quad_perm:[1,2,3,3] row_mask:0xf bank_mask:0xf bound_ctrl:1
	v_mad_u32_u24 v171, v168, v181, v170
	ds_write_b8_d16_hi v184, v171 offset:416
	global_store_short_d16_hi v185, v176, s[48:49]
	s_waitcnt lgkmcnt(0)
	s_barrier
	ds_read_b64 v[122:123], v106 offset:416
	ds_read_b64 v[124:125], v106 offset:424
	ds_read_b64 v[126:127], v106 offset:432
	s_barrier
	ds_read_b64 v[128:129], v106 offset:512
	ds_read_b64 v[130:131], v106 offset:520
	ds_read_b64 v[132:133], v106 offset:528
	s_waitcnt lgkmcnt(3)
	v_mfma_f32_16x16x128_f8f6f4 v[134:137], v[122:127], v[2:7], 0 cbsz:2 blgp:2
	v_mfma_f32_16x16x128_f8f6f4 v[138:141], v[122:127], v[14:19], 0 cbsz:2 blgp:2
	v_mfma_f32_16x16x128_f8f6f4 v[142:145], v[122:127], v[26:31], v[188:191] cbsz:2 blgp:2
	v_mfma_f32_16x16x128_f8f6f4 v[204:207], v[122:127], v[38:43], 0 cbsz:2 blgp:2
	v_mfma_f32_16x16x128_f8f6f4 v[208:211], v[122:127], v[50:55], 0 cbsz:2 blgp:2
	v_mfma_f32_16x16x128_f8f6f4 v[212:215], v[122:127], v[62:67], v[188:191] cbsz:2 blgp:2
	s_waitcnt lgkmcnt(0)
	v_mfma_f32_16x16x128_f8f6f4 v[134:137], v[128:133], v[8:13], v[134:137] cbsz:2 blgp:2
	v_mfma_f32_16x16x128_f8f6f4 v[204:207], v[128:133], v[44:49], v[204:207] cbsz:2 blgp:2
	v_mfma_f32_16x16x128_f8f6f4 v[138:141], v[128:133], v[20:25], v[138:141] cbsz:2 blgp:2
	v_mfma_f32_16x16x128_f8f6f4 v[208:211], v[128:133], v[56:61], v[208:211] cbsz:2 blgp:2
	v_mfma_f32_16x16x128_f8f6f4 v[142:145], v[128:133], v[32:37], v[142:145] cbsz:2 blgp:2
	v_mfma_f32_16x16x128_f8f6f4 v[212:215], v[128:133], v[68:73], v[212:215] cbsz:2 blgp:2
	v_cndmask_b32_e64 v158, v134, v204, s[4:5]
	v_cndmask_b32_e64 v159, v138, v208, s[4:5]
	v_fma_mix_f32 v158, v158, v1, v148 op_sel:[0,0,1] op_sel_hi:[0,0,1]
	v_fma_mix_f32 v159, v159, v99, v152 op_sel:[0,0,1] op_sel_hi:[0,0,1]
	v_exp_f32_e32 v158, v158
	v_exp_f32_e32 v159, v159
	v_fma_f32 v158, v158, v186, v186
	v_add_f32_e32 v159, 1.0, v159
	v_rcp_f32_e32 v158, v158
	v_rcp_f32_e32 v159, v159
	v_cndmask_b32_e64 v160, v142, v212, s[4:5]
	v_fma_mix_f32 v161, v158, v160, v156 op_sel:[0,0,1] op_sel_hi:[0,0,1]
	v_exp_f32_e32 v161, v161
	s_add_u32 s48, s48, s40
	v_add_f32_e32 v161, 1.0, v161
	v_rcp_f32_e32 v161, v161
	s_addc_u32 s49, s49, s41
	v_fma_f32 v162, v161, -2.0, 1.0
	v_sub_f32_e32 v163, v176, v162
	v_fma_f32 v176, v159, v163, v162
	v_fma_f32 v164, |v176|, s16, v117
	v_fma_f32 v165, |v176|, s17, v118
	v_fma_f32 v166, |v176|, s18, v119
	v_lshrrev_b32_e32 v167, 26, v176
	v_min3_u32 v164, v164, v165, v166
	v_bfi_b32 v168, 31, v164, v167
	s_nop 1
	v_mul_u32_u24_dpp v170, v168, v180 quad_perm:[1,2,3,3] row_mask:0xf bank_mask:0xf bound_ctrl:1
	v_mad_u32_u24 v171, v168, v181, v170
	ds_write_b8_d16_hi v184, v171
	global_store_short_d16_hi v185, v176, s[48:49]
	s_waitcnt lgkmcnt(0)
	s_barrier
	ds_read_b64 v[122:123], v106 offset:0
	ds_read_b64 v[124:125], v106 offset:8
	ds_read_b64 v[126:127], v106 offset:16
	s_barrier
	ds_read_b64 v[128:129], v106 offset:96
	ds_read_b64 v[130:131], v106 offset:104
	ds_read_b64 v[132:133], v106 offset:112
	s_waitcnt lgkmcnt(3)
	v_mfma_f32_16x16x128_f8f6f4 v[134:137], v[122:127], v[2:7], 0 cbsz:2 blgp:2
	v_mfma_f32_16x16x128_f8f6f4 v[138:141], v[122:127], v[14:19], 0 cbsz:2 blgp:2
	v_mfma_f32_16x16x128_f8f6f4 v[142:145], v[122:127], v[26:31], v[188:191] cbsz:2 blgp:2
	v_mfma_f32_16x16x128_f8f6f4 v[204:207], v[122:127], v[38:43], 0 cbsz:2 blgp:2
	v_mfma_f32_16x16x128_f8f6f4 v[208:211], v[122:127], v[50:55], 0 cbsz:2 blgp:2
	v_mfma_f32_16x16x128_f8f6f4 v[212:215], v[122:127], v[62:67], v[188:191] cbsz:2 blgp:2
	s_waitcnt lgkmcnt(0)
	v_mfma_f32_16x16x128_f8f6f4 v[134:137], v[128:133], v[8:13], v[134:137] cbsz:2 blgp:2
	v_mfma_f32_16x16x128_f8f6f4 v[204:207], v[128:133], v[44:49], v[204:207] cbsz:2 blgp:2
	v_mfma_f32_16x16x128_f8f6f4 v[138:141], v[128:133], v[20:25], v[138:141] cbsz:2 blgp:2
	v_mfma_f32_16x16x128_f8f6f4 v[208:211], v[128:133], v[56:61], v[208:211] cbsz:2 blgp:2
	v_mfma_f32_16x16x128_f8f6f4 v[142:145], v[128:133], v[32:37], v[142:145] cbsz:2 blgp:2
	v_mfma_f32_16x16x128_f8f6f4 v[212:215], v[128:133], v[68:73], v[212:215] cbsz:2 blgp:2
	v_cndmask_b32_e64 v158, v134, v204, s[4:5]
	v_cndmask_b32_e64 v159, v138, v208, s[4:5]
	v_fma_mix_f32 v158, v158, v1, v149 op_sel_hi:[0,0,1]
	v_fma_mix_f32 v159, v159, v99, v153 op_sel_hi:[0,0,1]
	v_exp_f32_e32 v158, v158
	v_exp_f32_e32 v159, v159
	v_fma_f32 v158, v158, v186, v186
	v_add_f32_e32 v159, 1.0, v159
	v_rcp_f32_e32 v158, v158
	v_rcp_f32_e32 v159, v159
	v_cndmask_b32_e64 v160, v142, v212, s[4:5]
	v_fma_mix_f32 v161, v158, v160, v157 op_sel_hi:[0,0,1]
	v_exp_f32_e32 v161, v161
	s_add_u32 s48, s48, s40
	v_add_f32_e32 v161, 1.0, v161
	v_rcp_f32_e32 v161, v161
	s_addc_u32 s49, s49, s41
	v_fma_f32 v162, v161, -2.0, 1.0
	v_sub_f32_e32 v163, v176, v162
	v_fma_f32 v176, v159, v163, v162
	v_fma_f32 v164, |v176|, s16, v117
	v_fma_f32 v165, |v176|, s17, v118
	v_fma_f32 v166, |v176|, s18, v119
	v_lshrrev_b32_e32 v167, 26, v176
	v_min3_u32 v164, v164, v165, v166
	v_bfi_b32 v168, 31, v164, v167
	s_nop 1
	v_mul_u32_u24_dpp v170, v168, v180 quad_perm:[1,2,3,3] row_mask:0xf bank_mask:0xf bound_ctrl:1
	v_mad_u32_u24 v171, v168, v181, v170
	ds_write_b8_d16_hi v184, v171 offset:416
	global_store_short_d16_hi v185, v176, s[48:49]
	s_waitcnt lgkmcnt(0)
	s_barrier
	ds_read_b64 v[122:123], v106 offset:416
	ds_read_b64 v[124:125], v106 offset:424
	ds_read_b64 v[126:127], v106 offset:432
	s_barrier
	ds_read_b64 v[128:129], v106 offset:512
	ds_read_b64 v[130:131], v106 offset:520
	ds_read_b64 v[132:133], v106 offset:528
	s_add_i32 s44, s44, 16
	s_waitcnt lgkmcnt(3)
	v_mfma_f32_16x16x128_f8f6f4 v[134:137], v[122:127], v[2:7], 0 cbsz:2 blgp:2
	v_mfma_f32_16x16x128_f8f6f4 v[138:141], v[122:127], v[14:19], 0 cbsz:2 blgp:2
	v_mfma_f32_16x16x128_f8f6f4 v[142:145], v[122:127], v[26:31], v[188:191] cbsz:2 blgp:2
	v_mfma_f32_16x16x128_f8f6f4 v[204:207], v[122:127], v[38:43], 0 cbsz:2 blgp:2
	v_mfma_f32_16x16x128_f8f6f4 v[208:211], v[122:127], v[50:55], 0 cbsz:2 blgp:2
	v_mfma_f32_16x16x128_f8f6f4 v[212:215], v[122:127], v[62:67], v[188:191] cbsz:2 blgp:2
	s_waitcnt lgkmcnt(0)
	v_mfma_f32_16x16x128_f8f6f4 v[134:137], v[128:133], v[8:13], v[134:137] cbsz:2 blgp:2
	v_mfma_f32_16x16x128_f8f6f4 v[204:207], v[128:133], v[44:49], v[204:207] cbsz:2 blgp:2
	v_mfma_f32_16x16x128_f8f6f4 v[138:141], v[128:133], v[20:25], v[138:141] cbsz:2 blgp:2
	v_mfma_f32_16x16x128_f8f6f4 v[208:211], v[128:133], v[56:61], v[208:211] cbsz:2 blgp:2
	v_mfma_f32_16x16x128_f8f6f4 v[142:145], v[128:133], v[32:37], v[142:145] cbsz:2 blgp:2
	v_mfma_f32_16x16x128_f8f6f4 v[212:215], v[128:133], v[68:73], v[212:215] cbsz:2 blgp:2
	v_cndmask_b32_e64 v158, v134, v204, s[4:5]
	v_cndmask_b32_e64 v159, v138, v208, s[4:5]
	v_fma_mix_f32 v158, v158, v1, v149 op_sel:[0,0,1] op_sel_hi:[0,0,1]
	v_fma_mix_f32 v159, v159, v99, v153 op_sel:[0,0,1] op_sel_hi:[0,0,1]
	v_exp_f32_e32 v158, v158
	v_exp_f32_e32 v159, v159
	v_fma_f32 v158, v158, v186, v186
	v_add_f32_e32 v159, 1.0, v159
	v_rcp_f32_e32 v158, v158
	v_rcp_f32_e32 v159, v159
	v_cndmask_b32_e64 v160, v142, v212, s[4:5]
	v_fma_mix_f32 v161, v158, v160, v157 op_sel:[0,0,1] op_sel_hi:[0,0,1]
	v_exp_f32_e32 v161, v161
	s_add_u32 s48, s48, s40
	v_add_f32_e32 v161, 1.0, v161
	v_rcp_f32_e32 v161, v161
	s_addc_u32 s49, s49, s41
	v_fma_f32 v162, v161, -2.0, 1.0
	v_sub_f32_e32 v163, v176, v162
	v_fma_f32 v176, v159, v163, v162
	v_fma_f32 v164, |v176|, s16, v117
	v_fma_f32 v165, |v176|, s17, v118
	v_fma_f32 v166, |v176|, s18, v119
	v_lshrrev_b32_e32 v167, 26, v176
	v_min3_u32 v164, v164, v165, v166
	v_bfi_b32 v168, 31, v164, v167
	s_nop 1
	v_mul_u32_u24_dpp v170, v168, v180 quad_perm:[1,2,3,3] row_mask:0xf bank_mask:0xf bound_ctrl:1
	v_mad_u32_u24 v171, v168, v181, v170
	ds_write_b8_d16_hi v184, v171
	global_store_short_d16_hi v185, v176, s[48:49]
	s_waitcnt lgkmcnt(0)
	s_barrier
	ds_read_b64 v[122:123], v106 offset:0
	ds_read_b64 v[124:125], v106 offset:8
	ds_read_b64 v[126:127], v106 offset:16
	s_cmp_lt_i32 s44, s45
	s_barrier
	s_cbranch_scc1 .Lscan_loop_a_st
	s_branch .Lscan_exit_st
.Lscan_entry_b_st:
.Lscan_loop_b_st:
	ds_read_b64 v[122:123], v106 offset:0
	ds_read_b64 v[124:125], v106 offset:8
	ds_read_b64 v[126:127], v106 offset:16
	ds_read_b64 v[128:129], v106 offset:96
	ds_read_b64 v[130:131], v106 offset:104
	ds_read_b64 v[132:133], v106 offset:112
	s_waitcnt vmcnt(8)
	global_load_dwordx4 v[146:149], v[196:197], off
	global_load_dwordx4 v[150:153], v[196:197], off offset:512
	global_load_dwordx4 v[154:157], v[196:197], off offset:1024
	v_lshl_add_u64 v[196:197], v[196:197], 0, s[42:43]
	s_waitcnt lgkmcnt(3)
	v_mfma_f32_16x16x128_f8f6f4 v[134:137], v[122:127], v[2:7], 0 cbsz:2 blgp:2
	v_mfma_f32_16x16x128_f8f6f4 v[138:141], v[122:127], v[14:19], 0 cbsz:2 blgp:2
	v_mfma_f32_16x16x128_f8f6f4 v[142:145], v[122:127], v[26:31], v[188:191] cbsz:2 blgp:2
	v_mfma_f32_16x16x128_f8f6f4 v[204:207], v[122:127], v[38:43], 0 cbsz:2 blgp:2
	v_mfma_f32_16x16x128_f8f6f4 v[208:211], v[122:127], v[50:55], 0 cbsz:2 blgp:2
	v_mfma_f32_16x16x128_f8f6f4 v[212:215], v[122:127], v[62:67], v[188:191] cbsz:2 blgp:2
	s_waitcnt lgkmcnt(0)
	v_mfma_f32_16x16x128_f8f6f4 v[134:137], v[128:133], v[8:13], v[134:137] cbsz:2 blgp:2
	v_mfma_f32_16x16x128_f8f6f4 v[204:207], v[128:133], v[44:49], v[204:207] cbsz:2 blgp:2
	v_mfma_f32_16x16x128_f8f6f4 v[138:141], v[128:133], v[20:25], v[138:141] cbsz:2 blgp:2
	v_mfma_f32_16x16x128_f8f6f4 v[208:211], v[128:133], v[56:61], v[208:211] cbsz:2 blgp:2
	v_mfma_f32_16x16x128_f8f6f4 v[142:145], v[128:133], v[32:37], v[142:145] cbsz:2 blgp:2
	v_mfma_f32_16x16x128_f8f6f4 v[212:215], v[128:133], v[68:73], v[212:215] cbsz:2 blgp:2
	v_cndmask_b32_e64 v158, v134, v204, s[4:5]
	v_cndmask_b32_e64 v159, v138, v208, s[4:5]
	v_fma_mix_f32 v158, v158, v1, v82 op_sel_hi:[0,0,1]
	v_fma_mix_f32 v159, v159, v99, v74 op_sel_hi:[0,0,1]
	v_exp_f32_e32 v158, v158
	v_exp_f32_e32 v159, v159
	v_fma_f32 v158, v158, v186, v186
	v_add_f32_e32 v159, 1.0, v159
	v_rcp_f32_e32 v158, v158
	v_rcp_f32_e32 v159, v159
	v_cndmask_b32_e64 v160, v142, v212, s[4:5]
	v_fma_mix_f32 v161, v158, v160, v78 op_sel_hi:[0,0,1]
	v_exp_f32_e32 v161, v161
	s_add_u32 s48, s48, s40
	v_add_f32_e32 v161, 1.0, v161
	v_rcp_f32_e32 v161, v161
	s_addc_u32 s49, s49, s41
	v_fma_f32 v162, v161, -2.0, 1.0
	v_sub_f32_e32 v163, v176, v162
	v_fma_f32 v176, v159, v163, v162
	v_fma_f32 v164, |v176|, s16, v117
	v_fma_f32 v165, |v176|, s17, v118
	v_fma_f32 v166, |v176|, s18, v119
	v_lshrrev_b32_e32 v167, 26, v176
	v_min3_u32 v164, v164, v165, v166
	v_bfi_b32 v168, 31, v164, v167
	s_nop 1
	v_mul_u32_u24_dpp v170, v168, v180 quad_perm:[1,2,3,3] row_mask:0xf bank_mask:0xf bound_ctrl:1
	v_mad_u32_u24 v171, v168, v181, v170
	ds_write_b8_d16_hi v184, v171 offset:416
	s_barrier
	global_store_short_d16_hi v185, v176, s[48:49]
	s_waitcnt lgkmcnt(0)
	s_barrier
	ds_read_b64 v[122:123], v106 offset:416
	ds_read_b64 v[124:125], v106 offset:424
	ds_read_b64 v[126:127], v106 offset:432
	ds_read_b64 v[128:129], v106 offset:512
	ds_read_b64 v[130:131], v106 offset:520
	ds_read_b64 v[132:133], v106 offset:528
	s_waitcnt lgkmcnt(3)
	v_mfma_f32_16x16x128_f8f6f4 v[134:137], v[122:127], v[2:7], 0 cbsz:2 blgp:2
	v_mfma_f32_16x16x128_f8f6f4 v[138:141], v[122:127], v[14:19], 0 cbsz:2 blgp:2
	v_mfma_f32_16x16x128_f8f6f4 v[142:145], v[122:127], v[26:31], v[188:191] cbsz:2 blgp:2
	v_mfma_f32_16x16x128_f8f6f4 v[204:207], v[122:127], v[38:43], 0 cbsz:2 blgp:2
	v_mfma_f32_16x16x128_f8f6f4 v[208:211], v[122:127], v[50:55], 0 cbsz:2 blgp:2
	v_mfma_f32_16x16x128_f8f6f4 v[212:215], v[122:127], v[62:67], v[188:191] cbsz:2 blgp:2
	s_waitcnt lgkmcnt(0)
	v_mfma_f32_16x16x128_f8f6f4 v[134:137], v[128:133], v[8:13], v[134:137] cbsz:2 blgp:2
	v_mfma_f32_16x16x128_f8f6f4 v[204:207], v[128:133], v[44:49], v[204:207] cbsz:2 blgp:2
	v_mfma_f32_16x16x128_f8f6f4 v[138:141], v[128:133], v[20:25], v[138:141] cbsz:2 blgp:2
	v_mfma_f32_16x16x128_f8f6f4 v[208:211], v[128:133], v[56:61], v[208:211] cbsz:2 blgp:2
	v_mfma_f32_16x16x128_f8f6f4 v[142:145], v[128:133], v[32:37], v[142:145] cbsz:2 blgp:2
	v_mfma_f32_16x16x128_f8f6f4 v[212:215], v[128:133], v[68:73], v[212:215] cbsz:2 blgp:2
	v_cndmask_b32_e64 v158, v134, v204, s[4:5]
	v_cndmask_b32_e64 v159, v138, v208, s[4:5]
	v_fma_mix_f32 v158, v158, v1, v82 op_sel:[0,0,1] op_sel_hi:[0,0,1]
	v_fma_mix_f32 v159, v159, v99, v74 op_sel:[0,0,1] op_sel_hi:[0,0,1]
	v_exp_f32_e32 v158, v158
	v_exp_f32_e32 v159, v159
	v_fma_f32 v158, v158, v186, v186
	v_add_f32_e32 v159, 1.0, v159
	v_rcp_f32_e32 v158, v158
	v_rcp_f32_e32 v159, v159
	v_cndmask_b32_e64 v160, v142, v212, s[4:5]
	v_fma_mix_f32 v161, v158, v160, v78 op_sel:[0,0,1] op_sel_hi:[0,0,1]
	v_exp_f32_e32 v161, v161
	s_add_u32 s48, s48, s40
	v_add_f32_e32 v161, 1.0, v161
	v_rcp_f32_e32 v161, v161
	s_addc_u32 s49, s49, s41
	v_fma_f32 v162, v161, -2.0, 1.0
	v_sub_f32_e32 v163, v176, v162
	v_fma_f32 v176, v159, v163, v162
	v_fma_f32 v164, |v176|, s16, v117
	v_fma_f32 v165, |v176|, s17, v118
	v_fma_f32 v166, |v176|, s18, v119
	v_lshrrev_b32_e32 v167, 26, v176
	v_min3_u32 v164, v164, v165, v166
	v_bfi_b32 v168, 31, v164, v167
	s_nop 1
	v_mul_u32_u24_dpp v170, v168, v180 quad_perm:[1,2,3,3] row_mask:0xf bank_mask:0xf bound_ctrl:1
	v_mad_u32_u24 v171, v168, v181, v170
	ds_write_b8_d16_hi v184, v171
	s_barrier
	global_store_short_d16_hi v185, v176, s[48:49]
	s_waitcnt lgkmcnt(0)
	s_barrier
	ds_read_b64 v[122:123], v106 offset:0
	ds_read_b64 v[124:125], v106 offset:8
	ds_read_b64 v[126:127], v106 offset:16
	ds_read_b64 v[128:129], v106 offset:96
	ds_read_b64 v[130:131], v106 offset:104
	ds_read_b64 v[132:133], v106 offset:112
	s_waitcnt lgkmcnt(3)
	v_mfma_f32_16x16x128_f8f6f4 v[134:137], v[122:127], v[2:7], 0 cbsz:2 blgp:2
	v_mfma_f32_16x16x128_f8f6f4 v[138:141], v[122:127], v[14:19], 0 cbsz:2 blgp:2
	v_mfma_f32_16x16x128_f8f6f4 v[142:145], v[122:127], v[26:31], v[188:191] cbsz:2 blgp:2
	v_mfma_f32_16x16x128_f8f6f4 v[204:207], v[122:127], v[38:43], 0 cbsz:2 blgp:2
	v_mfma_f32_16x16x128_f8f6f4 v[208:211], v[122:127], v[50:55], 0 cbsz:2 blgp:2
	v_mfma_f32_16x16x128_f8f6f4 v[212:215], v[122:127], v[62:67], v[188:191] cbsz:2 blgp:2
	s_waitcnt lgkmcnt(0)
	v_mfma_f32_16x16x128_f8f6f4 v[134:137], v[128:133], v[8:13], v[134:137] cbsz:2 blgp:2
	v_mfma_f32_16x16x128_f8f6f4 v[204:207], v[128:133], v[44:49], v[204:207] cbsz:2 blgp:2
	v_mfma_f32_16x16x128_f8f6f4 v[138:141], v[128:133], v[20:25], v[138:141] cbsz:2 blgp:2
	v_mfma_f32_16x16x128_f8f6f4 v[208:211], v[128:133], v[56:61], v[208:211] cbsz:2 blgp:2
	v_mfma_f32_16x16x128_f8f6f4 v[142:145], v[128:133], v[32:37], v[142:145] cbsz:2 blgp:2
	v_mfma_f32_16x16x128_f8f6f4 v[212:215], v[128:133], v[68:73], v[212:215] cbsz:2 blgp:2
	v_cndmask_b32_e64 v158, v134, v204, s[4:5]
	v_cndmask_b32_e64 v159, v138, v208, s[4:5]
	v_fma_mix_f32 v158, v158, v1, v83 op_sel_hi:[0,0,1]
	v_fma_mix_f32 v159, v159, v99, v75 op_sel_hi:[0,0,1]
	v_exp_f32_e32 v158, v158
	v_exp_f32_e32 v159, v159
	v_fma_f32 v158, v158, v186, v186
	v_add_f32_e32 v159, 1.0, v159
	v_rcp_f32_e32 v158, v158
	v_rcp_f32_e32 v159, v159
	v_cndmask_b32_e64 v160, v142, v212, s[4:5]
	v_fma_mix_f32 v161, v158, v160, v79 op_sel_hi:[0,0,1]
	v_exp_f32_e32 v161, v161
	s_add_u32 s48, s48, s40
	v_add_f32_e32 v161, 1.0, v161
	v_rcp_f32_e32 v161, v161
	s_addc_u32 s49, s49, s41
	v_fma_f32 v162, v161, -2.0, 1.0
	v_sub_f32_e32 v163, v176, v162
	v_fma_f32 v176, v159, v163, v162
	v_fma_f32 v164, |v176|, s16, v117
	v_fma_f32 v165, |v176|, s17, v118
	v_fma_f32 v166, |v176|, s18, v119
	v_lshrrev_b32_e32 v167, 26, v176
	v_min3_u32 v164, v164, v165, v166
	v_bfi_b32 v168, 31, v164, v167
	s_nop 1
	v_mul_u32_u24_dpp v170, v168, v180 quad_perm:[1,2,3,3] row_mask:0xf bank_mask:0xf bound_ctrl:1
	v_mad_u32_u24 v171, v168, v181, v170
	ds_write_b8_d16_hi v184, v171 offset:416
	s_barrier
	global_store_short_d16_hi v185, v176, s[48:49]
	s_waitcnt lgkmcnt(0)
	s_barrier
	ds_read_b64 v[122:123], v106 offset:416
	ds_read_b64 v[124:125], v106 offset:424
	ds_read_b64 v[126:127], v106 offset:432
	ds_read_b64 v[128:129], v106 offset:512
	ds_read_b64 v[130:131], v106 offset:520
	ds_read_b64 v[132:133], v106 offset:528
	s_waitcnt lgkmcnt(3)
	v_mfma_f32_16x16x128_f8f6f4 v[134:137], v[122:127], v[2:7], 0 cbsz:2 blgp:2
	v_mfma_f32_16x16x128_f8f6f4 v[138:141], v[122:127], v[14:19], 0 cbsz:2 blgp:2
	v_mfma_f32_16x16x128_f8f6f4 v[142:145], v[122:127], v[26:31], v[188:191] cbsz:2 blgp:2
	v_mfma_f32_16x16x128_f8f6f4 v[204:207], v[122:127], v[38:43], 0 cbsz:2 blgp:2
	v_mfma_f32_16x16x128_f8f6f4 v[208:211], v[122:127], v[50:55], 0 cbsz:2 blgp:2
	v_mfma_f32_16x16x128_f8f6f4 v[212:215], v[122:127], v[62:67], v[188:191] cbsz:2 blgp:2
	s_waitcnt lgkmcnt(0)
	v_mfma_f32_16x16x128_f8f6f4 v[134:137], v[128:133], v[8:13], v[134:137] cbsz:2 blgp:2
	v_mfma_f32_16x16x128_f8f6f4 v[204:207], v[128:133], v[44:49], v[204:207] cbsz:2 blgp:2
	v_mfma_f32_16x16x128_f8f6f4 v[138:141], v[128:133], v[20:25], v[138:141] cbsz:2 blgp:2
	v_mfma_f32_16x16x128_f8f6f4 v[208:211], v[128:133], v[56:61], v[208:211] cbsz:2 blgp:2
	v_mfma_f32_16x16x128_f8f6f4 v[142:145], v[128:133], v[32:37], v[142:145] cbsz:2 blgp:2
	v_mfma_f32_16x16x128_f8f6f4 v[212:215], v[128:133], v[68:73], v[212:215] cbsz:2 blgp:2
	v_cndmask_b32_e64 v158, v134, v204, s[4:5]
	v_cndmask_b32_e64 v159, v138, v208, s[4:5]
	v_fma_mix_f32 v158, v158, v1, v83 op_sel:[0,0,1] op_sel_hi:[0,0,1]
	v_fma_mix_f32 v159, v159, v99, v75 op_sel:[0,0,1] op_sel_hi:[0,0,1]
	v_exp_f32_e32 v158, v158
	v_exp_f32_e32 v159, v159
	v_fma_f32 v158, v158, v186, v186
	v_add_f32_e32 v159, 1.0, v159
	v_rcp_f32_e32 v158, v158
	v_rcp_f32_e32 v159, v159
	v_cndmask_b32_e64 v160, v142, v212, s[4:5]
	v_fma_mix_f32 v161, v158, v160, v79 op_sel:[0,0,1] op_sel_hi:[0,0,1]
	v_exp_f32_e32 v161, v161
	s_add_u32 s48, s48, s40
	v_add_f32_e32 v161, 1.0, v161
	v_rcp_f32_e32 v161, v161
	s_addc_u32 s49, s49, s41
	v_fma_f32 v162, v161, -2.0, 1.0
	v_sub_f32_e32 v163, v176, v162
	v_fma_f32 v176, v159, v163, v162
	v_fma_f32 v164, |v176|, s16, v117
	v_fma_f32 v165, |v176|, s17, v118
	v_fma_f32 v166, |v176|, s18, v119
	v_lshrrev_b32_e32 v167, 26, v176
	v_min3_u32 v164, v164, v165, v166
	v_bfi_b32 v168, 31, v164, v167
	s_nop 1
	v_mul_u32_u24_dpp v170, v168, v180 quad_perm:[1,2,3,3] row_mask:0xf bank_mask:0xf bound_ctrl:1
	v_mad_u32_u24 v171, v168, v181, v170
	ds_write_b8_d16_hi v184, v171
	s_barrier
	global_store_short_d16_hi v185, v176, s[48:49]
	s_waitcnt lgkmcnt(0)
	s_barrier
	ds_read_b64 v[122:123], v106 offset:0
	ds_read_b64 v[124:125], v106 offset:8
	ds_read_b64 v[126:127], v106 offset:16
	ds_read_b64 v[128:129], v106 offset:96
	ds_read_b64 v[130:131], v106 offset:104
	ds_read_b64 v[132:133], v106 offset:112
	s_waitcnt lgkmcnt(3)
	v_mfma_f32_16x16x128_f8f6f4 v[134:137], v[122:127], v[2:7], 0 cbsz:2 blgp:2
	v_mfma_f32_16x16x128_f8f6f4 v[138:141], v[122:127], v[14:19], 0 cbsz:2 blgp:2
	v_mfma_f32_16x16x128_f8f6f4 v[142:145], v[122:127], v[26:31], v[188:191] cbsz:2 blgp:2
	v_mfma_f32_16x16x128_f8f6f4 v[204:207], v[122:127], v[38:43], 0 cbsz:2 blgp:2
	v_mfma_f32_16x16x128_f8f6f4 v[208:211], v[122:127], v[50:55], 0 cbsz:2 blgp:2
	v_mfma_f32_16x16x128_f8f6f4 v[212:215], v[122:127], v[62:67], v[188:191] cbsz:2 blgp:2
	s_waitcnt lgkmcnt(0)
	v_mfma_f32_16x16x128_f8f6f4 v[134:137], v[128:133], v[8:13], v[134:137] cbsz:2 blgp:2
	v_mfma_f32_16x16x128_f8f6f4 v[204:207], v[128:133], v[44:49], v[204:207] cbsz:2 blgp:2
	v_mfma_f32_16x16x128_f8f6f4 v[138:141], v[128:133], v[20:25], v[138:141] cbsz:2 blgp:2
	v_mfma_f32_16x16x128_f8f6f4 v[208:211], v[128:133], v[56:61], v[208:211] cbsz:2 blgp:2
	v_mfma_f32_16x16x128_f8f6f4 v[142:145], v[128:133], v[32:37], v[142:145] cbsz:2 blgp:2
	v_mfma_f32_16x16x128_f8f6f4 v[212:215], v[128:133], v[68:73], v[212:215] cbsz:2 blgp:2
	v_cndmask_b32_e64 v158, v134, v204, s[4:5]
	v_cndmask_b32_e64 v159, v138, v208, s[4:5]
	v_fma_mix_f32 v158, v158, v1, v84 op_sel_hi:[0,0,1]
	v_fma_mix_f32 v159, v159, v99, v76 op_sel_hi:[0,0,1]
	v_exp_f32_e32 v158, v158
	v_exp_f32_e32 v159, v159
	v_fma_f32 v158, v158, v186, v186
	v_add_f32_e32 v159, 1.0, v159
	v_rcp_f32_e32 v158, v158
	v_rcp_f32_e32 v159, v159
	v_cndmask_b32_e64 v160, v142, v212, s[4:5]
	v_fma_mix_f32 v161, v158, v160, v80 op_sel_hi:[0,0,1]
	v_exp_f32_e32 v161, v161
	s_add_u32 s48, s48, s40
	v_add_f32_e32 v161, 1.0, v161
	v_rcp_f32_e32 v161, v161
	s_addc_u32 s49, s49, s41
	v_fma_f32 v162, v161, -2.0, 1.0
	v_sub_f32_e32 v163, v176, v162
	v_fma_f32 v176, v159, v163, v162
	v_fma_f32 v164, |v176|, s16, v117
	v_fma_f32 v165, |v176|, s17, v118
	v_fma_f32 v166, |v176|, s18, v119
	v_lshrrev_b32_e32 v167, 26, v176
	v_min3_u32 v164, v164, v165, v166
	v_bfi_b32 v168, 31, v164, v167
	s_nop 1
	v_mul_u32_u24_dpp v170, v168, v180 quad_perm:[1,2,3,3] row_mask:0xf bank_mask:0xf bound_ctrl:1
	v_mad_u32_u24 v171, v168, v181, v170
	ds_write_b8_d16_hi v184, v171 offset:416
	s_barrier
	global_store_short_d16_hi v185, v176, s[48:49]
	s_waitcnt lgkmcnt(0)
	s_barrier
	ds_read_b64 v[122:123], v106 offset:416
	ds_read_b64 v[124:125], v106 offset:424
	ds_read_b64 v[126:127], v106 offset:432
	ds_read_b64 v[128:129], v106 offset:512
	ds_read_b64 v[130:131], v106 offset:520
	ds_read_b64 v[132:133], v106 offset:528
	s_waitcnt lgkmcnt(3)
	v_mfma_f32_16x16x128_f8f6f4 v[134:137], v[122:127], v[2:7], 0 cbsz:2 blgp:2
	v_mfma_f32_16x16x128_f8f6f4 v[138:141], v[122:127], v[14:19], 0 cbsz:2 blgp:2
	v_mfma_f32_16x16x128_f8f6f4 v[142:145], v[122:127], v[26:31], v[188:191] cbsz:2 blgp:2
	v_mfma_f32_16x16x128_f8f6f4 v[204:207], v[122:127], v[38:43], 0 cbsz:2 blgp:2
	v_mfma_f32_16x16x128_f8f6f4 v[208:211], v[122:127], v[50:55], 0 cbsz:2 blgp:2
	v_mfma_f32_16x16x128_f8f6f4 v[212:215], v[122:127], v[62:67], v[188:191] cbsz:2 blgp:2
	s_waitcnt lgkmcnt(0)
	v_mfma_f32_16x16x128_f8f6f4 v[134:137], v[128:133], v[8:13], v[134:137] cbsz:2 blgp:2
	v_mfma_f32_16x16x128_f8f6f4 v[204:207], v[128:133], v[44:49], v[204:207] cbsz:2 blgp:2
	v_mfma_f32_16x16x128_f8f6f4 v[138:141], v[128:133], v[20:25], v[138:141] cbsz:2 blgp:2
	v_mfma_f32_16x16x128_f8f6f4 v[208:211], v[128:133], v[56:61], v[208:211] cbsz:2 blgp:2
	v_mfma_f32_16x16x128_f8f6f4 v[142:145], v[128:133], v[32:37], v[142:145] cbsz:2 blgp:2
	v_mfma_f32_16x16x128_f8f6f4 v[212:215], v[128:133], v[68:73], v[212:215] cbsz:2 blgp:2
	v_cndmask_b32_e64 v158, v134, v204, s[4:5]
	v_cndmask_b32_e64 v159, v138, v208, s[4:5]
	v_fma_mix_f32 v158, v158, v1, v84 op_sel:[0,0,1] op_sel_hi:[0,0,1]
	v_fma_mix_f32 v159, v159, v99, v76 op_sel:[0,0,1] op_sel_hi:[0,0,1]
	v_exp_f32_e32 v158, v158
	v_exp_f32_e32 v159, v159
	v_fma_f32 v158, v158, v186, v186
	v_add_f32_e32 v159, 1.0, v159
	v_rcp_f32_e32 v158, v158
	v_rcp_f32_e32 v159, v159
	v_cndmask_b32_e64 v160, v142, v212, s[4:5]
	v_fma_mix_f32 v161, v158, v160, v80 op_sel:[0,0,1] op_sel_hi:[0,0,1]
	v_exp_f32_e32 v161, v161
	s_add_u32 s48, s48, s40
	v_add_f32_e32 v161, 1.0, v161
	v_rcp_f32_e32 v161, v161
	s_addc_u32 s49, s49, s41
	v_fma_f32 v162, v161, -2.0, 1.0
	v_sub_f32_e32 v163, v176, v162
	v_fma_f32 v176, v159, v163, v162
	v_fma_f32 v164, |v176|, s16, v117
	v_fma_f32 v165, |v176|, s17, v118
	v_fma_f32 v166, |v176|, s18, v119
	v_lshrrev_b32_e32 v167, 26, v176
	v_min3_u32 v164, v164, v165, v166
	v_bfi_b32 v168, 31, v164, v167
	s_nop 1
	v_mul_u32_u24_dpp v170, v168, v180 quad_perm:[1,2,3,3] row_mask:0xf bank_mask:0xf bound_ctrl:1
	v_mad_u32_u24 v171, v168, v181, v170
	ds_write_b8_d16_hi v184, v171
	s_barrier
	global_store_short_d16_hi v185, v176, s[48:49]
	s_waitcnt lgkmcnt(0)
	s_barrier
	ds_read_b64 v[122:123], v106 offset:0
	ds_read_b64 v[124:125], v106 offset:8
	ds_read_b64 v[126:127], v106 offset:16
	ds_read_b64 v[128:129], v106 offset:96
	ds_read_b64 v[130:131], v106 offset:104
	ds_read_b64 v[132:133], v106 offset:112
	s_waitcnt lgkmcnt(3)
	v_mfma_f32_16x16x128_f8f6f4 v[134:137], v[122:127], v[2:7], 0 cbsz:2 blgp:2
	v_mfma_f32_16x16x128_f8f6f4 v[138:141], v[122:127], v[14:19], 0 cbsz:2 blgp:2
	v_mfma_f32_16x16x128_f8f6f4 v[142:145], v[122:127], v[26:31], v[188:191] cbsz:2 blgp:2
	v_mfma_f32_16x16x128_f8f6f4 v[204:207], v[122:127], v[38:43], 0 cbsz:2 blgp:2
	v_mfma_f32_16x16x128_f8f6f4 v[208:211], v[122:127], v[50:55], 0 cbsz:2 blgp:2
	v_mfma_f32_16x16x128_f8f6f4 v[212:215], v[122:127], v[62:67], v[188:191] cbsz:2 blgp:2
	s_waitcnt lgkmcnt(0)
	v_mfma_f32_16x16x128_f8f6f4 v[134:137], v[128:133], v[8:13], v[134:137] cbsz:2 blgp:2
	v_mfma_f32_16x16x128_f8f6f4 v[204:207], v[128:133], v[44:49], v[204:207] cbsz:2 blgp:2
	v_mfma_f32_16x16x128_f8f6f4 v[138:141], v[128:133], v[20:25], v[138:141] cbsz:2 blgp:2
	v_mfma_f32_16x16x128_f8f6f4 v[208:211], v[128:133], v[56:61], v[208:211] cbsz:2 blgp:2
	v_mfma_f32_16x16x128_f8f6f4 v[142:145], v[128:133], v[32:37], v[142:145] cbsz:2 blgp:2
	v_mfma_f32_16x16x128_f8f6f4 v[212:215], v[128:133], v[68:73], v[212:215] cbsz:2 blgp:2
	v_cndmask_b32_e64 v158, v134, v204, s[4:5]
	v_cndmask_b32_e64 v159, v138, v208, s[4:5]
	v_fma_mix_f32 v158, v158, v1, v85 op_sel_hi:[0,0,1]
	v_fma_mix_f32 v159, v159, v99, v77 op_sel_hi:[0,0,1]
	v_exp_f32_e32 v158, v158
	v_exp_f32_e32 v159, v159
	v_fma_f32 v158, v158, v186, v186
	v_add_f32_e32 v159, 1.0, v159
	v_rcp_f32_e32 v158, v158
	v_rcp_f32_e32 v159, v159
	v_cndmask_b32_e64 v160, v142, v212, s[4:5]
	v_fma_mix_f32 v161, v158, v160, v81 op_sel_hi:[0,0,1]
	v_exp_f32_e32 v161, v161
	s_add_u32 s48, s48, s40
	v_add_f32_e32 v161, 1.0, v161
	v_rcp_f32_e32 v161, v161
	s_addc_u32 s49, s49, s41
	v_fma_f32 v162, v161, -2.0, 1.0
	v_sub_f32_e32 v163, v176, v162
	v_fma_f32 v176, v159, v163, v162
	v_fma_f32 v164, |v176|, s16, v117
	v_fma_f32 v165, |v176|, s17, v118
	v_fma_f32 v166, |v176|, s18, v119
	v_lshrrev_b32_e32 v167, 26, v176
	v_min3_u32 v164, v164, v165, v166
	v_bfi_b32 v168, 31, v164, v167
	s_nop 1
	v_mul_u32_u24_dpp v170, v168, v180 quad_perm:[1,2,3,3] row_mask:0xf bank_mask:0xf bound_ctrl:1
	v_mad_u32_u24 v171, v168, v181, v170
	ds_write_b8_d16_hi v184, v171 offset:416
	s_barrier
	global_store_short_d16_hi v185, v176, s[48:49]
	s_waitcnt lgkmcnt(0)
	s_barrier
	ds_read_b64 v[122:123], v106 offset:416
	ds_read_b64 v[124:125], v106 offset:424
	ds_read_b64 v[126:127], v106 offset:432
	ds_read_b64 v[128:129], v106 offset:512
	ds_read_b64 v[130:131], v106 offset:520
	ds_read_b64 v[132:133], v106 offset:528
	s_waitcnt lgkmcnt(3)
	v_mfma_f32_16x16x128_f8f6f4 v[134:137], v[122:127], v[2:7], 0 cbsz:2 blgp:2
	v_mfma_f32_16x16x128_f8f6f4 v[138:141], v[122:127], v[14:19], 0 cbsz:2 blgp:2
	v_mfma_f32_16x16x128_f8f6f4 v[142:145], v[122:127], v[26:31], v[188:191] cbsz:2 blgp:2
	v_mfma_f32_16x16x128_f8f6f4 v[204:207], v[122:127], v[38:43], 0 cbsz:2 blgp:2
	v_mfma_f32_16x16x128_f8f6f4 v[208:211], v[122:127], v[50:55], 0 cbsz:2 blgp:2
	v_mfma_f32_16x16x128_f8f6f4 v[212:215], v[122:127], v[62:67], v[188:191] cbsz:2 blgp:2
	s_waitcnt lgkmcnt(0)
	v_mfma_f32_16x16x128_f8f6f4 v[134:137], v[128:133], v[8:13], v[134:137] cbsz:2 blgp:2
	v_mfma_f32_16x16x128_f8f6f4 v[204:207], v[128:133], v[44:49], v[204:207] cbsz:2 blgp:2
	v_mfma_f32_16x16x128_f8f6f4 v[138:141], v[128:133], v[20:25], v[138:141] cbsz:2 blgp:2
	v_mfma_f32_16x16x128_f8f6f4 v[208:211], v[128:133], v[56:61], v[208:211] cbsz:2 blgp:2
	v_mfma_f32_16x16x128_f8f6f4 v[142:145], v[128:133], v[32:37], v[142:145] cbsz:2 blgp:2
	v_mfma_f32_16x16x128_f8f6f4 v[212:215], v[128:133], v[68:73], v[212:215] cbsz:2 blgp:2
	v_cndmask_b32_e64 v158, v134, v204, s[4:5]
	v_cndmask_b32_e64 v159, v138, v208, s[4:5]
	v_fma_mix_f32 v158, v158, v1, v85 op_sel:[0,0,1] op_sel_hi:[0,0,1]
	v_fma_mix_f32 v159, v159, v99, v77 op_sel:[0,0,1] op_sel_hi:[0,0,1]
	v_exp_f32_e32 v158, v158
	v_exp_f32_e32 v159, v159
	v_fma_f32 v158, v158, v186, v186
	v_add_f32_e32 v159, 1.0, v159
	v_rcp_f32_e32 v158, v158
	v_rcp_f32_e32 v159, v159
	v_cndmask_b32_e64 v160, v142, v212, s[4:5]
	v_fma_mix_f32 v161, v158, v160, v81 op_sel:[0,0,1] op_sel_hi:[0,0,1]
	v_exp_f32_e32 v161, v161
	s_add_u32 s48, s48, s40
	v_add_f32_e32 v161, 1.0, v161
	v_rcp_f32_e32 v161, v161
	s_addc_u32 s49, s49, s41
	v_fma_f32 v162, v161, -2.0, 1.0
	v_sub_f32_e32 v163, v176, v162
	v_fma_f32 v176, v159, v163, v162
	v_fma_f32 v164, |v176|, s16, v117
	v_fma_f32 v165, |v176|, s17, v118
	v_fma_f32 v166, |v176|, s18, v119
	v_lshrrev_b32_e32 v167, 26, v176
	v_min3_u32 v164, v164, v165, v166
	v_bfi_b32 v168, 31, v164, v167
	s_nop 1
	v_mul_u32_u24_dpp v170, v168, v180 quad_perm:[1,2,3,3] row_mask:0xf bank_mask:0xf bound_ctrl:1
	v_mad_u32_u24 v171, v168, v181, v170
	ds_write_b8_d16_hi v184, v171
	s_barrier
	global_store_short_d16_hi v185, v176, s[48:49]
	s_waitcnt lgkmcnt(0)
	s_barrier
	ds_read_b64 v[122:123], v106 offset:0
	ds_read_b64 v[124:125], v106 offset:8
	ds_read_b64 v[126:127], v106 offset:16
	ds_read_b64 v[128:129], v106 offset:96
	ds_read_b64 v[130:131], v106 offset:104
	ds_read_b64 v[132:133], v106 offset:112
	s_waitcnt vmcnt(8)
	global_load_dwordx4 v[82:85], v[196:197], off
	global_load_dwordx4 v[74:77], v[196:197], off offset:512
	global_load_dwordx4 v[78:81], v[196:197], off offset:1024
	v_lshl_add_u64 v[196:197], v[196:197], 0, s[42:43]
	s_waitcnt lgkmcnt(3)
	v_mfma_f32_16x16x128_f8f6f4 v[134:137], v[122:127], v[2:7], 0 cbsz:2 blgp:2
	v_mfma_f32_16x16x128_f8f6f4 v[138:141], v[122:127], v[14:19], 0 cbsz:2 blgp:2
	v_mfma_f32_16x16x128_f8f6f4 v[142:145], v[122:127], v[26:31], v[188:191] cbsz:2 blgp:2
	v_mfma_f32_16x16x128_f8f6f4 v[204:207], v[122:127], v[38:43], 0 cbsz:2 blgp:2
	v_mfma_f32_16x16x128_f8f6f4 v[208:211], v[122:127], v[50:55], 0 cbsz:2 blgp:2
	v_mfma_f32_16x16x128_f8f6f4 v[212:215], v[122:127], v[62:67], v[188:191] cbsz:2 blgp:2
	s_waitcnt lgkmcnt(0)
	v_mfma_f32_16x16x128_f8f6f4 v[134:137], v[128:133], v[8:13], v[134:137] cbsz:2 blgp:2
	v_mfma_f32_16x16x128_f8f6f4 v[204:207], v[128:133], v[44:49], v[204:207] cbsz:2 blgp:2
	v_mfma_f32_16x16x128_f8f6f4 v[138:141], v[128:133], v[20:25], v[138:141] cbsz:2 blgp:2
	v_mfma_f32_16x16x128_f8f6f4 v[208:211], v[128:133], v[56:61], v[208:211] cbsz:2 blgp:2
	v_mfma_f32_16x16x128_f8f6f4 v[142:145], v[128:133], v[32:37], v[142:145] cbsz:2 blgp:2
	v_mfma_f32_16x16x128_f8f6f4 v[212:215], v[128:133], v[68:73], v[212:215] cbsz:2 blgp:2
	v_cndmask_b32_e64 v158, v134, v204, s[4:5]
	v_cndmask_b32_e64 v159, v138, v208, s[4:5]
	v_fma_mix_f32 v158, v158, v1, v146 op_sel_hi:[0,0,1]
	v_fma_mix_f32 v159, v159, v99, v150 op_sel_hi:[0,0,1]
	v_exp_f32_e32 v158, v158
	v_exp_f32_e32 v159, v159
	v_fma_f32 v158, v158, v186, v186
	v_add_f32_e32 v159, 1.0, v159
	v_rcp_f32_e32 v158, v158
	v_rcp_f32_e32 v159, v159
	v_cndmask_b32_e64 v160, v142, v212, s[4:5]
	v_fma_mix_f32 v161, v158, v160, v154 op_sel_hi:[0,0,1]
	v_exp_f32_e32 v161, v161
	s_add_u32 s48, s48, s40
	v_add_f32_e32 v161, 1.0, v161
	v_rcp_f32_e32 v161, v161
	s_addc_u32 s49, s49, s41
	v_fma_f32 v162, v161, -2.0, 1.0
	v_sub_f32_e32 v163, v176, v162
	v_fma_f32 v176, v159, v163, v162
	v_fma_f32 v164, |v176|, s16, v117
	v_fma_f32 v165, |v176|, s17, v118
	v_fma_f32 v166, |v176|, s18, v119
	v_lshrrev_b32_e32 v167, 26, v176
	v_min3_u32 v164, v164, v165, v166
	v_bfi_b32 v168, 31, v164, v167
	s_nop 1
	v_mul_u32_u24_dpp v170, v168, v180 quad_perm:[1,2,3,3] row_mask:0xf bank_mask:0xf bound_ctrl:1
	v_mad_u32_u24 v171, v168, v181, v170
	ds_write_b8_d16_hi v184, v171 offset:416
	s_barrier
	global_store_short_d16_hi v185, v176, s[48:49]
	s_waitcnt lgkmcnt(0)
	s_barrier
	ds_read_b64 v[122:123], v106 offset:416
	ds_read_b64 v[124:125], v106 offset:424
	ds_read_b64 v[126:127], v106 offset:432
	ds_read_b64 v[128:129], v106 offset:512
	ds_read_b64 v[130:131], v106 offset:520
	ds_read_b64 v[132:133], v106 offset:528
	s_waitcnt lgkmcnt(3)
	v_mfma_f32_16x16x128_f8f6f4 v[134:137], v[122:127], v[2:7], 0 cbsz:2 blgp:2
	v_mfma_f32_16x16x128_f8f6f4 v[138:141], v[122:127], v[14:19], 0 cbsz:2 blgp:2
	v_mfma_f32_16x16x128_f8f6f4 v[142:145], v[122:127], v[26:31], v[188:191] cbsz:2 blgp:2
	v_mfma_f32_16x16x128_f8f6f4 v[204:207], v[122:127], v[38:43], 0 cbsz:2 blgp:2
	v_mfma_f32_16x16x128_f8f6f4 v[208:211], v[122:127], v[50:55], 0 cbsz:2 blgp:2
	v_mfma_f32_16x16x128_f8f6f4 v[212:215], v[122:127], v[62:67], v[188:191] cbsz:2 blgp:2
	s_waitcnt lgkmcnt(0)
	v_mfma_f32_16x16x128_f8f6f4 v[134:137], v[128:133], v[8:13], v[134:137] cbsz:2 blgp:2
	v_mfma_f32_16x16x128_f8f6f4 v[204:207], v[128:133], v[44:49], v[204:207] cbsz:2 blgp:2
	v_mfma_f32_16x16x128_f8f6f4 v[138:141], v[128:133], v[20:25], v[138:141] cbsz:2 blgp:2
	v_mfma_f32_16x16x128_f8f6f4 v[208:211], v[128:133], v[56:61], v[208:211] cbsz:2 blgp:2
	v_mfma_f32_16x16x128_f8f6f4 v[142:145], v[128:133], v[32:37], v[142:145] cbsz:2 blgp:2
	v_mfma_f32_16x16x128_f8f6f4 v[212:215], v[128:133], v[68:73], v[212:215] cbsz:2 blgp:2
	v_cndmask_b32_e64 v158, v134, v204, s[4:5]
	v_cndmask_b32_e64 v159, v138, v208, s[4:5]
	v_fma_mix_f32 v158, v158, v1, v146 op_sel:[0,0,1] op_sel_hi:[0,0,1]
	v_fma_mix_f32 v159, v159, v99, v150 op_sel:[0,0,1] op_sel_hi:[0,0,1]
	v_exp_f32_e32 v158, v158
	v_exp_f32_e32 v159, v159
	v_fma_f32 v158, v158, v186, v186
	v_add_f32_e32 v159, 1.0, v159
	v_rcp_f32_e32 v158, v158
	v_rcp_f32_e32 v159, v159
	v_cndmask_b32_e64 v160, v142, v212, s[4:5]
	v_fma_mix_f32 v161, v158, v160, v154 op_sel:[0,0,1] op_sel_hi:[0,0,1]
	v_exp_f32_e32 v161, v161
	s_add_u32 s48, s48, s40
	v_add_f32_e32 v161, 1.0, v161
	v_rcp_f32_e32 v161, v161
	s_addc_u32 s49, s49, s41
	v_fma_f32 v162, v161, -2.0, 1.0
	v_sub_f32_e32 v163, v176, v162
	v_fma_f32 v176, v159, v163, v162
	v_fma_f32 v164, |v176|, s16, v117
	v_fma_f32 v165, |v176|, s17, v118
	v_fma_f32 v166, |v176|, s18, v119
	v_lshrrev_b32_e32 v167, 26, v176
	v_min3_u32 v164, v164, v165, v166
	v_bfi_b32 v168, 31, v164, v167
	s_nop 1
	v_mul_u32_u24_dpp v170, v168, v180 quad_perm:[1,2,3,3] row_mask:0xf bank_mask:0xf bound_ctrl:1
	v_mad_u32_u24 v171, v168, v181, v170
	ds_write_b8_d16_hi v184, v171
	s_barrier
	global_store_short_d16_hi v185, v176, s[48:49]
	s_waitcnt lgkmcnt(0)
	s_barrier
	ds_read_b64 v[122:123], v106 offset:0
	ds_read_b64 v[124:125], v106 offset:8
	ds_read_b64 v[126:127], v106 offset:16
	ds_read_b64 v[128:129], v106 offset:96
	ds_read_b64 v[130:131], v106 offset:104
	ds_read_b64 v[132:133], v106 offset:112
	s_waitcnt lgkmcnt(3)
	v_mfma_f32_16x16x128_f8f6f4 v[134:137], v[122:127], v[2:7], 0 cbsz:2 blgp:2
	v_mfma_f32_16x16x128_f8f6f4 v[138:141], v[122:127], v[14:19], 0 cbsz:2 blgp:2
	v_mfma_f32_16x16x128_f8f6f4 v[142:145], v[122:127], v[26:31], v[188:191] cbsz:2 blgp:2
	v_mfma_f32_16x16x128_f8f6f4 v[204:207], v[122:127], v[38:43], 0 cbsz:2 blgp:2
	v_mfma_f32_16x16x128_f8f6f4 v[208:211], v[122:127], v[50:55], 0 cbsz:2 blgp:2
	v_mfma_f32_16x16x128_f8f6f4 v[212:215], v[122:127], v[62:67], v[188:191] cbsz:2 blgp:2
	s_waitcnt lgkmcnt(0)
	v_mfma_f32_16x16x128_f8f6f4 v[134:137], v[128:133], v[8:13], v[134:137] cbsz:2 blgp:2
	v_mfma_f32_16x16x128_f8f6f4 v[204:207], v[128:133], v[44:49], v[204:207] cbsz:2 blgp:2
	v_mfma_f32_16x16x128_f8f6f4 v[138:141], v[128:133], v[20:25], v[138:141] cbsz:2 blgp:2
	v_mfma_f32_16x16x128_f8f6f4 v[208:211], v[128:133], v[56:61], v[208:211] cbsz:2 blgp:2
	v_mfma_f32_16x16x128_f8f6f4 v[142:145], v[128:133], v[32:37], v[142:145] cbsz:2 blgp:2
	v_mfma_f32_16x16x128_f8f6f4 v[212:215], v[128:133], v[68:73], v[212:215] cbsz:2 blgp:2
	v_cndmask_b32_e64 v158, v134, v204, s[4:5]
	v_cndmask_b32_e64 v159, v138, v208, s[4:5]
	v_fma_mix_f32 v158, v158, v1, v147 op_sel_hi:[0,0,1]
	v_fma_mix_f32 v159, v159, v99, v151 op_sel_hi:[0,0,1]
	v_exp_f32_e32 v158, v158
	v_exp_f32_e32 v159, v159
	v_fma_f32 v158, v158, v186, v186
	v_add_f32_e32 v159, 1.0, v159
	v_rcp_f32_e32 v158, v158
	v_rcp_f32_e32 v159, v159
	v_cndmask_b32_e64 v160, v142, v212, s[4:5]
	v_fma_mix_f32 v161, v158, v160, v155 op_sel_hi:[0,0,1]
	v_exp_f32_e32 v161, v161
	s_add_u32 s48, s48, s40
	v_add_f32_e32 v161, 1.0, v161
	v_rcp_f32_e32 v161, v161
	s_addc_u32 s49, s49, s41
	v_fma_f32 v162, v161, -2.0, 1.0
	v_sub_f32_e32 v163, v176, v162
	v_fma_f32 v176, v159, v163, v162
	v_fma_f32 v164, |v176|, s16, v117
	v_fma_f32 v165, |v176|, s17, v118
	v_fma_f32 v166, |v176|, s18, v119
	v_lshrrev_b32_e32 v167, 26, v176
	v_min3_u32 v164, v164, v165, v166
	v_bfi_b32 v168, 31, v164, v167
	s_nop 1
	v_mul_u32_u24_dpp v170, v168, v180 quad_perm:[1,2,3,3] row_mask:0xf bank_mask:0xf bound_ctrl:1
	v_mad_u32_u24 v171, v168, v181, v170
	ds_write_b8_d16_hi v184, v171 offset:416
	s_barrier
	global_store_short_d16_hi v185, v176, s[48:49]
	s_waitcnt lgkmcnt(0)
	s_barrier
	ds_read_b64 v[122:123], v106 offset:416
	ds_read_b64 v[124:125], v106 offset:424
	ds_read_b64 v[126:127], v106 offset:432
	ds_read_b64 v[128:129], v106 offset:512
	ds_read_b64 v[130:131], v106 offset:520
	ds_read_b64 v[132:133], v106 offset:528
	s_waitcnt lgkmcnt(3)
	v_mfma_f32_16x16x128_f8f6f4 v[134:137], v[122:127], v[2:7], 0 cbsz:2 blgp:2
	v_mfma_f32_16x16x128_f8f6f4 v[138:141], v[122:127], v[14:19], 0 cbsz:2 blgp:2
	v_mfma_f32_16x16x128_f8f6f4 v[142:145], v[122:127], v[26:31], v[188:191] cbsz:2 blgp:2
	v_mfma_f32_16x16x128_f8f6f4 v[204:207], v[122:127], v[38:43], 0 cbsz:2 blgp:2
	v_mfma_f32_16x16x128_f8f6f4 v[208:211], v[122:127], v[50:55], 0 cbsz:2 blgp:2
	v_mfma_f32_16x16x128_f8f6f4 v[212:215], v[122:127], v[62:67], v[188:191] cbsz:2 blgp:2
	s_waitcnt lgkmcnt(0)
	v_mfma_f32_16x16x128_f8f6f4 v[134:137], v[128:133], v[8:13], v[134:137] cbsz:2 blgp:2
	v_mfma_f32_16x16x128_f8f6f4 v[204:207], v[128:133], v[44:49], v[204:207] cbsz:2 blgp:2
	v_mfma_f32_16x16x128_f8f6f4 v[138:141], v[128:133], v[20:25], v[138:141] cbsz:2 blgp:2
	v_mfma_f32_16x16x128_f8f6f4 v[208:211], v[128:133], v[56:61], v[208:211] cbsz:2 blgp:2
	v_mfma_f32_16x16x128_f8f6f4 v[142:145], v[128:133], v[32:37], v[142:145] cbsz:2 blgp:2
	v_mfma_f32_16x16x128_f8f6f4 v[212:215], v[128:133], v[68:73], v[212:215] cbsz:2 blgp:2
	v_cndmask_b32_e64 v158, v134, v204, s[4:5]
	v_cndmask_b32_e64 v159, v138, v208, s[4:5]
	v_fma_mix_f32 v158, v158, v1, v147 op_sel:[0,0,1] op_sel_hi:[0,0,1]
	v_fma_mix_f32 v159, v159, v99, v151 op_sel:[0,0,1] op_sel_hi:[0,0,1]
	v_exp_f32_e32 v158, v158
	v_exp_f32_e32 v159, v159
	v_fma_f32 v158, v158, v186, v186
	v_add_f32_e32 v159, 1.0, v159
	v_rcp_f32_e32 v158, v158
	v_rcp_f32_e32 v159, v159
	v_cndmask_b32_e64 v160, v142, v212, s[4:5]
	v_fma_mix_f32 v161, v158, v160, v155 op_sel:[0,0,1] op_sel_hi:[0,0,1]
	v_exp_f32_e32 v161, v161
	s_add_u32 s48, s48, s40
	v_add_f32_e32 v161, 1.0, v161
	v_rcp_f32_e32 v161, v161
	s_addc_u32 s49, s49, s41
	v_fma_f32 v162, v161, -2.0, 1.0
	v_sub_f32_e32 v163, v176, v162
	v_fma_f32 v176, v159, v163, v162
	v_fma_f32 v164, |v176|, s16, v117
	v_fma_f32 v165, |v176|, s17, v118
	v_fma_f32 v166, |v176|, s18, v119
	v_lshrrev_b32_e32 v167, 26, v176
	v_min3_u32 v164, v164, v165, v166
	v_bfi_b32 v168, 31, v164, v167
	s_nop 1
	v_mul_u32_u24_dpp v170, v168, v180 quad_perm:[1,2,3,3] row_mask:0xf bank_mask:0xf bound_ctrl:1
	v_mad_u32_u24 v171, v168, v181, v170
	ds_write_b8_d16_hi v184, v171
	s_barrier
	global_store_short_d16_hi v185, v176, s[48:49]
	s_waitcnt lgkmcnt(0)
	s_barrier
	ds_read_b64 v[122:123], v106 offset:0
	ds_read_b64 v[124:125], v106 offset:8
	ds_read_b64 v[126:127], v106 offset:16
	ds_read_b64 v[128:129], v106 offset:96
	ds_read_b64 v[130:131], v106 offset:104
	ds_read_b64 v[132:133], v106 offset:112
	s_waitcnt lgkmcnt(3)
	v_mfma_f32_16x16x128_f8f6f4 v[134:137], v[122:127], v[2:7], 0 cbsz:2 blgp:2
	v_mfma_f32_16x16x128_f8f6f4 v[138:141], v[122:127], v[14:19], 0 cbsz:2 blgp:2
	v_mfma_f32_16x16x128_f8f6f4 v[142:145], v[122:127], v[26:31], v[188:191] cbsz:2 blgp:2
	v_mfma_f32_16x16x128_f8f6f4 v[204:207], v[122:127], v[38:43], 0 cbsz:2 blgp:2
	v_mfma_f32_16x16x128_f8f6f4 v[208:211], v[122:127], v[50:55], 0 cbsz:2 blgp:2
	v_mfma_f32_16x16x128_f8f6f4 v[212:215], v[122:127], v[62:67], v[188:191] cbsz:2 blgp:2
	s_waitcnt lgkmcnt(0)
	v_mfma_f32_16x16x128_f8f6f4 v[134:137], v[128:133], v[8:13], v[134:137] cbsz:2 blgp:2
	v_mfma_f32_16x16x128_f8f6f4 v[204:207], v[128:133], v[44:49], v[204:207] cbsz:2 blgp:2
	v_mfma_f32_16x16x128_f8f6f4 v[138:141], v[128:133], v[20:25], v[138:141] cbsz:2 blgp:2
	v_mfma_f32_16x16x128_f8f6f4 v[208:211], v[128:133], v[56:61], v[208:211] cbsz:2 blgp:2
	v_mfma_f32_16x16x128_f8f6f4 v[142:145], v[128:133], v[32:37], v[142:145] cbsz:2 blgp:2
	v_mfma_f32_16x16x128_f8f6f4 v[212:215], v[128:133], v[68:73], v[212:215] cbsz:2 blgp:2
	v_cndmask_b32_e64 v158, v134, v204, s[4:5]
	v_cndmask_b32_e64 v159, v138, v208, s[4:5]
	v_fma_mix_f32 v158, v158, v1, v148 op_sel_hi:[0,0,1]
	v_fma_mix_f32 v159, v159, v99, v152 op_sel_hi:[0,0,1]
	v_exp_f32_e32 v158, v158
	v_exp_f32_e32 v159, v159
	v_fma_f32 v158, v158, v186, v186
	v_add_f32_e32 v159, 1.0, v159
	v_rcp_f32_e32 v158, v158
	v_rcp_f32_e32 v159, v159
	v_cndmask_b32_e64 v160, v142, v212, s[4:5]
	v_fma_mix_f32 v161, v158, v160, v156 op_sel_hi:[0,0,1]
	v_exp_f32_e32 v161, v161
	s_add_u32 s48, s48, s40
	v_add_f32_e32 v161, 1.0, v161
	v_rcp_f32_e32 v161, v161
	s_addc_u32 s49, s49, s41
	v_fma_f32 v162, v161, -2.0, 1.0
	v_sub_f32_e32 v163, v176, v162
	v_fma_f32 v176, v159, v163, v162
	v_fma_f32 v164, |v176|, s16, v117
	v_fma_f32 v165, |v176|, s17, v118
	v_fma_f32 v166, |v176|, s18, v119
	v_lshrrev_b32_e32 v167, 26, v176
	v_min3_u32 v164, v164, v165, v166
	v_bfi_b32 v168, 31, v164, v167
	s_nop 1
	v_mul_u32_u24_dpp v170, v168, v180 quad_perm:[1,2,3,3] row_mask:0xf bank_mask:0xf bound_ctrl:1
	v_mad_u32_u24 v171, v168, v181, v170
	ds_write_b8_d16_hi v184, v171 offset:416
	s_barrier
	global_store_short_d16_hi v185, v176, s[48:49]
	s_waitcnt lgkmcnt(0)
	s_barrier
	ds_read_b64 v[122:123], v106 offset:416
	ds_read_b64 v[124:125], v106 offset:424
	ds_read_b64 v[126:127], v106 offset:432
	ds_read_b64 v[128:129], v106 offset:512
	ds_read_b64 v[130:131], v106 offset:520
	ds_read_b64 v[132:133], v106 offset:528
	s_waitcnt lgkmcnt(3)
	v_mfma_f32_16x16x128_f8f6f4 v[134:137], v[122:127], v[2:7], 0 cbsz:2 blgp:2
	v_mfma_f32_16x16x128_f8f6f4 v[138:141], v[122:127], v[14:19], 0 cbsz:2 blgp:2
	v_mfma_f32_16x16x128_f8f6f4 v[142:145], v[122:127], v[26:31], v[188:191] cbsz:2 blgp:2
	v_mfma_f32_16x16x128_f8f6f4 v[204:207], v[122:127], v[38:43], 0 cbsz:2 blgp:2
	v_mfma_f32_16x16x128_f8f6f4 v[208:211], v[122:127], v[50:55], 0 cbsz:2 blgp:2
	v_mfma_f32_16x16x128_f8f6f4 v[212:215], v[122:127], v[62:67], v[188:191] cbsz:2 blgp:2
	s_waitcnt lgkmcnt(0)
	v_mfma_f32_16x16x128_f8f6f4 v[134:137], v[128:133], v[8:13], v[134:137] cbsz:2 blgp:2
	v_mfma_f32_16x16x128_f8f6f4 v[204:207], v[128:133], v[44:49], v[204:207] cbsz:2 blgp:2
	v_mfma_f32_16x16x128_f8f6f4 v[138:141], v[128:133], v[20:25], v[138:141] cbsz:2 blgp:2
	v_mfma_f32_16x16x128_f8f6f4 v[208:211], v[128:133], v[56:61], v[208:211] cbsz:2 blgp:2
	v_mfma_f32_16x16x128_f8f6f4 v[142:145], v[128:133], v[32:37], v[142:145] cbsz:2 blgp:2
	v_mfma_f32_16x16x128_f8f6f4 v[212:215], v[128:133], v[68:73], v[212:215] cbsz:2 blgp:2
	v_cndmask_b32_e64 v158, v134, v204, s[4:5]
	v_cndmask_b32_e64 v159, v138, v208, s[4:5]
	v_fma_mix_f32 v158, v158, v1, v148 op_sel:[0,0,1] op_sel_hi:[0,0,1]
	v_fma_mix_f32 v159, v159, v99, v152 op_sel:[0,0,1] op_sel_hi:[0,0,1]
	v_exp_f32_e32 v158, v158
	v_exp_f32_e32 v159, v159
	v_fma_f32 v158, v158, v186, v186
	v_add_f32_e32 v159, 1.0, v159
	v_rcp_f32_e32 v158, v158
	v_rcp_f32_e32 v159, v159
	v_cndmask_b32_e64 v160, v142, v212, s[4:5]
	v_fma_mix_f32 v161, v158, v160, v156 op_sel:[0,0,1] op_sel_hi:[0,0,1]
	v_exp_f32_e32 v161, v161
	s_add_u32 s48, s48, s40
	v_add_f32_e32 v161, 1.0, v161
	v_rcp_f32_e32 v161, v161
	s_addc_u32 s49, s49, s41
	v_fma_f32 v162, v161, -2.0, 1.0
	v_sub_f32_e32 v163, v176, v162
	v_fma_f32 v176, v159, v163, v162
	v_fma_f32 v164, |v176|, s16, v117
	v_fma_f32 v165, |v176|, s17, v118
	v_fma_f32 v166, |v176|, s18, v119
	v_lshrrev_b32_e32 v167, 26, v176
	v_min3_u32 v164, v164, v165, v166
	v_bfi_b32 v168, 31, v164, v167
	s_nop 1
	v_mul_u32_u24_dpp v170, v168, v180 quad_perm:[1,2,3,3] row_mask:0xf bank_mask:0xf bound_ctrl:1
	v_mad_u32_u24 v171, v168, v181, v170
	ds_write_b8_d16_hi v184, v171
	s_barrier
	global_store_short_d16_hi v185, v176, s[48:49]
	s_waitcnt lgkmcnt(0)
	s_barrier
	ds_read_b64 v[122:123], v106 offset:0
	ds_read_b64 v[124:125], v106 offset:8
	ds_read_b64 v[126:127], v106 offset:16
	ds_read_b64 v[128:129], v106 offset:96
	ds_read_b64 v[130:131], v106 offset:104
	ds_read_b64 v[132:133], v106 offset:112
	s_waitcnt lgkmcnt(3)
	v_mfma_f32_16x16x128_f8f6f4 v[134:137], v[122:127], v[2:7], 0 cbsz:2 blgp:2
	v_mfma_f32_16x16x128_f8f6f4 v[138:141], v[122:127], v[14:19], 0 cbsz:2 blgp:2
	v_mfma_f32_16x16x128_f8f6f4 v[142:145], v[122:127], v[26:31], v[188:191] cbsz:2 blgp:2
	v_mfma_f32_16x16x128_f8f6f4 v[204:207], v[122:127], v[38:43], 0 cbsz:2 blgp:2
	v_mfma_f32_16x16x128_f8f6f4 v[208:211], v[122:127], v[50:55], 0 cbsz:2 blgp:2
	v_mfma_f32_16x16x128_f8f6f4 v[212:215], v[122:127], v[62:67], v[188:191] cbsz:2 blgp:2
	s_waitcnt lgkmcnt(0)
	v_mfma_f32_16x16x128_f8f6f4 v[134:137], v[128:133], v[8:13], v[134:137] cbsz:2 blgp:2
	v_mfma_f32_16x16x128_f8f6f4 v[204:207], v[128:133], v[44:49], v[204:207] cbsz:2 blgp:2
	v_mfma_f32_16x16x128_f8f6f4 v[138:141], v[128:133], v[20:25], v[138:141] cbsz:2 blgp:2
	v_mfma_f32_16x16x128_f8f6f4 v[208:211], v[128:133], v[56:61], v[208:211] cbsz:2 blgp:2
	v_mfma_f32_16x16x128_f8f6f4 v[142:145], v[128:133], v[32:37], v[142:145] cbsz:2 blgp:2
	v_mfma_f32_16x16x128_f8f6f4 v[212:215], v[128:133], v[68:73], v[212:215] cbsz:2 blgp:2
	v_cndmask_b32_e64 v158, v134, v204, s[4:5]
	v_cndmask_b32_e64 v159, v138, v208, s[4:5]
	v_fma_mix_f32 v158, v158, v1, v149 op_sel_hi:[0,0,1]
	v_fma_mix_f32 v159, v159, v99, v153 op_sel_hi:[0,0,1]
	v_exp_f32_e32 v158, v158
	v_exp_f32_e32 v159, v159
	v_fma_f32 v158, v158, v186, v186
	v_add_f32_e32 v159, 1.0, v159
	v_rcp_f32_e32 v158, v158
	v_rcp_f32_e32 v159, v159
	v_cndmask_b32_e64 v160, v142, v212, s[4:5]
	v_fma_mix_f32 v161, v158, v160, v157 op_sel_hi:[0,0,1]
	v_exp_f32_e32 v161, v161
	s_add_u32 s48, s48, s40
	v_add_f32_e32 v161, 1.0, v161
	v_rcp_f32_e32 v161, v161
	s_addc_u32 s49, s49, s41
	v_fma_f32 v162, v161, -2.0, 1.0
	v_sub_f32_e32 v163, v176, v162
	v_fma_f32 v176, v159, v163, v162
	v_fma_f32 v164, |v176|, s16, v117
	v_fma_f32 v165, |v176|, s17, v118
	v_fma_f32 v166, |v176|, s18, v119
	v_lshrrev_b32_e32 v167, 26, v176
	v_min3_u32 v164, v164, v165, v166
	v_bfi_b32 v168, 31, v164, v167
	s_nop 1
	v_mul_u32_u24_dpp v170, v168, v180 quad_perm:[1,2,3,3] row_mask:0xf bank_mask:0xf bound_ctrl:1
	v_mad_u32_u24 v171, v168, v181, v170
	ds_write_b8_d16_hi v184, v171 offset:416
	s_barrier
	global_store_short_d16_hi v185, v176, s[48:49]
	s_waitcnt lgkmcnt(0)
	s_barrier
	ds_read_b64 v[122:123], v106 offset:416
	ds_read_b64 v[124:125], v106 offset:424
	ds_read_b64 v[126:127], v106 offset:432
	ds_read_b64 v[128:129], v106 offset:512
	ds_read_b64 v[130:131], v106 offset:520
	ds_read_b64 v[132:133], v106 offset:528
	s_add_i32 s44, s44, 16
	s_waitcnt lgkmcnt(3)
	v_mfma_f32_16x16x128_f8f6f4 v[134:137], v[122:127], v[2:7], 0 cbsz:2 blgp:2
	v_mfma_f32_16x16x128_f8f6f4 v[138:141], v[122:127], v[14:19], 0 cbsz:2 blgp:2
	v_mfma_f32_16x16x128_f8f6f4 v[142:145], v[122:127], v[26:31], v[188:191] cbsz:2 blgp:2
	v_mfma_f32_16x16x128_f8f6f4 v[204:207], v[122:127], v[38:43], 0 cbsz:2 blgp:2
	v_mfma_f32_16x16x128_f8f6f4 v[208:211], v[122:127], v[50:55], 0 cbsz:2 blgp:2
	v_mfma_f32_16x16x128_f8f6f4 v[212:215], v[122:127], v[62:67], v[188:191] cbsz:2 blgp:2
	s_waitcnt lgkmcnt(0)
	v_mfma_f32_16x16x128_f8f6f4 v[134:137], v[128:133], v[8:13], v[134:137] cbsz:2 blgp:2
	v_mfma_f32_16x16x128_f8f6f4 v[204:207], v[128:133], v[44:49], v[204:207] cbsz:2 blgp:2
	v_mfma_f32_16x16x128_f8f6f4 v[138:141], v[128:133], v[20:25], v[138:141] cbsz:2 blgp:2
	v_mfma_f32_16x16x128_f8f6f4 v[208:211], v[128:133], v[56:61], v[208:211] cbsz:2 blgp:2
	v_mfma_f32_16x16x128_f8f6f4 v[142:145], v[128:133], v[32:37], v[142:145] cbsz:2 blgp:2
	v_mfma_f32_16x16x128_f8f6f4 v[212:215], v[128:133], v[68:73], v[212:215] cbsz:2 blgp:2
	v_cndmask_b32_e64 v158, v134, v204, s[4:5]
	v_cndmask_b32_e64 v159, v138, v208, s[4:5]
	v_fma_mix_f32 v158, v158, v1, v149 op_sel:[0,0,1] op_sel_hi:[0,0,1]
	v_fma_mix_f32 v159, v159, v99, v153 op_sel:[0,0,1] op_sel_hi:[0,0,1]
	v_exp_f32_e32 v158, v158
	v_exp_f32_e32 v159, v159
	v_fma_f32 v158, v158, v186, v186
	v_add_f32_e32 v159, 1.0, v159
	v_rcp_f32_e32 v158, v158
	v_rcp_f32_e32 v159, v159
	v_cndmask_b32_e64 v160, v142, v212, s[4:5]
	v_fma_mix_f32 v161, v158, v160, v157 op_sel:[0,0,1] op_sel_hi:[0,0,1]
	v_exp_f32_e32 v161, v161
	s_add_u32 s48, s48, s40
	v_add_f32_e32 v161, 1.0, v161
	v_rcp_f32_e32 v161, v161
	s_addc_u32 s49, s49, s41
	v_fma_f32 v162, v161, -2.0, 1.0
	v_sub_f32_e32 v163, v176, v162
	v_fma_f32 v176, v159, v163, v162
	v_fma_f32 v164, |v176|, s16, v117
	v_fma_f32 v165, |v176|, s17, v118
	v_fma_f32 v166, |v176|, s18, v119
	v_lshrrev_b32_e32 v167, 26, v176
	v_min3_u32 v164, v164, v165, v166
	v_bfi_b32 v168, 31, v164, v167
	s_nop 1
	v_mul_u32_u24_dpp v170, v168, v180 quad_perm:[1,2,3,3] row_mask:0xf bank_mask:0xf bound_ctrl:1
	v_mad_u32_u24 v171, v168, v181, v170
	ds_write_b8_d16_hi v184, v171
	s_barrier
	global_store_short_d16_hi v185, v176, s[48:49]
	s_cmp_lt_i32 s44, s45
	s_waitcnt lgkmcnt(0)
	s_barrier
	s_cbranch_scc1 .Lscan_loop_b_st

.Lscan_loop_a_f2:
	ds_read_b64 v[128:129], v105 offset:96
	ds_read_b64 v[130:131], v105 offset:104
	ds_read_b64 v[132:133], v105 offset:112
	s_waitcnt vmcnt(8)
	global_load_dwordx4 v[146:149], v[196:197], off
	global_load_dwordx4 v[150:153], v[196:197], off offset:512
	global_load_dwordx4 v[154:157], v[196:197], off offset:1024
	v_lshl_add_u64 v[196:197], v[196:197], 0, s[42:43]
	s_waitcnt lgkmcnt(3)
	v_mfma_f32_16x16x128_f8f6f4 v[134:137], v[122:127], v[2:7], 0 cbsz:2 blgp:2
	v_mfma_f32_16x16x128_f8f6f4 v[138:141], v[122:127], v[14:19], 0 cbsz:2 blgp:2
	v_mfma_f32_16x16x128_f8f6f4 v[142:145], v[122:127], v[26:31], v[188:191] cbsz:2 blgp:2
	v_mfma_f32_16x16x128_f8f6f4 v[204:207], v[122:127], v[38:43], 0 cbsz:2 blgp:2
	v_mfma_f32_16x16x128_f8f6f4 v[208:211], v[122:127], v[50:55], 0 cbsz:2 blgp:2
	v_mfma_f32_16x16x128_f8f6f4 v[212:215], v[122:127], v[62:67], v[188:191] cbsz:2 blgp:2
	s_waitcnt lgkmcnt(0)
	v_mfma_f32_16x16x128_f8f6f4 v[134:137], v[128:133], v[8:13], v[134:137] cbsz:2 blgp:2
	v_mfma_f32_16x16x128_f8f6f4 v[204:207], v[128:133], v[44:49], v[204:207] cbsz:2 blgp:2
	v_mfma_f32_16x16x128_f8f6f4 v[138:141], v[128:133], v[20:25], v[138:141] cbsz:2 blgp:2
	v_mfma_f32_16x16x128_f8f6f4 v[208:211], v[128:133], v[56:61], v[208:211] cbsz:2 blgp:2
	v_mfma_f32_16x16x128_f8f6f4 v[142:145], v[128:133], v[32:37], v[142:145] cbsz:2 blgp:2
	v_mfma_f32_16x16x128_f8f6f4 v[212:215], v[128:133], v[68:73], v[212:215] cbsz:2 blgp:2
	v_cndmask_b32_e64 v158, v134, v204, s[0:1]
	v_cndmask_b32_e64 v159, v138, v208, s[0:1]
	v_fma_mix_f32 v158, v158, v100, v82 op_sel_hi:[0,0,1]
	v_fma_mix_f32 v159, v159, v101, v74 op_sel_hi:[0,0,1]
	v_exp_f32_e32 v158, v158
	v_exp_f32_e32 v159, v159
	v_fma_f32 v158, v158, v186, v186
	v_add_f32_e32 v159, 1.0, v159
	v_rcp_f32_e32 v158, v158
	v_rcp_f32_e32 v159, v159
	v_cndmask_b32_e64 v160, v142, v212, s[0:1]
	v_fma_mix_f32 v161, v158, v160, v78 op_sel_hi:[0,0,1]
	v_exp_f32_e32 v161, v161
	s_add_u32 s48, s48, s40
	v_add_f32_e32 v161, 1.0, v161
	v_rcp_f32_e32 v161, v161
	s_addc_u32 s49, s49, s41
	v_fma_f32 v162, v161, -2.0, 1.0
	v_sub_f32_e32 v163, v176, v162
	v_fma_f32 v176, v159, v163, v162
	v_fma_f32 v164, |v176|, s17, v113
	v_fma_f32 v165, |v176|, s18, v114
	v_fma_f32 v166, |v176|, s19, v115
	v_lshrrev_b32_e32 v167, 26, v176
	v_min3_u32 v164, v164, v165, v166
	v_bfi_b32 v168, 31, v164, v167
	s_nop 1
	v_mul_u32_u24_dpp v170, v168, v180 quad_perm:[1,2,3,3] row_mask:0xf bank_mask:0xf bound_ctrl:1
	v_mad_u32_u24 v171, v168, v181, v170
	ds_write_b8_d16_hi v184, v171 offset:416
	global_store_short_d16_hi v185, v176, s[48:49]
	s_waitcnt lgkmcnt(0)
	s_barrier
	ds_read_b64 v[122:123], v105 offset:416
	ds_read_b64 v[124:125], v105 offset:424
	ds_read_b64 v[126:127], v105 offset:432
	s_barrier
	ds_read_b64 v[128:129], v105 offset:512
	ds_read_b64 v[130:131], v105 offset:520
	ds_read_b64 v[132:133], v105 offset:528
	s_waitcnt lgkmcnt(3)
	v_mfma_f32_16x16x128_f8f6f4 v[134:137], v[122:127], v[2:7], 0 cbsz:2 blgp:2
	v_mfma_f32_16x16x128_f8f6f4 v[138:141], v[122:127], v[14:19], 0 cbsz:2 blgp:2
	v_mfma_f32_16x16x128_f8f6f4 v[142:145], v[122:127], v[26:31], v[188:191] cbsz:2 blgp:2
	v_mfma_f32_16x16x128_f8f6f4 v[204:207], v[122:127], v[38:43], 0 cbsz:2 blgp:2
	v_mfma_f32_16x16x128_f8f6f4 v[208:211], v[122:127], v[50:55], 0 cbsz:2 blgp:2
	v_mfma_f32_16x16x128_f8f6f4 v[212:215], v[122:127], v[62:67], v[188:191] cbsz:2 blgp:2
	s_waitcnt lgkmcnt(0)
	v_mfma_f32_16x16x128_f8f6f4 v[134:137], v[128:133], v[8:13], v[134:137] cbsz:2 blgp:2
	v_mfma_f32_16x16x128_f8f6f4 v[204:207], v[128:133], v[44:49], v[204:207] cbsz:2 blgp:2
	v_mfma_f32_16x16x128_f8f6f4 v[138:141], v[128:133], v[20:25], v[138:141] cbsz:2 blgp:2
	v_mfma_f32_16x16x128_f8f6f4 v[208:211], v[128:133], v[56:61], v[208:211] cbsz:2 blgp:2
	v_mfma_f32_16x16x128_f8f6f4 v[142:145], v[128:133], v[32:37], v[142:145] cbsz:2 blgp:2
	v_mfma_f32_16x16x128_f8f6f4 v[212:215], v[128:133], v[68:73], v[212:215] cbsz:2 blgp:2
	v_cndmask_b32_e64 v158, v134, v204, s[0:1]
	v_cndmask_b32_e64 v159, v138, v208, s[0:1]
	v_fma_mix_f32 v158, v158, v100, v82 op_sel:[0,0,1] op_sel_hi:[0,0,1]
	v_fma_mix_f32 v159, v159, v101, v74 op_sel:[0,0,1] op_sel_hi:[0,0,1]
	v_exp_f32_e32 v158, v158
	v_exp_f32_e32 v159, v159
	v_fma_f32 v158, v158, v186, v186
	v_add_f32_e32 v159, 1.0, v159
	v_rcp_f32_e32 v158, v158
	v_rcp_f32_e32 v159, v159
	v_cndmask_b32_e64 v160, v142, v212, s[0:1]
	v_fma_mix_f32 v161, v158, v160, v78 op_sel:[0,0,1] op_sel_hi:[0,0,1]
	v_exp_f32_e32 v161, v161
	s_add_u32 s48, s48, s40
	v_add_f32_e32 v161, 1.0, v161
	v_rcp_f32_e32 v161, v161
	s_addc_u32 s49, s49, s41
	v_fma_f32 v162, v161, -2.0, 1.0
	v_sub_f32_e32 v163, v176, v162
	v_fma_f32 v176, v159, v163, v162
	v_fma_f32 v164, |v176|, s17, v113
	v_fma_f32 v165, |v176|, s18, v114
	v_fma_f32 v166, |v176|, s19, v115
	v_lshrrev_b32_e32 v167, 26, v176
	v_min3_u32 v164, v164, v165, v166
	v_bfi_b32 v168, 31, v164, v167
	s_nop 1
	v_mul_u32_u24_dpp v170, v168, v180 quad_perm:[1,2,3,3] row_mask:0xf bank_mask:0xf bound_ctrl:1
	v_mad_u32_u24 v171, v168, v181, v170
	ds_write_b8_d16_hi v184, v171
	global_store_short_d16_hi v185, v176, s[48:49]
	s_waitcnt lgkmcnt(0)
	s_barrier
	ds_read_b64 v[122:123], v105 offset:0
	ds_read_b64 v[124:125], v105 offset:8
	ds_read_b64 v[126:127], v105 offset:16
	s_barrier
	ds_read_b64 v[128:129], v105 offset:96
	ds_read_b64 v[130:131], v105 offset:104
	ds_read_b64 v[132:133], v105 offset:112
	s_waitcnt lgkmcnt(3)
	v_mfma_f32_16x16x128_f8f6f4 v[134:137], v[122:127], v[2:7], 0 cbsz:2 blgp:2
	v_mfma_f32_16x16x128_f8f6f4 v[138:141], v[122:127], v[14:19], 0 cbsz:2 blgp:2
	v_mfma_f32_16x16x128_f8f6f4 v[142:145], v[122:127], v[26:31], v[188:191] cbsz:2 blgp:2
	v_mfma_f32_16x16x128_f8f6f4 v[204:207], v[122:127], v[38:43], 0 cbsz:2 blgp:2
	v_mfma_f32_16x16x128_f8f6f4 v[208:211], v[122:127], v[50:55], 0 cbsz:2 blgp:2
	v_mfma_f32_16x16x128_f8f6f4 v[212:215], v[122:127], v[62:67], v[188:191] cbsz:2 blgp:2
	s_waitcnt lgkmcnt(0)
	v_mfma_f32_16x16x128_f8f6f4 v[134:137], v[128:133], v[8:13], v[134:137] cbsz:2 blgp:2
	v_mfma_f32_16x16x128_f8f6f4 v[204:207], v[128:133], v[44:49], v[204:207] cbsz:2 blgp:2
	v_mfma_f32_16x16x128_f8f6f4 v[138:141], v[128:133], v[20:25], v[138:141] cbsz:2 blgp:2
	v_mfma_f32_16x16x128_f8f6f4 v[208:211], v[128:133], v[56:61], v[208:211] cbsz:2 blgp:2
	v_mfma_f32_16x16x128_f8f6f4 v[142:145], v[128:133], v[32:37], v[142:145] cbsz:2 blgp:2
	v_mfma_f32_16x16x128_f8f6f4 v[212:215], v[128:133], v[68:73], v[212:215] cbsz:2 blgp:2
	v_cndmask_b32_e64 v158, v134, v204, s[0:1]
	v_cndmask_b32_e64 v159, v138, v208, s[0:1]
	v_fma_mix_f32 v158, v158, v100, v83 op_sel_hi:[0,0,1]
	v_fma_mix_f32 v159, v159, v101, v75 op_sel_hi:[0,0,1]
	v_exp_f32_e32 v158, v158
	v_exp_f32_e32 v159, v159
	v_fma_f32 v158, v158, v186, v186
	v_add_f32_e32 v159, 1.0, v159
	v_rcp_f32_e32 v158, v158
	v_rcp_f32_e32 v159, v159
	v_cndmask_b32_e64 v160, v142, v212, s[0:1]
	v_fma_mix_f32 v161, v158, v160, v79 op_sel_hi:[0,0,1]
	v_exp_f32_e32 v161, v161
	s_add_u32 s48, s48, s40
	v_add_f32_e32 v161, 1.0, v161
	v_rcp_f32_e32 v161, v161
	s_addc_u32 s49, s49, s41
	v_fma_f32 v162, v161, -2.0, 1.0
	v_sub_f32_e32 v163, v176, v162
	v_fma_f32 v176, v159, v163, v162
	v_fma_f32 v164, |v176|, s17, v113
	v_fma_f32 v165, |v176|, s18, v114
	v_fma_f32 v166, |v176|, s19, v115
	v_lshrrev_b32_e32 v167, 26, v176
	v_min3_u32 v164, v164, v165, v166
	v_bfi_b32 v168, 31, v164, v167
	s_nop 1
	v_mul_u32_u24_dpp v170, v168, v180 quad_perm:[1,2,3,3] row_mask:0xf bank_mask:0xf bound_ctrl:1
	v_mad_u32_u24 v171, v168, v181, v170
	ds_write_b8_d16_hi v184, v171 offset:416
	global_store_short_d16_hi v185, v176, s[48:49]
	s_waitcnt lgkmcnt(0)
	s_barrier
	ds_read_b64 v[122:123], v105 offset:416
	ds_read_b64 v[124:125], v105 offset:424
	ds_read_b64 v[126:127], v105 offset:432
	s_barrier
	ds_read_b64 v[128:129], v105 offset:512
	ds_read_b64 v[130:131], v105 offset:520
	ds_read_b64 v[132:133], v105 offset:528
	s_waitcnt lgkmcnt(3)
	v_mfma_f32_16x16x128_f8f6f4 v[134:137], v[122:127], v[2:7], 0 cbsz:2 blgp:2
	v_mfma_f32_16x16x128_f8f6f4 v[138:141], v[122:127], v[14:19], 0 cbsz:2 blgp:2
	v_mfma_f32_16x16x128_f8f6f4 v[142:145], v[122:127], v[26:31], v[188:191] cbsz:2 blgp:2
	v_mfma_f32_16x16x128_f8f6f4 v[204:207], v[122:127], v[38:43], 0 cbsz:2 blgp:2
	v_mfma_f32_16x16x128_f8f6f4 v[208:211], v[122:127], v[50:55], 0 cbsz:2 blgp:2
	v_mfma_f32_16x16x128_f8f6f4 v[212:215], v[122:127], v[62:67], v[188:191] cbsz:2 blgp:2
	s_waitcnt lgkmcnt(0)
	v_mfma_f32_16x16x128_f8f6f4 v[134:137], v[128:133], v[8:13], v[134:137] cbsz:2 blgp:2
	v_mfma_f32_16x16x128_f8f6f4 v[204:207], v[128:133], v[44:49], v[204:207] cbsz:2 blgp:2
	v_mfma_f32_16x16x128_f8f6f4 v[138:141], v[128:133], v[20:25], v[138:141] cbsz:2 blgp:2
	v_mfma_f32_16x16x128_f8f6f4 v[208:211], v[128:133], v[56:61], v[208:211] cbsz:2 blgp:2
	v_mfma_f32_16x16x128_f8f6f4 v[142:145], v[128:133], v[32:37], v[142:145] cbsz:2 blgp:2
	v_mfma_f32_16x16x128_f8f6f4 v[212:215], v[128:133], v[68:73], v[212:215] cbsz:2 blgp:2
	v_cndmask_b32_e64 v158, v134, v204, s[0:1]
	v_cndmask_b32_e64 v159, v138, v208, s[0:1]
	v_fma_mix_f32 v158, v158, v100, v83 op_sel:[0,0,1] op_sel_hi:[0,0,1]
	v_fma_mix_f32 v159, v159, v101, v75 op_sel:[0,0,1] op_sel_hi:[0,0,1]
	v_exp_f32_e32 v158, v158
	v_exp_f32_e32 v159, v159
	v_fma_f32 v158, v158, v186, v186
	v_add_f32_e32 v159, 1.0, v159
	v_rcp_f32_e32 v158, v158
	v_rcp_f32_e32 v159, v159
	v_cndmask_b32_e64 v160, v142, v212, s[0:1]
	v_fma_mix_f32 v161, v158, v160, v79 op_sel:[0,0,1] op_sel_hi:[0,0,1]
	v_exp_f32_e32 v161, v161
	s_add_u32 s48, s48, s40
	v_add_f32_e32 v161, 1.0, v161
	v_rcp_f32_e32 v161, v161
	s_addc_u32 s49, s49, s41
	v_fma_f32 v162, v161, -2.0, 1.0
	v_sub_f32_e32 v163, v176, v162
	v_fma_f32 v176, v159, v163, v162
	v_fma_f32 v164, |v176|, s17, v113
	v_fma_f32 v165, |v176|, s18, v114
	v_fma_f32 v166, |v176|, s19, v115
	v_lshrrev_b32_e32 v167, 26, v176
	v_min3_u32 v164, v164, v165, v166
	v_bfi_b32 v168, 31, v164, v167
	s_nop 1
	v_mul_u32_u24_dpp v170, v168, v180 quad_perm:[1,2,3,3] row_mask:0xf bank_mask:0xf bound_ctrl:1
	v_mad_u32_u24 v171, v168, v181, v170
	ds_write_b8_d16_hi v184, v171
	global_store_short_d16_hi v185, v176, s[48:49]
	s_waitcnt lgkmcnt(0)
	s_barrier
	ds_read_b64 v[122:123], v105 offset:0
	ds_read_b64 v[124:125], v105 offset:8
	ds_read_b64 v[126:127], v105 offset:16
	s_barrier
	ds_read_b64 v[128:129], v105 offset:96
	ds_read_b64 v[130:131], v105 offset:104
	ds_read_b64 v[132:133], v105 offset:112
	s_waitcnt lgkmcnt(3)
	v_mfma_f32_16x16x128_f8f6f4 v[134:137], v[122:127], v[2:7], 0 cbsz:2 blgp:2
	v_mfma_f32_16x16x128_f8f6f4 v[138:141], v[122:127], v[14:19], 0 cbsz:2 blgp:2
	v_mfma_f32_16x16x128_f8f6f4 v[142:145], v[122:127], v[26:31], v[188:191] cbsz:2 blgp:2
	v_mfma_f32_16x16x128_f8f6f4 v[204:207], v[122:127], v[38:43], 0 cbsz:2 blgp:2
	v_mfma_f32_16x16x128_f8f6f4 v[208:211], v[122:127], v[50:55], 0 cbsz:2 blgp:2
	v_mfma_f32_16x16x128_f8f6f4 v[212:215], v[122:127], v[62:67], v[188:191] cbsz:2 blgp:2
	s_waitcnt lgkmcnt(0)
	v_mfma_f32_16x16x128_f8f6f4 v[134:137], v[128:133], v[8:13], v[134:137] cbsz:2 blgp:2
	v_mfma_f32_16x16x128_f8f6f4 v[204:207], v[128:133], v[44:49], v[204:207] cbsz:2 blgp:2
	v_mfma_f32_16x16x128_f8f6f4 v[138:141], v[128:133], v[20:25], v[138:141] cbsz:2 blgp:2
	v_mfma_f32_16x16x128_f8f6f4 v[208:211], v[128:133], v[56:61], v[208:211] cbsz:2 blgp:2
	v_mfma_f32_16x16x128_f8f6f4 v[142:145], v[128:133], v[32:37], v[142:145] cbsz:2 blgp:2
	v_mfma_f32_16x16x128_f8f6f4 v[212:215], v[128:133], v[68:73], v[212:215] cbsz:2 blgp:2
	v_cndmask_b32_e64 v158, v134, v204, s[0:1]
	v_cndmask_b32_e64 v159, v138, v208, s[0:1]
	v_fma_mix_f32 v158, v158, v100, v84 op_sel_hi:[0,0,1]
	v_fma_mix_f32 v159, v159, v101, v76 op_sel_hi:[0,0,1]
	v_exp_f32_e32 v158, v158
	v_exp_f32_e32 v159, v159
	v_fma_f32 v158, v158, v186, v186
	v_add_f32_e32 v159, 1.0, v159
	v_rcp_f32_e32 v158, v158
	v_rcp_f32_e32 v159, v159
	v_cndmask_b32_e64 v160, v142, v212, s[0:1]
	v_fma_mix_f32 v161, v158, v160, v80 op_sel_hi:[0,0,1]
	v_exp_f32_e32 v161, v161
	s_add_u32 s48, s48, s40
	v_add_f32_e32 v161, 1.0, v161
	v_rcp_f32_e32 v161, v161
	s_addc_u32 s49, s49, s41
	v_fma_f32 v162, v161, -2.0, 1.0
	v_sub_f32_e32 v163, v176, v162
	v_fma_f32 v176, v159, v163, v162
	v_fma_f32 v164, |v176|, s17, v113
	v_fma_f32 v165, |v176|, s18, v114
	v_fma_f32 v166, |v176|, s19, v115
	v_lshrrev_b32_e32 v167, 26, v176
	v_min3_u32 v164, v164, v165, v166
	v_bfi_b32 v168, 31, v164, v167
	s_nop 1
	v_mul_u32_u24_dpp v170, v168, v180 quad_perm:[1,2,3,3] row_mask:0xf bank_mask:0xf bound_ctrl:1
	v_mad_u32_u24 v171, v168, v181, v170
	ds_write_b8_d16_hi v184, v171 offset:416
	global_store_short_d16_hi v185, v176, s[48:49]
	s_waitcnt lgkmcnt(0)
	s_barrier
	ds_read_b64 v[122:123], v105 offset:416
	ds_read_b64 v[124:125], v105 offset:424
	ds_read_b64 v[126:127], v105 offset:432
	s_barrier
	ds_read_b64 v[128:129], v105 offset:512
	ds_read_b64 v[130:131], v105 offset:520
	ds_read_b64 v[132:133], v105 offset:528
	s_waitcnt lgkmcnt(3)
	v_mfma_f32_16x16x128_f8f6f4 v[134:137], v[122:127], v[2:7], 0 cbsz:2 blgp:2
	v_mfma_f32_16x16x128_f8f6f4 v[138:141], v[122:127], v[14:19], 0 cbsz:2 blgp:2
	v_mfma_f32_16x16x128_f8f6f4 v[142:145], v[122:127], v[26:31], v[188:191] cbsz:2 blgp:2
	v_mfma_f32_16x16x128_f8f6f4 v[204:207], v[122:127], v[38:43], 0 cbsz:2 blgp:2
	v_mfma_f32_16x16x128_f8f6f4 v[208:211], v[122:127], v[50:55], 0 cbsz:2 blgp:2
	v_mfma_f32_16x16x128_f8f6f4 v[212:215], v[122:127], v[62:67], v[188:191] cbsz:2 blgp:2
	s_waitcnt lgkmcnt(0)
	v_mfma_f32_16x16x128_f8f6f4 v[134:137], v[128:133], v[8:13], v[134:137] cbsz:2 blgp:2
	v_mfma_f32_16x16x128_f8f6f4 v[204:207], v[128:133], v[44:49], v[204:207] cbsz:2 blgp:2
	v_mfma_f32_16x16x128_f8f6f4 v[138:141], v[128:133], v[20:25], v[138:141] cbsz:2 blgp:2
	v_mfma_f32_16x16x128_f8f6f4 v[208:211], v[128:133], v[56:61], v[208:211] cbsz:2 blgp:2
	v_mfma_f32_16x16x128_f8f6f4 v[142:145], v[128:133], v[32:37], v[142:145] cbsz:2 blgp:2
	v_mfma_f32_16x16x128_f8f6f4 v[212:215], v[128:133], v[68:73], v[212:215] cbsz:2 blgp:2
	v_cndmask_b32_e64 v158, v134, v204, s[0:1]
	v_cndmask_b32_e64 v159, v138, v208, s[0:1]
	v_fma_mix_f32 v158, v158, v100, v84 op_sel:[0,0,1] op_sel_hi:[0,0,1]
	v_fma_mix_f32 v159, v159, v101, v76 op_sel:[0,0,1] op_sel_hi:[0,0,1]
	v_exp_f32_e32 v158, v158
	v_exp_f32_e32 v159, v159
	v_fma_f32 v158, v158, v186, v186
	v_add_f32_e32 v159, 1.0, v159
	v_rcp_f32_e32 v158, v158
	v_rcp_f32_e32 v159, v159
	v_cndmask_b32_e64 v160, v142, v212, s[0:1]
	v_fma_mix_f32 v161, v158, v160, v80 op_sel:[0,0,1] op_sel_hi:[0,0,1]
	v_exp_f32_e32 v161, v161
	s_add_u32 s48, s48, s40
	v_add_f32_e32 v161, 1.0, v161
	v_rcp_f32_e32 v161, v161
	s_addc_u32 s49, s49, s41
	v_fma_f32 v162, v161, -2.0, 1.0
	v_sub_f32_e32 v163, v176, v162
	v_fma_f32 v176, v159, v163, v162
	v_fma_f32 v164, |v176|, s17, v113
	v_fma_f32 v165, |v176|, s18, v114
	v_fma_f32 v166, |v176|, s19, v115
	v_lshrrev_b32_e32 v167, 26, v176
	v_min3_u32 v164, v164, v165, v166
	v_bfi_b32 v168, 31, v164, v167
	s_nop 1
	v_mul_u32_u24_dpp v170, v168, v180 quad_perm:[1,2,3,3] row_mask:0xf bank_mask:0xf bound_ctrl:1
	v_mad_u32_u24 v171, v168, v181, v170
	ds_write_b8_d16_hi v184, v171
	global_store_short_d16_hi v185, v176, s[48:49]
	s_waitcnt lgkmcnt(0)
	s_barrier
	ds_read_b64 v[122:123], v105 offset:0
	ds_read_b64 v[124:125], v105 offset:8
	ds_read_b64 v[126:127], v105 offset:16
	s_barrier
	ds_read_b64 v[128:129], v105 offset:96
	ds_read_b64 v[130:131], v105 offset:104
	ds_read_b64 v[132:133], v105 offset:112
	s_waitcnt lgkmcnt(3)
	v_mfma_f32_16x16x128_f8f6f4 v[134:137], v[122:127], v[2:7], 0 cbsz:2 blgp:2
	v_mfma_f32_16x16x128_f8f6f4 v[138:141], v[122:127], v[14:19], 0 cbsz:2 blgp:2
	v_mfma_f32_16x16x128_f8f6f4 v[142:145], v[122:127], v[26:31], v[188:191] cbsz:2 blgp:2
	v_mfma_f32_16x16x128_f8f6f4 v[204:207], v[122:127], v[38:43], 0 cbsz:2 blgp:2
	v_mfma_f32_16x16x128_f8f6f4 v[208:211], v[122:127], v[50:55], 0 cbsz:2 blgp:2
	v_mfma_f32_16x16x128_f8f6f4 v[212:215], v[122:127], v[62:67], v[188:191] cbsz:2 blgp:2
	s_waitcnt lgkmcnt(0)
	v_mfma_f32_16x16x128_f8f6f4 v[134:137], v[128:133], v[8:13], v[134:137] cbsz:2 blgp:2
	v_mfma_f32_16x16x128_f8f6f4 v[204:207], v[128:133], v[44:49], v[204:207] cbsz:2 blgp:2
	v_mfma_f32_16x16x128_f8f6f4 v[138:141], v[128:133], v[20:25], v[138:141] cbsz:2 blgp:2
	v_mfma_f32_16x16x128_f8f6f4 v[208:211], v[128:133], v[56:61], v[208:211] cbsz:2 blgp:2
	v_mfma_f32_16x16x128_f8f6f4 v[142:145], v[128:133], v[32:37], v[142:145] cbsz:2 blgp:2
	v_mfma_f32_16x16x128_f8f6f4 v[212:215], v[128:133], v[68:73], v[212:215] cbsz:2 blgp:2
	v_cndmask_b32_e64 v158, v134, v204, s[0:1]
	v_cndmask_b32_e64 v159, v138, v208, s[0:1]
	v_fma_mix_f32 v158, v158, v100, v85 op_sel_hi:[0,0,1]
	v_fma_mix_f32 v159, v159, v101, v77 op_sel_hi:[0,0,1]
	v_exp_f32_e32 v158, v158
	v_exp_f32_e32 v159, v159
	v_fma_f32 v158, v158, v186, v186
	v_add_f32_e32 v159, 1.0, v159
	v_rcp_f32_e32 v158, v158
	v_rcp_f32_e32 v159, v159
	v_cndmask_b32_e64 v160, v142, v212, s[0:1]
	v_fma_mix_f32 v161, v158, v160, v81 op_sel_hi:[0,0,1]
	v_exp_f32_e32 v161, v161
	s_add_u32 s48, s48, s40
	v_add_f32_e32 v161, 1.0, v161
	v_rcp_f32_e32 v161, v161
	s_addc_u32 s49, s49, s41
	v_fma_f32 v162, v161, -2.0, 1.0
	v_sub_f32_e32 v163, v176, v162
	v_fma_f32 v176, v159, v163, v162
	v_fma_f32 v164, |v176|, s17, v113
	v_fma_f32 v165, |v176|, s18, v114
	v_fma_f32 v166, |v176|, s19, v115
	v_lshrrev_b32_e32 v167, 26, v176
	v_min3_u32 v164, v164, v165, v166
	v_bfi_b32 v168, 31, v164, v167
	s_nop 1
	v_mul_u32_u24_dpp v170, v168, v180 quad_perm:[1,2,3,3] row_mask:0xf bank_mask:0xf bound_ctrl:1
	v_mad_u32_u24 v171, v168, v181, v170
	ds_write_b8_d16_hi v184, v171 offset:416
	global_store_short_d16_hi v185, v176, s[48:49]
	s_waitcnt lgkmcnt(0)
	s_barrier
	ds_read_b64 v[122:123], v105 offset:416
	ds_read_b64 v[124:125], v105 offset:424
	ds_read_b64 v[126:127], v105 offset:432
	s_barrier
	ds_read_b64 v[128:129], v105 offset:512
	ds_read_b64 v[130:131], v105 offset:520
	ds_read_b64 v[132:133], v105 offset:528
	s_waitcnt lgkmcnt(3)
	v_mfma_f32_16x16x128_f8f6f4 v[134:137], v[122:127], v[2:7], 0 cbsz:2 blgp:2
	v_mfma_f32_16x16x128_f8f6f4 v[138:141], v[122:127], v[14:19], 0 cbsz:2 blgp:2
	v_mfma_f32_16x16x128_f8f6f4 v[142:145], v[122:127], v[26:31], v[188:191] cbsz:2 blgp:2
	v_mfma_f32_16x16x128_f8f6f4 v[204:207], v[122:127], v[38:43], 0 cbsz:2 blgp:2
	v_mfma_f32_16x16x128_f8f6f4 v[208:211], v[122:127], v[50:55], 0 cbsz:2 blgp:2
	v_mfma_f32_16x16x128_f8f6f4 v[212:215], v[122:127], v[62:67], v[188:191] cbsz:2 blgp:2
	s_waitcnt lgkmcnt(0)
	v_mfma_f32_16x16x128_f8f6f4 v[134:137], v[128:133], v[8:13], v[134:137] cbsz:2 blgp:2
	v_mfma_f32_16x16x128_f8f6f4 v[204:207], v[128:133], v[44:49], v[204:207] cbsz:2 blgp:2
	v_mfma_f32_16x16x128_f8f6f4 v[138:141], v[128:133], v[20:25], v[138:141] cbsz:2 blgp:2
	v_mfma_f32_16x16x128_f8f6f4 v[208:211], v[128:133], v[56:61], v[208:211] cbsz:2 blgp:2
	v_mfma_f32_16x16x128_f8f6f4 v[142:145], v[128:133], v[32:37], v[142:145] cbsz:2 blgp:2
	v_mfma_f32_16x16x128_f8f6f4 v[212:215], v[128:133], v[68:73], v[212:215] cbsz:2 blgp:2
	v_cndmask_b32_e64 v158, v134, v204, s[0:1]
	v_cndmask_b32_e64 v159, v138, v208, s[0:1]
	v_fma_mix_f32 v158, v158, v100, v85 op_sel:[0,0,1] op_sel_hi:[0,0,1]
	v_fma_mix_f32 v159, v159, v101, v77 op_sel:[0,0,1] op_sel_hi:[0,0,1]
	v_exp_f32_e32 v158, v158
	v_exp_f32_e32 v159, v159
	v_fma_f32 v158, v158, v186, v186
	v_add_f32_e32 v159, 1.0, v159
	v_rcp_f32_e32 v158, v158
	v_rcp_f32_e32 v159, v159
	v_cndmask_b32_e64 v160, v142, v212, s[0:1]
	v_fma_mix_f32 v161, v158, v160, v81 op_sel:[0,0,1] op_sel_hi:[0,0,1]
	v_exp_f32_e32 v161, v161
	s_add_u32 s48, s48, s40
	v_add_f32_e32 v161, 1.0, v161
	v_rcp_f32_e32 v161, v161
	s_addc_u32 s49, s49, s41
	v_fma_f32 v162, v161, -2.0, 1.0
	v_sub_f32_e32 v163, v176, v162
	v_fma_f32 v176, v159, v163, v162
	v_fma_f32 v164, |v176|, s17, v113
	v_fma_f32 v165, |v176|, s18, v114
	v_fma_f32 v166, |v176|, s19, v115
	v_lshrrev_b32_e32 v167, 26, v176
	v_min3_u32 v164, v164, v165, v166
	v_bfi_b32 v168, 31, v164, v167
	s_nop 1
	v_mul_u32_u24_dpp v170, v168, v180 quad_perm:[1,2,3,3] row_mask:0xf bank_mask:0xf bound_ctrl:1
	v_mad_u32_u24 v171, v168, v181, v170
	ds_write_b8_d16_hi v184, v171
	global_store_short_d16_hi v185, v176, s[48:49]
	s_waitcnt lgkmcnt(0)
	s_barrier
	ds_read_b64 v[122:123], v105 offset:0
	ds_read_b64 v[124:125], v105 offset:8
	ds_read_b64 v[126:127], v105 offset:16
	s_barrier
	ds_read_b64 v[128:129], v105 offset:96
	ds_read_b64 v[130:131], v105 offset:104
	ds_read_b64 v[132:133], v105 offset:112
	s_waitcnt vmcnt(8)
	global_load_dwordx4 v[82:85], v[196:197], off
	global_load_dwordx4 v[74:77], v[196:197], off offset:512
	global_load_dwordx4 v[78:81], v[196:197], off offset:1024
	v_lshl_add_u64 v[196:197], v[196:197], 0, s[42:43]
	s_waitcnt lgkmcnt(3)
	v_mfma_f32_16x16x128_f8f6f4 v[134:137], v[122:127], v[2:7], 0 cbsz:2 blgp:2
	v_mfma_f32_16x16x128_f8f6f4 v[138:141], v[122:127], v[14:19], 0 cbsz:2 blgp:2
	v_mfma_f32_16x16x128_f8f6f4 v[142:145], v[122:127], v[26:31], v[188:191] cbsz:2 blgp:2
	v_mfma_f32_16x16x128_f8f6f4 v[204:207], v[122:127], v[38:43], 0 cbsz:2 blgp:2
	v_mfma_f32_16x16x128_f8f6f4 v[208:211], v[122:127], v[50:55], 0 cbsz:2 blgp:2
	v_mfma_f32_16x16x128_f8f6f4 v[212:215], v[122:127], v[62:67], v[188:191] cbsz:2 blgp:2
	s_waitcnt lgkmcnt(0)
	v_mfma_f32_16x16x128_f8f6f4 v[134:137], v[128:133], v[8:13], v[134:137] cbsz:2 blgp:2
	v_mfma_f32_16x16x128_f8f6f4 v[204:207], v[128:133], v[44:49], v[204:207] cbsz:2 blgp:2
	v_mfma_f32_16x16x128_f8f6f4 v[138:141], v[128:133], v[20:25], v[138:141] cbsz:2 blgp:2
	v_mfma_f32_16x16x128_f8f6f4 v[208:211], v[128:133], v[56:61], v[208:211] cbsz:2 blgp:2
	v_mfma_f32_16x16x128_f8f6f4 v[142:145], v[128:133], v[32:37], v[142:145] cbsz:2 blgp:2
	v_mfma_f32_16x16x128_f8f6f4 v[212:215], v[128:133], v[68:73], v[212:215] cbsz:2 blgp:2
	v_cndmask_b32_e64 v158, v134, v204, s[0:1]
	v_cndmask_b32_e64 v159, v138, v208, s[0:1]
	v_fma_mix_f32 v158, v158, v100, v146 op_sel_hi:[0,0,1]
	v_fma_mix_f32 v159, v159, v101, v150 op_sel_hi:[0,0,1]
	v_exp_f32_e32 v158, v158
	v_exp_f32_e32 v159, v159
	v_fma_f32 v158, v158, v186, v186
	v_add_f32_e32 v159, 1.0, v159
	v_rcp_f32_e32 v158, v158
	v_rcp_f32_e32 v159, v159
	v_cndmask_b32_e64 v160, v142, v212, s[0:1]
	v_fma_mix_f32 v161, v158, v160, v154 op_sel_hi:[0,0,1]
	v_exp_f32_e32 v161, v161
	s_add_u32 s48, s48, s40
	v_add_f32_e32 v161, 1.0, v161
	v_rcp_f32_e32 v161, v161
	s_addc_u32 s49, s49, s41
	v_fma_f32 v162, v161, -2.0, 1.0
	v_sub_f32_e32 v163, v176, v162
	v_fma_f32 v176, v159, v163, v162
	v_fma_f32 v164, |v176|, s17, v113
	v_fma_f32 v165, |v176|, s18, v114
	v_fma_f32 v166, |v176|, s19, v115
	v_lshrrev_b32_e32 v167, 26, v176
	v_min3_u32 v164, v164, v165, v166
	v_bfi_b32 v168, 31, v164, v167
	s_nop 1
	v_mul_u32_u24_dpp v170, v168, v180 quad_perm:[1,2,3,3] row_mask:0xf bank_mask:0xf bound_ctrl:1
	v_mad_u32_u24 v171, v168, v181, v170
	ds_write_b8_d16_hi v184, v171 offset:416
	global_store_short_d16_hi v185, v176, s[48:49]
	s_waitcnt lgkmcnt(0)
	s_barrier
	ds_read_b64 v[122:123], v105 offset:416
	ds_read_b64 v[124:125], v105 offset:424
	ds_read_b64 v[126:127], v105 offset:432
	s_barrier
	ds_read_b64 v[128:129], v105 offset:512
	ds_read_b64 v[130:131], v105 offset:520
	ds_read_b64 v[132:133], v105 offset:528
	s_waitcnt lgkmcnt(3)
	v_mfma_f32_16x16x128_f8f6f4 v[134:137], v[122:127], v[2:7], 0 cbsz:2 blgp:2
	v_mfma_f32_16x16x128_f8f6f4 v[138:141], v[122:127], v[14:19], 0 cbsz:2 blgp:2
	v_mfma_f32_16x16x128_f8f6f4 v[142:145], v[122:127], v[26:31], v[188:191] cbsz:2 blgp:2
	v_mfma_f32_16x16x128_f8f6f4 v[204:207], v[122:127], v[38:43], 0 cbsz:2 blgp:2
	v_mfma_f32_16x16x128_f8f6f4 v[208:211], v[122:127], v[50:55], 0 cbsz:2 blgp:2
	v_mfma_f32_16x16x128_f8f6f4 v[212:215], v[122:127], v[62:67], v[188:191] cbsz:2 blgp:2
	s_waitcnt lgkmcnt(0)
	v_mfma_f32_16x16x128_f8f6f4 v[134:137], v[128:133], v[8:13], v[134:137] cbsz:2 blgp:2
	v_mfma_f32_16x16x128_f8f6f4 v[204:207], v[128:133], v[44:49], v[204:207] cbsz:2 blgp:2
	v_mfma_f32_16x16x128_f8f6f4 v[138:141], v[128:133], v[20:25], v[138:141] cbsz:2 blgp:2
	v_mfma_f32_16x16x128_f8f6f4 v[208:211], v[128:133], v[56:61], v[208:211] cbsz:2 blgp:2
	v_mfma_f32_16x16x128_f8f6f4 v[142:145], v[128:133], v[32:37], v[142:145] cbsz:2 blgp:2
	v_mfma_f32_16x16x128_f8f6f4 v[212:215], v[128:133], v[68:73], v[212:215] cbsz:2 blgp:2
	v_cndmask_b32_e64 v158, v134, v204, s[0:1]
	v_cndmask_b32_e64 v159, v138, v208, s[0:1]
	v_fma_mix_f32 v158, v158, v100, v146 op_sel:[0,0,1] op_sel_hi:[0,0,1]
	v_fma_mix_f32 v159, v159, v101, v150 op_sel:[0,0,1] op_sel_hi:[0,0,1]
	v_exp_f32_e32 v158, v158
	v_exp_f32_e32 v159, v159
	v_fma_f32 v158, v158, v186, v186
	v_add_f32_e32 v159, 1.0, v159
	v_rcp_f32_e32 v158, v158
	v_rcp_f32_e32 v159, v159
	v_cndmask_b32_e64 v160, v142, v212, s[0:1]
	v_fma_mix_f32 v161, v158, v160, v154 op_sel:[0,0,1] op_sel_hi:[0,0,1]
	v_exp_f32_e32 v161, v161
	s_add_u32 s48, s48, s40
	v_add_f32_e32 v161, 1.0, v161
	v_rcp_f32_e32 v161, v161
	s_addc_u32 s49, s49, s41
	v_fma_f32 v162, v161, -2.0, 1.0
	v_sub_f32_e32 v163, v176, v162
	v_fma_f32 v176, v159, v163, v162
	v_fma_f32 v164, |v176|, s17, v113
	v_fma_f32 v165, |v176|, s18, v114
	v_fma_f32 v166, |v176|, s19, v115
	v_lshrrev_b32_e32 v167, 26, v176
	v_min3_u32 v164, v164, v165, v166
	v_bfi_b32 v168, 31, v164, v167
	s_nop 1
	v_mul_u32_u24_dpp v170, v168, v180 quad_perm:[1,2,3,3] row_mask:0xf bank_mask:0xf bound_ctrl:1
	v_mad_u32_u24 v171, v168, v181, v170
	ds_write_b8_d16_hi v184, v171
	global_store_short_d16_hi v185, v176, s[48:49]
	s_waitcnt lgkmcnt(0)
	s_barrier
	ds_read_b64 v[122:123], v105 offset:0
	ds_read_b64 v[124:125], v105 offset:8
	ds_read_b64 v[126:127], v105 offset:16
	s_barrier
	ds_read_b64 v[128:129], v105 offset:96
	ds_read_b64 v[130:131], v105 offset:104
	ds_read_b64 v[132:133], v105 offset:112
	s_waitcnt lgkmcnt(3)
	v_mfma_f32_16x16x128_f8f6f4 v[134:137], v[122:127], v[2:7], 0 cbsz:2 blgp:2
	v_mfma_f32_16x16x128_f8f6f4 v[138:141], v[122:127], v[14:19], 0 cbsz:2 blgp:2
	v_mfma_f32_16x16x128_f8f6f4 v[142:145], v[122:127], v[26:31], v[188:191] cbsz:2 blgp:2
	v_mfma_f32_16x16x128_f8f6f4 v[204:207], v[122:127], v[38:43], 0 cbsz:2 blgp:2
	v_mfma_f32_16x16x128_f8f6f4 v[208:211], v[122:127], v[50:55], 0 cbsz:2 blgp:2
	v_mfma_f32_16x16x128_f8f6f4 v[212:215], v[122:127], v[62:67], v[188:191] cbsz:2 blgp:2
	s_waitcnt lgkmcnt(0)
	v_mfma_f32_16x16x128_f8f6f4 v[134:137], v[128:133], v[8:13], v[134:137] cbsz:2 blgp:2
	v_mfma_f32_16x16x128_f8f6f4 v[204:207], v[128:133], v[44:49], v[204:207] cbsz:2 blgp:2
	v_mfma_f32_16x16x128_f8f6f4 v[138:141], v[128:133], v[20:25], v[138:141] cbsz:2 blgp:2
	v_mfma_f32_16x16x128_f8f6f4 v[208:211], v[128:133], v[56:61], v[208:211] cbsz:2 blgp:2
	v_mfma_f32_16x16x128_f8f6f4 v[142:145], v[128:133], v[32:37], v[142:145] cbsz:2 blgp:2
	v_mfma_f32_16x16x128_f8f6f4 v[212:215], v[128:133], v[68:73], v[212:215] cbsz:2 blgp:2
	v_cndmask_b32_e64 v158, v134, v204, s[0:1]
	v_cndmask_b32_e64 v159, v138, v208, s[0:1]
	v_fma_mix_f32 v158, v158, v100, v147 op_sel_hi:[0,0,1]
	v_fma_mix_f32 v159, v159, v101, v151 op_sel_hi:[0,0,1]
	v_exp_f32_e32 v158, v158
	v_exp_f32_e32 v159, v159
	v_fma_f32 v158, v158, v186, v186
	v_add_f32_e32 v159, 1.0, v159
	v_rcp_f32_e32 v158, v158
	v_rcp_f32_e32 v159, v159
	v_cndmask_b32_e64 v160, v142, v212, s[0:1]
	v_fma_mix_f32 v161, v158, v160, v155 op_sel_hi:[0,0,1]
	v_exp_f32_e32 v161, v161
	s_add_u32 s48, s48, s40
	v_add_f32_e32 v161, 1.0, v161
	v_rcp_f32_e32 v161, v161
	s_addc_u32 s49, s49, s41
	v_fma_f32 v162, v161, -2.0, 1.0
	v_sub_f32_e32 v163, v176, v162
	v_fma_f32 v176, v159, v163, v162
	v_fma_f32 v164, |v176|, s17, v113
	v_fma_f32 v165, |v176|, s18, v114
	v_fma_f32 v166, |v176|, s19, v115
	v_lshrrev_b32_e32 v167, 26, v176
	v_min3_u32 v164, v164, v165, v166
	v_bfi_b32 v168, 31, v164, v167
	s_nop 1
	v_mul_u32_u24_dpp v170, v168, v180 quad_perm:[1,2,3,3] row_mask:0xf bank_mask:0xf bound_ctrl:1
	v_mad_u32_u24 v171, v168, v181, v170
	ds_write_b8_d16_hi v184, v171 offset:416
	global_store_short_d16_hi v185, v176, s[48:49]
	s_waitcnt lgkmcnt(0)
	s_barrier
	ds_read_b64 v[122:123], v105 offset:416
	ds_read_b64 v[124:125], v105 offset:424
	ds_read_b64 v[126:127], v105 offset:432
	s_barrier
	ds_read_b64 v[128:129], v105 offset:512
	ds_read_b64 v[130:131], v105 offset:520
	ds_read_b64 v[132:133], v105 offset:528
	s_waitcnt lgkmcnt(3)
	v_mfma_f32_16x16x128_f8f6f4 v[134:137], v[122:127], v[2:7], 0 cbsz:2 blgp:2
	v_mfma_f32_16x16x128_f8f6f4 v[138:141], v[122:127], v[14:19], 0 cbsz:2 blgp:2
	v_mfma_f32_16x16x128_f8f6f4 v[142:145], v[122:127], v[26:31], v[188:191] cbsz:2 blgp:2
	v_mfma_f32_16x16x128_f8f6f4 v[204:207], v[122:127], v[38:43], 0 cbsz:2 blgp:2
	v_mfma_f32_16x16x128_f8f6f4 v[208:211], v[122:127], v[50:55], 0 cbsz:2 blgp:2
	v_mfma_f32_16x16x128_f8f6f4 v[212:215], v[122:127], v[62:67], v[188:191] cbsz:2 blgp:2
	s_waitcnt lgkmcnt(0)
	v_mfma_f32_16x16x128_f8f6f4 v[134:137], v[128:133], v[8:13], v[134:137] cbsz:2 blgp:2
	v_mfma_f32_16x16x128_f8f6f4 v[204:207], v[128:133], v[44:49], v[204:207] cbsz:2 blgp:2
	v_mfma_f32_16x16x128_f8f6f4 v[138:141], v[128:133], v[20:25], v[138:141] cbsz:2 blgp:2
	v_mfma_f32_16x16x128_f8f6f4 v[208:211], v[128:133], v[56:61], v[208:211] cbsz:2 blgp:2
	v_mfma_f32_16x16x128_f8f6f4 v[142:145], v[128:133], v[32:37], v[142:145] cbsz:2 blgp:2
	v_mfma_f32_16x16x128_f8f6f4 v[212:215], v[128:133], v[68:73], v[212:215] cbsz:2 blgp:2
	v_cndmask_b32_e64 v158, v134, v204, s[0:1]
	v_cndmask_b32_e64 v159, v138, v208, s[0:1]
	v_fma_mix_f32 v158, v158, v100, v147 op_sel:[0,0,1] op_sel_hi:[0,0,1]
	v_fma_mix_f32 v159, v159, v101, v151 op_sel:[0,0,1] op_sel_hi:[0,0,1]
	v_exp_f32_e32 v158, v158
	v_exp_f32_e32 v159, v159
	v_fma_f32 v158, v158, v186, v186
	v_add_f32_e32 v159, 1.0, v159
	v_rcp_f32_e32 v158, v158
	v_rcp_f32_e32 v159, v159
	v_cndmask_b32_e64 v160, v142, v212, s[0:1]
	v_fma_mix_f32 v161, v158, v160, v155 op_sel:[0,0,1] op_sel_hi:[0,0,1]
	v_exp_f32_e32 v161, v161
	s_add_u32 s48, s48, s40
	v_add_f32_e32 v161, 1.0, v161
	v_rcp_f32_e32 v161, v161
	s_addc_u32 s49, s49, s41
	v_fma_f32 v162, v161, -2.0, 1.0
	v_sub_f32_e32 v163, v176, v162
	v_fma_f32 v176, v159, v163, v162
	v_fma_f32 v164, |v176|, s17, v113
	v_fma_f32 v165, |v176|, s18, v114
	v_fma_f32 v166, |v176|, s19, v115
	v_lshrrev_b32_e32 v167, 26, v176
	v_min3_u32 v164, v164, v165, v166
	v_bfi_b32 v168, 31, v164, v167
	s_nop 1
	v_mul_u32_u24_dpp v170, v168, v180 quad_perm:[1,2,3,3] row_mask:0xf bank_mask:0xf bound_ctrl:1
	v_mad_u32_u24 v171, v168, v181, v170
	ds_write_b8_d16_hi v184, v171
	global_store_short_d16_hi v185, v176, s[48:49]
	s_waitcnt lgkmcnt(0)
	s_barrier
	ds_read_b64 v[122:123], v105 offset:0
	ds_read_b64 v[124:125], v105 offset:8
	ds_read_b64 v[126:127], v105 offset:16
	s_barrier
	ds_read_b64 v[128:129], v105 offset:96
	ds_read_b64 v[130:131], v105 offset:104
	ds_read_b64 v[132:133], v105 offset:112
	s_waitcnt lgkmcnt(3)
	v_mfma_f32_16x16x128_f8f6f4 v[134:137], v[122:127], v[2:7], 0 cbsz:2 blgp:2
	v_mfma_f32_16x16x128_f8f6f4 v[138:141], v[122:127], v[14:19], 0 cbsz:2 blgp:2
	v_mfma_f32_16x16x128_f8f6f4 v[142:145], v[122:127], v[26:31], v[188:191] cbsz:2 blgp:2
	v_mfma_f32_16x16x128_f8f6f4 v[204:207], v[122:127], v[38:43], 0 cbsz:2 blgp:2
	v_mfma_f32_16x16x128_f8f6f4 v[208:211], v[122:127], v[50:55], 0 cbsz:2 blgp:2
	v_mfma_f32_16x16x128_f8f6f4 v[212:215], v[122:127], v[62:67], v[188:191] cbsz:2 blgp:2
	s_waitcnt lgkmcnt(0)
	v_mfma_f32_16x16x128_f8f6f4 v[134:137], v[128:133], v[8:13], v[134:137] cbsz:2 blgp:2
	v_mfma_f32_16x16x128_f8f6f4 v[204:207], v[128:133], v[44:49], v[204:207] cbsz:2 blgp:2
	v_mfma_f32_16x16x128_f8f6f4 v[138:141], v[128:133], v[20:25], v[138:141] cbsz:2 blgp:2
	v_mfma_f32_16x16x128_f8f6f4 v[208:211], v[128:133], v[56:61], v[208:211] cbsz:2 blgp:2
	v_mfma_f32_16x16x128_f8f6f4 v[142:145], v[128:133], v[32:37], v[142:145] cbsz:2 blgp:2
	v_mfma_f32_16x16x128_f8f6f4 v[212:215], v[128:133], v[68:73], v[212:215] cbsz:2 blgp:2
	v_cndmask_b32_e64 v158, v134, v204, s[0:1]
	v_cndmask_b32_e64 v159, v138, v208, s[0:1]
	v_fma_mix_f32 v158, v158, v100, v148 op_sel_hi:[0,0,1]
	v_fma_mix_f32 v159, v159, v101, v152 op_sel_hi:[0,0,1]
	v_exp_f32_e32 v158, v158
	v_exp_f32_e32 v159, v159
	v_fma_f32 v158, v158, v186, v186
	v_add_f32_e32 v159, 1.0, v159
	v_rcp_f32_e32 v158, v158
	v_rcp_f32_e32 v159, v159
	v_cndmask_b32_e64 v160, v142, v212, s[0:1]
	v_fma_mix_f32 v161, v158, v160, v156 op_sel_hi:[0,0,1]
	v_exp_f32_e32 v161, v161
	s_add_u32 s48, s48, s40
	v_add_f32_e32 v161, 1.0, v161
	v_rcp_f32_e32 v161, v161
	s_addc_u32 s49, s49, s41
	v_fma_f32 v162, v161, -2.0, 1.0
	v_sub_f32_e32 v163, v176, v162
	v_fma_f32 v176, v159, v163, v162
	v_fma_f32 v164, |v176|, s17, v113
	v_fma_f32 v165, |v176|, s18, v114
	v_fma_f32 v166, |v176|, s19, v115
	v_lshrrev_b32_e32 v167, 26, v176
	v_min3_u32 v164, v164, v165, v166
	v_bfi_b32 v168, 31, v164, v167
	s_nop 1
	v_mul_u32_u24_dpp v170, v168, v180 quad_perm:[1,2,3,3] row_mask:0xf bank_mask:0xf bound_ctrl:1
	v_mad_u32_u24 v171, v168, v181, v170
	ds_write_b8_d16_hi v184, v171 offset:416
	global_store_short_d16_hi v185, v176, s[48:49]
	s_waitcnt lgkmcnt(0)
	s_barrier
	ds_read_b64 v[122:123], v105 offset:416
	ds_read_b64 v[124:125], v105 offset:424
	ds_read_b64 v[126:127], v105 offset:432
	s_barrier
	ds_read_b64 v[128:129], v105 offset:512
	ds_read_b64 v[130:131], v105 offset:520
	ds_read_b64 v[132:133], v105 offset:528
	s_waitcnt lgkmcnt(3)
	v_mfma_f32_16x16x128_f8f6f4 v[134:137], v[122:127], v[2:7], 0 cbsz:2 blgp:2
	v_mfma_f32_16x16x128_f8f6f4 v[138:141], v[122:127], v[14:19], 0 cbsz:2 blgp:2
	v_mfma_f32_16x16x128_f8f6f4 v[142:145], v[122:127], v[26:31], v[188:191] cbsz:2 blgp:2
	v_mfma_f32_16x16x128_f8f6f4 v[204:207], v[122:127], v[38:43], 0 cbsz:2 blgp:2
	v_mfma_f32_16x16x128_f8f6f4 v[208:211], v[122:127], v[50:55], 0 cbsz:2 blgp:2
	v_mfma_f32_16x16x128_f8f6f4 v[212:215], v[122:127], v[62:67], v[188:191] cbsz:2 blgp:2
	s_waitcnt lgkmcnt(0)
	v_mfma_f32_16x16x128_f8f6f4 v[134:137], v[128:133], v[8:13], v[134:137] cbsz:2 blgp:2
	v_mfma_f32_16x16x128_f8f6f4 v[204:207], v[128:133], v[44:49], v[204:207] cbsz:2 blgp:2
	v_mfma_f32_16x16x128_f8f6f4 v[138:141], v[128:133], v[20:25], v[138:141] cbsz:2 blgp:2
	v_mfma_f32_16x16x128_f8f6f4 v[208:211], v[128:133], v[56:61], v[208:211] cbsz:2 blgp:2
	v_mfma_f32_16x16x128_f8f6f4 v[142:145], v[128:133], v[32:37], v[142:145] cbsz:2 blgp:2
	v_mfma_f32_16x16x128_f8f6f4 v[212:215], v[128:133], v[68:73], v[212:215] cbsz:2 blgp:2
	v_cndmask_b32_e64 v158, v134, v204, s[0:1]
	v_cndmask_b32_e64 v159, v138, v208, s[0:1]
	v_fma_mix_f32 v158, v158, v100, v148 op_sel:[0,0,1] op_sel_hi:[0,0,1]
	v_fma_mix_f32 v159, v159, v101, v152 op_sel:[0,0,1] op_sel_hi:[0,0,1]
	v_exp_f32_e32 v158, v158
	v_exp_f32_e32 v159, v159
	v_fma_f32 v158, v158, v186, v186
	v_add_f32_e32 v159, 1.0, v159
	v_rcp_f32_e32 v158, v158
	v_rcp_f32_e32 v159, v159
	v_cndmask_b32_e64 v160, v142, v212, s[0:1]
	v_fma_mix_f32 v161, v158, v160, v156 op_sel:[0,0,1] op_sel_hi:[0,0,1]
	v_exp_f32_e32 v161, v161
	s_add_u32 s48, s48, s40
	v_add_f32_e32 v161, 1.0, v161
	v_rcp_f32_e32 v161, v161
	s_addc_u32 s49, s49, s41
	v_fma_f32 v162, v161, -2.0, 1.0
	v_sub_f32_e32 v163, v176, v162
	v_fma_f32 v176, v159, v163, v162
	v_fma_f32 v164, |v176|, s17, v113
	v_fma_f32 v165, |v176|, s18, v114
	v_fma_f32 v166, |v176|, s19, v115
	v_lshrrev_b32_e32 v167, 26, v176
	v_min3_u32 v164, v164, v165, v166
	v_bfi_b32 v168, 31, v164, v167
	s_nop 1
	v_mul_u32_u24_dpp v170, v168, v180 quad_perm:[1,2,3,3] row_mask:0xf bank_mask:0xf bound_ctrl:1
	v_mad_u32_u24 v171, v168, v181, v170
	ds_write_b8_d16_hi v184, v171
	global_store_short_d16_hi v185, v176, s[48:49]
	s_waitcnt lgkmcnt(0)
	s_barrier
	ds_read_b64 v[122:123], v105 offset:0
	ds_read_b64 v[124:125], v105 offset:8
	ds_read_b64 v[126:127], v105 offset:16
	s_barrier
	ds_read_b64 v[128:129], v105 offset:96
	ds_read_b64 v[130:131], v105 offset:104
	ds_read_b64 v[132:133], v105 offset:112
	s_waitcnt lgkmcnt(3)
	v_mfma_f32_16x16x128_f8f6f4 v[134:137], v[122:127], v[2:7], 0 cbsz:2 blgp:2
	v_mfma_f32_16x16x128_f8f6f4 v[138:141], v[122:127], v[14:19], 0 cbsz:2 blgp:2
	v_mfma_f32_16x16x128_f8f6f4 v[142:145], v[122:127], v[26:31], v[188:191] cbsz:2 blgp:2
	v_mfma_f32_16x16x128_f8f6f4 v[204:207], v[122:127], v[38:43], 0 cbsz:2 blgp:2
	v_mfma_f32_16x16x128_f8f6f4 v[208:211], v[122:127], v[50:55], 0 cbsz:2 blgp:2
	v_mfma_f32_16x16x128_f8f6f4 v[212:215], v[122:127], v[62:67], v[188:191] cbsz:2 blgp:2
	s_waitcnt lgkmcnt(0)
	v_mfma_f32_16x16x128_f8f6f4 v[134:137], v[128:133], v[8:13], v[134:137] cbsz:2 blgp:2
	v_mfma_f32_16x16x128_f8f6f4 v[204:207], v[128:133], v[44:49], v[204:207] cbsz:2 blgp:2
	v_mfma_f32_16x16x128_f8f6f4 v[138:141], v[128:133], v[20:25], v[138:141] cbsz:2 blgp:2
	v_mfma_f32_16x16x128_f8f6f4 v[208:211], v[128:133], v[56:61], v[208:211] cbsz:2 blgp:2
	v_mfma_f32_16x16x128_f8f6f4 v[142:145], v[128:133], v[32:37], v[142:145] cbsz:2 blgp:2
	v_mfma_f32_16x16x128_f8f6f4 v[212:215], v[128:133], v[68:73], v[212:215] cbsz:2 blgp:2
	v_cndmask_b32_e64 v158, v134, v204, s[0:1]
	v_cndmask_b32_e64 v159, v138, v208, s[0:1]
	v_fma_mix_f32 v158, v158, v100, v149 op_sel_hi:[0,0,1]
	v_fma_mix_f32 v159, v159, v101, v153 op_sel_hi:[0,0,1]
	v_exp_f32_e32 v158, v158
	v_exp_f32_e32 v159, v159
	v_fma_f32 v158, v158, v186, v186
	v_add_f32_e32 v159, 1.0, v159
	v_rcp_f32_e32 v158, v158
	v_rcp_f32_e32 v159, v159
	v_cndmask_b32_e64 v160, v142, v212, s[0:1]
	v_fma_mix_f32 v161, v158, v160, v157 op_sel_hi:[0,0,1]
	v_exp_f32_e32 v161, v161
	s_add_u32 s48, s48, s40
	v_add_f32_e32 v161, 1.0, v161
	v_rcp_f32_e32 v161, v161
	s_addc_u32 s49, s49, s41
	v_fma_f32 v162, v161, -2.0, 1.0
	v_sub_f32_e32 v163, v176, v162
	v_fma_f32 v176, v159, v163, v162
	v_fma_f32 v164, |v176|, s17, v113
	v_fma_f32 v165, |v176|, s18, v114
	v_fma_f32 v166, |v176|, s19, v115
	v_lshrrev_b32_e32 v167, 26, v176
	v_min3_u32 v164, v164, v165, v166
	v_bfi_b32 v168, 31, v164, v167
	s_nop 1
	v_mul_u32_u24_dpp v170, v168, v180 quad_perm:[1,2,3,3] row_mask:0xf bank_mask:0xf bound_ctrl:1
	v_mad_u32_u24 v171, v168, v181, v170
	ds_write_b8_d16_hi v184, v171 offset:416
	global_store_short_d16_hi v185, v176, s[48:49]
	s_waitcnt lgkmcnt(0)
	s_barrier
	ds_read_b64 v[122:123], v105 offset:416
	ds_read_b64 v[124:125], v105 offset:424
	ds_read_b64 v[126:127], v105 offset:432
	s_barrier
	ds_read_b64 v[128:129], v105 offset:512
	ds_read_b64 v[130:131], v105 offset:520
	ds_read_b64 v[132:133], v105 offset:528
	s_add_i32 s44, s44, 16
	s_waitcnt lgkmcnt(3)
	v_mfma_f32_16x16x128_f8f6f4 v[134:137], v[122:127], v[2:7], 0 cbsz:2 blgp:2
	v_mfma_f32_16x16x128_f8f6f4 v[138:141], v[122:127], v[14:19], 0 cbsz:2 blgp:2
	v_mfma_f32_16x16x128_f8f6f4 v[142:145], v[122:127], v[26:31], v[188:191] cbsz:2 blgp:2
	v_mfma_f32_16x16x128_f8f6f4 v[204:207], v[122:127], v[38:43], 0 cbsz:2 blgp:2
	v_mfma_f32_16x16x128_f8f6f4 v[208:211], v[122:127], v[50:55], 0 cbsz:2 blgp:2
	v_mfma_f32_16x16x128_f8f6f4 v[212:215], v[122:127], v[62:67], v[188:191] cbsz:2 blgp:2
	s_waitcnt lgkmcnt(0)
	v_mfma_f32_16x16x128_f8f6f4 v[134:137], v[128:133], v[8:13], v[134:137] cbsz:2 blgp:2
	v_mfma_f32_16x16x128_f8f6f4 v[204:207], v[128:133], v[44:49], v[204:207] cbsz:2 blgp:2
	v_mfma_f32_16x16x128_f8f6f4 v[138:141], v[128:133], v[20:25], v[138:141] cbsz:2 blgp:2
	v_mfma_f32_16x16x128_f8f6f4 v[208:211], v[128:133], v[56:61], v[208:211] cbsz:2 blgp:2
	v_mfma_f32_16x16x128_f8f6f4 v[142:145], v[128:133], v[32:37], v[142:145] cbsz:2 blgp:2
	v_mfma_f32_16x16x128_f8f6f4 v[212:215], v[128:133], v[68:73], v[212:215] cbsz:2 blgp:2
	v_cndmask_b32_e64 v158, v134, v204, s[0:1]
	v_cndmask_b32_e64 v159, v138, v208, s[0:1]
	v_fma_mix_f32 v158, v158, v100, v149 op_sel:[0,0,1] op_sel_hi:[0,0,1]
	v_fma_mix_f32 v159, v159, v101, v153 op_sel:[0,0,1] op_sel_hi:[0,0,1]
	v_exp_f32_e32 v158, v158
	v_exp_f32_e32 v159, v159
	v_fma_f32 v158, v158, v186, v186
	v_add_f32_e32 v159, 1.0, v159
	v_rcp_f32_e32 v158, v158
	v_rcp_f32_e32 v159, v159
	v_cndmask_b32_e64 v160, v142, v212, s[0:1]
	v_fma_mix_f32 v161, v158, v160, v157 op_sel:[0,0,1] op_sel_hi:[0,0,1]
	v_exp_f32_e32 v161, v161
	s_add_u32 s48, s48, s40
	v_add_f32_e32 v161, 1.0, v161
	v_rcp_f32_e32 v161, v161
	s_addc_u32 s49, s49, s41
	v_fma_f32 v162, v161, -2.0, 1.0
	v_sub_f32_e32 v163, v176, v162
	v_fma_f32 v176, v159, v163, v162
	v_fma_f32 v164, |v176|, s17, v113
	v_fma_f32 v165, |v176|, s18, v114
	v_fma_f32 v166, |v176|, s19, v115
	v_lshrrev_b32_e32 v167, 26, v176
	v_min3_u32 v164, v164, v165, v166
	v_bfi_b32 v168, 31, v164, v167
	s_nop 1
	v_mul_u32_u24_dpp v170, v168, v180 quad_perm:[1,2,3,3] row_mask:0xf bank_mask:0xf bound_ctrl:1
	v_mad_u32_u24 v171, v168, v181, v170
	ds_write_b8_d16_hi v184, v171
	global_store_short_d16_hi v185, v176, s[48:49]
	s_waitcnt lgkmcnt(0)
	s_barrier
	ds_read_b64 v[122:123], v105 offset:0
	ds_read_b64 v[124:125], v105 offset:8
	ds_read_b64 v[126:127], v105 offset:16
	s_cmp_lt_i32 s44, s45
	s_barrier
	s_cbranch_scc1 .Lscan_loop_a_f2
	s_branch .Lscan_exit_f2
.Lscan_entry_b_f2:
.Lscan_loop_b_f2:
	ds_read_b64 v[122:123], v105 offset:0
	ds_read_b64 v[124:125], v105 offset:8
	ds_read_b64 v[126:127], v105 offset:16
	ds_read_b64 v[128:129], v105 offset:96
	ds_read_b64 v[130:131], v105 offset:104
	ds_read_b64 v[132:133], v105 offset:112
	s_waitcnt vmcnt(8)
	global_load_dwordx4 v[146:149], v[196:197], off
	global_load_dwordx4 v[150:153], v[196:197], off offset:512
	global_load_dwordx4 v[154:157], v[196:197], off offset:1024
	v_lshl_add_u64 v[196:197], v[196:197], 0, s[42:43]
	s_waitcnt lgkmcnt(3)
	v_mfma_f32_16x16x128_f8f6f4 v[134:137], v[122:127], v[2:7], 0 cbsz:2 blgp:2
	v_mfma_f32_16x16x128_f8f6f4 v[138:141], v[122:127], v[14:19], 0 cbsz:2 blgp:2
	v_mfma_f32_16x16x128_f8f6f4 v[142:145], v[122:127], v[26:31], v[188:191] cbsz:2 blgp:2
	v_mfma_f32_16x16x128_f8f6f4 v[204:207], v[122:127], v[38:43], 0 cbsz:2 blgp:2
	v_mfma_f32_16x16x128_f8f6f4 v[208:211], v[122:127], v[50:55], 0 cbsz:2 blgp:2
	v_mfma_f32_16x16x128_f8f6f4 v[212:215], v[122:127], v[62:67], v[188:191] cbsz:2 blgp:2
	s_waitcnt lgkmcnt(0)
	v_mfma_f32_16x16x128_f8f6f4 v[134:137], v[128:133], v[8:13], v[134:137] cbsz:2 blgp:2
	v_mfma_f32_16x16x128_f8f6f4 v[204:207], v[128:133], v[44:49], v[204:207] cbsz:2 blgp:2
	v_mfma_f32_16x16x128_f8f6f4 v[138:141], v[128:133], v[20:25], v[138:141] cbsz:2 blgp:2
	v_mfma_f32_16x16x128_f8f6f4 v[208:211], v[128:133], v[56:61], v[208:211] cbsz:2 blgp:2
	v_mfma_f32_16x16x128_f8f6f4 v[142:145], v[128:133], v[32:37], v[142:145] cbsz:2 blgp:2
	v_mfma_f32_16x16x128_f8f6f4 v[212:215], v[128:133], v[68:73], v[212:215] cbsz:2 blgp:2
	v_cndmask_b32_e64 v158, v134, v204, s[0:1]
	v_cndmask_b32_e64 v159, v138, v208, s[0:1]
	v_fma_mix_f32 v158, v158, v100, v82 op_sel_hi:[0,0,1]
	v_fma_mix_f32 v159, v159, v101, v74 op_sel_hi:[0,0,1]
	v_exp_f32_e32 v158, v158
	v_exp_f32_e32 v159, v159
	v_fma_f32 v158, v158, v186, v186
	v_add_f32_e32 v159, 1.0, v159
	v_rcp_f32_e32 v158, v158
	v_rcp_f32_e32 v159, v159
	v_cndmask_b32_e64 v160, v142, v212, s[0:1]
	v_fma_mix_f32 v161, v158, v160, v78 op_sel_hi:[0,0,1]
	v_exp_f32_e32 v161, v161
	s_add_u32 s48, s48, s40
	v_add_f32_e32 v161, 1.0, v161
	v_rcp_f32_e32 v161, v161
	s_addc_u32 s49, s49, s41
	v_fma_f32 v162, v161, -2.0, 1.0
	v_sub_f32_e32 v163, v176, v162
	v_fma_f32 v176, v159, v163, v162
	v_fma_f32 v164, |v176|, s17, v113
	v_fma_f32 v165, |v176|, s18, v114
	v_fma_f32 v166, |v176|, s19, v115
	v_lshrrev_b32_e32 v167, 26, v176
	v_min3_u32 v164, v164, v165, v166
	v_bfi_b32 v168, 31, v164, v167
	s_nop 1
	v_mul_u32_u24_dpp v170, v168, v180 quad_perm:[1,2,3,3] row_mask:0xf bank_mask:0xf bound_ctrl:1
	v_mad_u32_u24 v171, v168, v181, v170
	ds_write_b8_d16_hi v184, v171 offset:416
	s_barrier
	global_store_short_d16_hi v185, v176, s[48:49]
	s_waitcnt lgkmcnt(0)
	s_barrier
	ds_read_b64 v[122:123], v105 offset:416
	ds_read_b64 v[124:125], v105 offset:424
	ds_read_b64 v[126:127], v105 offset:432
	ds_read_b64 v[128:129], v105 offset:512
	ds_read_b64 v[130:131], v105 offset:520
	ds_read_b64 v[132:133], v105 offset:528
	s_waitcnt lgkmcnt(3)
	v_mfma_f32_16x16x128_f8f6f4 v[134:137], v[122:127], v[2:7], 0 cbsz:2 blgp:2
	v_mfma_f32_16x16x128_f8f6f4 v[138:141], v[122:127], v[14:19], 0 cbsz:2 blgp:2
	v_mfma_f32_16x16x128_f8f6f4 v[142:145], v[122:127], v[26:31], v[188:191] cbsz:2 blgp:2
	v_mfma_f32_16x16x128_f8f6f4 v[204:207], v[122:127], v[38:43], 0 cbsz:2 blgp:2
	v_mfma_f32_16x16x128_f8f6f4 v[208:211], v[122:127], v[50:55], 0 cbsz:2 blgp:2
	v_mfma_f32_16x16x128_f8f6f4 v[212:215], v[122:127], v[62:67], v[188:191] cbsz:2 blgp:2
	s_waitcnt lgkmcnt(0)
	v_mfma_f32_16x16x128_f8f6f4 v[134:137], v[128:133], v[8:13], v[134:137] cbsz:2 blgp:2
	v_mfma_f32_16x16x128_f8f6f4 v[204:207], v[128:133], v[44:49], v[204:207] cbsz:2 blgp:2
	v_mfma_f32_16x16x128_f8f6f4 v[138:141], v[128:133], v[20:25], v[138:141] cbsz:2 blgp:2
	v_mfma_f32_16x16x128_f8f6f4 v[208:211], v[128:133], v[56:61], v[208:211] cbsz:2 blgp:2
	v_mfma_f32_16x16x128_f8f6f4 v[142:145], v[128:133], v[32:37], v[142:145] cbsz:2 blgp:2
	v_mfma_f32_16x16x128_f8f6f4 v[212:215], v[128:133], v[68:73], v[212:215] cbsz:2 blgp:2
	v_cndmask_b32_e64 v158, v134, v204, s[0:1]
	v_cndmask_b32_e64 v159, v138, v208, s[0:1]
	v_fma_mix_f32 v158, v158, v100, v82 op_sel:[0,0,1] op_sel_hi:[0,0,1]
	v_fma_mix_f32 v159, v159, v101, v74 op_sel:[0,0,1] op_sel_hi:[0,0,1]
	v_exp_f32_e32 v158, v158
	v_exp_f32_e32 v159, v159
	v_fma_f32 v158, v158, v186, v186
	v_add_f32_e32 v159, 1.0, v159
	v_rcp_f32_e32 v158, v158
	v_rcp_f32_e32 v159, v159
	v_cndmask_b32_e64 v160, v142, v212, s[0:1]
	v_fma_mix_f32 v161, v158, v160, v78 op_sel:[0,0,1] op_sel_hi:[0,0,1]
	v_exp_f32_e32 v161, v161
	s_add_u32 s48, s48, s40
	v_add_f32_e32 v161, 1.0, v161
	v_rcp_f32_e32 v161, v161
	s_addc_u32 s49, s49, s41
	v_fma_f32 v162, v161, -2.0, 1.0
	v_sub_f32_e32 v163, v176, v162
	v_fma_f32 v176, v159, v163, v162
	v_fma_f32 v164, |v176|, s17, v113
	v_fma_f32 v165, |v176|, s18, v114
	v_fma_f32 v166, |v176|, s19, v115
	v_lshrrev_b32_e32 v167, 26, v176
	v_min3_u32 v164, v164, v165, v166
	v_bfi_b32 v168, 31, v164, v167
	s_nop 1
	v_mul_u32_u24_dpp v170, v168, v180 quad_perm:[1,2,3,3] row_mask:0xf bank_mask:0xf bound_ctrl:1
	v_mad_u32_u24 v171, v168, v181, v170
	ds_write_b8_d16_hi v184, v171
	s_barrier
	global_store_short_d16_hi v185, v176, s[48:49]
	s_waitcnt lgkmcnt(0)
	s_barrier
	ds_read_b64 v[122:123], v105 offset:0
	ds_read_b64 v[124:125], v105 offset:8
	ds_read_b64 v[126:127], v105 offset:16
	ds_read_b64 v[128:129], v105 offset:96
	ds_read_b64 v[130:131], v105 offset:104
	ds_read_b64 v[132:133], v105 offset:112
	s_waitcnt lgkmcnt(3)
	v_mfma_f32_16x16x128_f8f6f4 v[134:137], v[122:127], v[2:7], 0 cbsz:2 blgp:2
	v_mfma_f32_16x16x128_f8f6f4 v[138:141], v[122:127], v[14:19], 0 cbsz:2 blgp:2
	v_mfma_f32_16x16x128_f8f6f4 v[142:145], v[122:127], v[26:31], v[188:191] cbsz:2 blgp:2
	v_mfma_f32_16x16x128_f8f6f4 v[204:207], v[122:127], v[38:43], 0 cbsz:2 blgp:2
	v_mfma_f32_16x16x128_f8f6f4 v[208:211], v[122:127], v[50:55], 0 cbsz:2 blgp:2
	v_mfma_f32_16x16x128_f8f6f4 v[212:215], v[122:127], v[62:67], v[188:191] cbsz:2 blgp:2
	s_waitcnt lgkmcnt(0)
	v_mfma_f32_16x16x128_f8f6f4 v[134:137], v[128:133], v[8:13], v[134:137] cbsz:2 blgp:2
	v_mfma_f32_16x16x128_f8f6f4 v[204:207], v[128:133], v[44:49], v[204:207] cbsz:2 blgp:2
	v_mfma_f32_16x16x128_f8f6f4 v[138:141], v[128:133], v[20:25], v[138:141] cbsz:2 blgp:2
	v_mfma_f32_16x16x128_f8f6f4 v[208:211], v[128:133], v[56:61], v[208:211] cbsz:2 blgp:2
	v_mfma_f32_16x16x128_f8f6f4 v[142:145], v[128:133], v[32:37], v[142:145] cbsz:2 blgp:2
	v_mfma_f32_16x16x128_f8f6f4 v[212:215], v[128:133], v[68:73], v[212:215] cbsz:2 blgp:2
	v_cndmask_b32_e64 v158, v134, v204, s[0:1]
	v_cndmask_b32_e64 v159, v138, v208, s[0:1]
	v_fma_mix_f32 v158, v158, v100, v83 op_sel_hi:[0,0,1]
	v_fma_mix_f32 v159, v159, v101, v75 op_sel_hi:[0,0,1]
	v_exp_f32_e32 v158, v158
	v_exp_f32_e32 v159, v159
	v_fma_f32 v158, v158, v186, v186
	v_add_f32_e32 v159, 1.0, v159
	v_rcp_f32_e32 v158, v158
	v_rcp_f32_e32 v159, v159
	v_cndmask_b32_e64 v160, v142, v212, s[0:1]
	v_fma_mix_f32 v161, v158, v160, v79 op_sel_hi:[0,0,1]
	v_exp_f32_e32 v161, v161
	s_add_u32 s48, s48, s40
	v_add_f32_e32 v161, 1.0, v161
	v_rcp_f32_e32 v161, v161
	s_addc_u32 s49, s49, s41
	v_fma_f32 v162, v161, -2.0, 1.0
	v_sub_f32_e32 v163, v176, v162
	v_fma_f32 v176, v159, v163, v162
	v_fma_f32 v164, |v176|, s17, v113
	v_fma_f32 v165, |v176|, s18, v114
	v_fma_f32 v166, |v176|, s19, v115
	v_lshrrev_b32_e32 v167, 26, v176
	v_min3_u32 v164, v164, v165, v166
	v_bfi_b32 v168, 31, v164, v167
	s_nop 1
	v_mul_u32_u24_dpp v170, v168, v180 quad_perm:[1,2,3,3] row_mask:0xf bank_mask:0xf bound_ctrl:1
	v_mad_u32_u24 v171, v168, v181, v170
	ds_write_b8_d16_hi v184, v171 offset:416
	s_barrier
	global_store_short_d16_hi v185, v176, s[48:49]
	s_waitcnt lgkmcnt(0)
	s_barrier
	ds_read_b64 v[122:123], v105 offset:416
	ds_read_b64 v[124:125], v105 offset:424
	ds_read_b64 v[126:127], v105 offset:432
	ds_read_b64 v[128:129], v105 offset:512
	ds_read_b64 v[130:131], v105 offset:520
	ds_read_b64 v[132:133], v105 offset:528
	s_waitcnt lgkmcnt(3)
	v_mfma_f32_16x16x128_f8f6f4 v[134:137], v[122:127], v[2:7], 0 cbsz:2 blgp:2
	v_mfma_f32_16x16x128_f8f6f4 v[138:141], v[122:127], v[14:19], 0 cbsz:2 blgp:2
	v_mfma_f32_16x16x128_f8f6f4 v[142:145], v[122:127], v[26:31], v[188:191] cbsz:2 blgp:2
	v_mfma_f32_16x16x128_f8f6f4 v[204:207], v[122:127], v[38:43], 0 cbsz:2 blgp:2
	v_mfma_f32_16x16x128_f8f6f4 v[208:211], v[122:127], v[50:55], 0 cbsz:2 blgp:2
	v_mfma_f32_16x16x128_f8f6f4 v[212:215], v[122:127], v[62:67], v[188:191] cbsz:2 blgp:2
	s_waitcnt lgkmcnt(0)
	v_mfma_f32_16x16x128_f8f6f4 v[134:137], v[128:133], v[8:13], v[134:137] cbsz:2 blgp:2
	v_mfma_f32_16x16x128_f8f6f4 v[204:207], v[128:133], v[44:49], v[204:207] cbsz:2 blgp:2
	v_mfma_f32_16x16x128_f8f6f4 v[138:141], v[128:133], v[20:25], v[138:141] cbsz:2 blgp:2
	v_mfma_f32_16x16x128_f8f6f4 v[208:211], v[128:133], v[56:61], v[208:211] cbsz:2 blgp:2
	v_mfma_f32_16x16x128_f8f6f4 v[142:145], v[128:133], v[32:37], v[142:145] cbsz:2 blgp:2
	v_mfma_f32_16x16x128_f8f6f4 v[212:215], v[128:133], v[68:73], v[212:215] cbsz:2 blgp:2
	v_cndmask_b32_e64 v158, v134, v204, s[0:1]
	v_cndmask_b32_e64 v159, v138, v208, s[0:1]
	v_fma_mix_f32 v158, v158, v100, v83 op_sel:[0,0,1] op_sel_hi:[0,0,1]
	v_fma_mix_f32 v159, v159, v101, v75 op_sel:[0,0,1] op_sel_hi:[0,0,1]
	v_exp_f32_e32 v158, v158
	v_exp_f32_e32 v159, v159
	v_fma_f32 v158, v158, v186, v186
	v_add_f32_e32 v159, 1.0, v159
	v_rcp_f32_e32 v158, v158
	v_rcp_f32_e32 v159, v159
	v_cndmask_b32_e64 v160, v142, v212, s[0:1]
	v_fma_mix_f32 v161, v158, v160, v79 op_sel:[0,0,1] op_sel_hi:[0,0,1]
	v_exp_f32_e32 v161, v161
	s_add_u32 s48, s48, s40
	v_add_f32_e32 v161, 1.0, v161
	v_rcp_f32_e32 v161, v161
	s_addc_u32 s49, s49, s41
	v_fma_f32 v162, v161, -2.0, 1.0
	v_sub_f32_e32 v163, v176, v162
	v_fma_f32 v176, v159, v163, v162
	v_fma_f32 v164, |v176|, s17, v113
	v_fma_f32 v165, |v176|, s18, v114
	v_fma_f32 v166, |v176|, s19, v115
	v_lshrrev_b32_e32 v167, 26, v176
	v_min3_u32 v164, v164, v165, v166
	v_bfi_b32 v168, 31, v164, v167
	s_nop 1
	v_mul_u32_u24_dpp v170, v168, v180 quad_perm:[1,2,3,3] row_mask:0xf bank_mask:0xf bound_ctrl:1
	v_mad_u32_u24 v171, v168, v181, v170
	ds_write_b8_d16_hi v184, v171
	s_barrier
	global_store_short_d16_hi v185, v176, s[48:49]
	s_waitcnt lgkmcnt(0)
	s_barrier
	ds_read_b64 v[122:123], v105 offset:0
	ds_read_b64 v[124:125], v105 offset:8
	ds_read_b64 v[126:127], v105 offset:16
	ds_read_b64 v[128:129], v105 offset:96
	ds_read_b64 v[130:131], v105 offset:104
	ds_read_b64 v[132:133], v105 offset:112
	s_waitcnt lgkmcnt(3)
	v_mfma_f32_16x16x128_f8f6f4 v[134:137], v[122:127], v[2:7], 0 cbsz:2 blgp:2
	v_mfma_f32_16x16x128_f8f6f4 v[138:141], v[122:127], v[14:19], 0 cbsz:2 blgp:2
	v_mfma_f32_16x16x128_f8f6f4 v[142:145], v[122:127], v[26:31], v[188:191] cbsz:2 blgp:2
	v_mfma_f32_16x16x128_f8f6f4 v[204:207], v[122:127], v[38:43], 0 cbsz:2 blgp:2
	v_mfma_f32_16x16x128_f8f6f4 v[208:211], v[122:127], v[50:55], 0 cbsz:2 blgp:2
	v_mfma_f32_16x16x128_f8f6f4 v[212:215], v[122:127], v[62:67], v[188:191] cbsz:2 blgp:2
	s_waitcnt lgkmcnt(0)
	v_mfma_f32_16x16x128_f8f6f4 v[134:137], v[128:133], v[8:13], v[134:137] cbsz:2 blgp:2
	v_mfma_f32_16x16x128_f8f6f4 v[204:207], v[128:133], v[44:49], v[204:207] cbsz:2 blgp:2
	v_mfma_f32_16x16x128_f8f6f4 v[138:141], v[128:133], v[20:25], v[138:141] cbsz:2 blgp:2
	v_mfma_f32_16x16x128_f8f6f4 v[208:211], v[128:133], v[56:61], v[208:211] cbsz:2 blgp:2
	v_mfma_f32_16x16x128_f8f6f4 v[142:145], v[128:133], v[32:37], v[142:145] cbsz:2 blgp:2
	v_mfma_f32_16x16x128_f8f6f4 v[212:215], v[128:133], v[68:73], v[212:215] cbsz:2 blgp:2
	v_cndmask_b32_e64 v158, v134, v204, s[0:1]
	v_cndmask_b32_e64 v159, v138, v208, s[0:1]
	v_fma_mix_f32 v158, v158, v100, v84 op_sel_hi:[0,0,1]
	v_fma_mix_f32 v159, v159, v101, v76 op_sel_hi:[0,0,1]
	v_exp_f32_e32 v158, v158
	v_exp_f32_e32 v159, v159
	v_fma_f32 v158, v158, v186, v186
	v_add_f32_e32 v159, 1.0, v159
	v_rcp_f32_e32 v158, v158
	v_rcp_f32_e32 v159, v159
	v_cndmask_b32_e64 v160, v142, v212, s[0:1]
	v_fma_mix_f32 v161, v158, v160, v80 op_sel_hi:[0,0,1]
	v_exp_f32_e32 v161, v161
	s_add_u32 s48, s48, s40
	v_add_f32_e32 v161, 1.0, v161
	v_rcp_f32_e32 v161, v161
	s_addc_u32 s49, s49, s41
	v_fma_f32 v162, v161, -2.0, 1.0
	v_sub_f32_e32 v163, v176, v162
	v_fma_f32 v176, v159, v163, v162
	v_fma_f32 v164, |v176|, s17, v113
	v_fma_f32 v165, |v176|, s18, v114
	v_fma_f32 v166, |v176|, s19, v115
	v_lshrrev_b32_e32 v167, 26, v176
	v_min3_u32 v164, v164, v165, v166
	v_bfi_b32 v168, 31, v164, v167
	s_nop 1
	v_mul_u32_u24_dpp v170, v168, v180 quad_perm:[1,2,3,3] row_mask:0xf bank_mask:0xf bound_ctrl:1
	v_mad_u32_u24 v171, v168, v181, v170
	ds_write_b8_d16_hi v184, v171 offset:416
	s_barrier
	global_store_short_d16_hi v185, v176, s[48:49]
	s_waitcnt lgkmcnt(0)
	s_barrier
	ds_read_b64 v[122:123], v105 offset:416
	ds_read_b64 v[124:125], v105 offset:424
	ds_read_b64 v[126:127], v105 offset:432
	ds_read_b64 v[128:129], v105 offset:512
	ds_read_b64 v[130:131], v105 offset:520
	ds_read_b64 v[132:133], v105 offset:528
	s_waitcnt lgkmcnt(3)
	v_mfma_f32_16x16x128_f8f6f4 v[134:137], v[122:127], v[2:7], 0 cbsz:2 blgp:2
	v_mfma_f32_16x16x128_f8f6f4 v[138:141], v[122:127], v[14:19], 0 cbsz:2 blgp:2
	v_mfma_f32_16x16x128_f8f6f4 v[142:145], v[122:127], v[26:31], v[188:191] cbsz:2 blgp:2
	v_mfma_f32_16x16x128_f8f6f4 v[204:207], v[122:127], v[38:43], 0 cbsz:2 blgp:2
	v_mfma_f32_16x16x128_f8f6f4 v[208:211], v[122:127], v[50:55], 0 cbsz:2 blgp:2
	v_mfma_f32_16x16x128_f8f6f4 v[212:215], v[122:127], v[62:67], v[188:191] cbsz:2 blgp:2
	s_waitcnt lgkmcnt(0)
	v_mfma_f32_16x16x128_f8f6f4 v[134:137], v[128:133], v[8:13], v[134:137] cbsz:2 blgp:2
	v_mfma_f32_16x16x128_f8f6f4 v[204:207], v[128:133], v[44:49], v[204:207] cbsz:2 blgp:2
	v_mfma_f32_16x16x128_f8f6f4 v[138:141], v[128:133], v[20:25], v[138:141] cbsz:2 blgp:2
	v_mfma_f32_16x16x128_f8f6f4 v[208:211], v[128:133], v[56:61], v[208:211] cbsz:2 blgp:2
	v_mfma_f32_16x16x128_f8f6f4 v[142:145], v[128:133], v[32:37], v[142:145] cbsz:2 blgp:2
	v_mfma_f32_16x16x128_f8f6f4 v[212:215], v[128:133], v[68:73], v[212:215] cbsz:2 blgp:2
	v_cndmask_b32_e64 v158, v134, v204, s[0:1]
	v_cndmask_b32_e64 v159, v138, v208, s[0:1]
	v_fma_mix_f32 v158, v158, v100, v84 op_sel:[0,0,1] op_sel_hi:[0,0,1]
	v_fma_mix_f32 v159, v159, v101, v76 op_sel:[0,0,1] op_sel_hi:[0,0,1]
	v_exp_f32_e32 v158, v158
	v_exp_f32_e32 v159, v159
	v_fma_f32 v158, v158, v186, v186
	v_add_f32_e32 v159, 1.0, v159
	v_rcp_f32_e32 v158, v158
	v_rcp_f32_e32 v159, v159
	v_cndmask_b32_e64 v160, v142, v212, s[0:1]
	v_fma_mix_f32 v161, v158, v160, v80 op_sel:[0,0,1] op_sel_hi:[0,0,1]
	v_exp_f32_e32 v161, v161
	s_add_u32 s48, s48, s40
	v_add_f32_e32 v161, 1.0, v161
	v_rcp_f32_e32 v161, v161
	s_addc_u32 s49, s49, s41
	v_fma_f32 v162, v161, -2.0, 1.0
	v_sub_f32_e32 v163, v176, v162
	v_fma_f32 v176, v159, v163, v162
	v_fma_f32 v164, |v176|, s17, v113
	v_fma_f32 v165, |v176|, s18, v114
	v_fma_f32 v166, |v176|, s19, v115
	v_lshrrev_b32_e32 v167, 26, v176
	v_min3_u32 v164, v164, v165, v166
	v_bfi_b32 v168, 31, v164, v167
	s_nop 1
	v_mul_u32_u24_dpp v170, v168, v180 quad_perm:[1,2,3,3] row_mask:0xf bank_mask:0xf bound_ctrl:1
	v_mad_u32_u24 v171, v168, v181, v170
	ds_write_b8_d16_hi v184, v171
	s_barrier
	global_store_short_d16_hi v185, v176, s[48:49]
	s_waitcnt lgkmcnt(0)
	s_barrier
	ds_read_b64 v[122:123], v105 offset:0
	ds_read_b64 v[124:125], v105 offset:8
	ds_read_b64 v[126:127], v105 offset:16
	ds_read_b64 v[128:129], v105 offset:96
	ds_read_b64 v[130:131], v105 offset:104
	ds_read_b64 v[132:133], v105 offset:112
	s_waitcnt lgkmcnt(3)
	v_mfma_f32_16x16x128_f8f6f4 v[134:137], v[122:127], v[2:7], 0 cbsz:2 blgp:2
	v_mfma_f32_16x16x128_f8f6f4 v[138:141], v[122:127], v[14:19], 0 cbsz:2 blgp:2
	v_mfma_f32_16x16x128_f8f6f4 v[142:145], v[122:127], v[26:31], v[188:191] cbsz:2 blgp:2
	v_mfma_f32_16x16x128_f8f6f4 v[204:207], v[122:127], v[38:43], 0 cbsz:2 blgp:2
	v_mfma_f32_16x16x128_f8f6f4 v[208:211], v[122:127], v[50:55], 0 cbsz:2 blgp:2
	v_mfma_f32_16x16x128_f8f6f4 v[212:215], v[122:127], v[62:67], v[188:191] cbsz:2 blgp:2
	s_waitcnt lgkmcnt(0)
	v_mfma_f32_16x16x128_f8f6f4 v[134:137], v[128:133], v[8:13], v[134:137] cbsz:2 blgp:2
	v_mfma_f32_16x16x128_f8f6f4 v[204:207], v[128:133], v[44:49], v[204:207] cbsz:2 blgp:2
	v_mfma_f32_16x16x128_f8f6f4 v[138:141], v[128:133], v[20:25], v[138:141] cbsz:2 blgp:2
	v_mfma_f32_16x16x128_f8f6f4 v[208:211], v[128:133], v[56:61], v[208:211] cbsz:2 blgp:2
	v_mfma_f32_16x16x128_f8f6f4 v[142:145], v[128:133], v[32:37], v[142:145] cbsz:2 blgp:2
	v_mfma_f32_16x16x128_f8f6f4 v[212:215], v[128:133], v[68:73], v[212:215] cbsz:2 blgp:2
	v_cndmask_b32_e64 v158, v134, v204, s[0:1]
	v_cndmask_b32_e64 v159, v138, v208, s[0:1]
	v_fma_mix_f32 v158, v158, v100, v85 op_sel_hi:[0,0,1]
	v_fma_mix_f32 v159, v159, v101, v77 op_sel_hi:[0,0,1]
	v_exp_f32_e32 v158, v158
	v_exp_f32_e32 v159, v159
	v_fma_f32 v158, v158, v186, v186
	v_add_f32_e32 v159, 1.0, v159
	v_rcp_f32_e32 v158, v158
	v_rcp_f32_e32 v159, v159
	v_cndmask_b32_e64 v160, v142, v212, s[0:1]
	v_fma_mix_f32 v161, v158, v160, v81 op_sel_hi:[0,0,1]
	v_exp_f32_e32 v161, v161
	s_add_u32 s48, s48, s40
	v_add_f32_e32 v161, 1.0, v161
	v_rcp_f32_e32 v161, v161
	s_addc_u32 s49, s49, s41
	v_fma_f32 v162, v161, -2.0, 1.0
	v_sub_f32_e32 v163, v176, v162
	v_fma_f32 v176, v159, v163, v162
	v_fma_f32 v164, |v176|, s17, v113
	v_fma_f32 v165, |v176|, s18, v114
	v_fma_f32 v166, |v176|, s19, v115
	v_lshrrev_b32_e32 v167, 26, v176
	v_min3_u32 v164, v164, v165, v166
	v_bfi_b32 v168, 31, v164, v167
	s_nop 1
	v_mul_u32_u24_dpp v170, v168, v180 quad_perm:[1,2,3,3] row_mask:0xf bank_mask:0xf bound_ctrl:1
	v_mad_u32_u24 v171, v168, v181, v170
	ds_write_b8_d16_hi v184, v171 offset:416
	s_barrier
	global_store_short_d16_hi v185, v176, s[48:49]
	s_waitcnt lgkmcnt(0)
	s_barrier
	ds_read_b64 v[122:123], v105 offset:416
	ds_read_b64 v[124:125], v105 offset:424
	ds_read_b64 v[126:127], v105 offset:432
	ds_read_b64 v[128:129], v105 offset:512
	ds_read_b64 v[130:131], v105 offset:520
	ds_read_b64 v[132:133], v105 offset:528
	s_waitcnt lgkmcnt(3)
	v_mfma_f32_16x16x128_f8f6f4 v[134:137], v[122:127], v[2:7], 0 cbsz:2 blgp:2
	v_mfma_f32_16x16x128_f8f6f4 v[138:141], v[122:127], v[14:19], 0 cbsz:2 blgp:2
	v_mfma_f32_16x16x128_f8f6f4 v[142:145], v[122:127], v[26:31], v[188:191] cbsz:2 blgp:2
	v_mfma_f32_16x16x128_f8f6f4 v[204:207], v[122:127], v[38:43], 0 cbsz:2 blgp:2
	v_mfma_f32_16x16x128_f8f6f4 v[208:211], v[122:127], v[50:55], 0 cbsz:2 blgp:2
	v_mfma_f32_16x16x128_f8f6f4 v[212:215], v[122:127], v[62:67], v[188:191] cbsz:2 blgp:2
	s_waitcnt lgkmcnt(0)
	v_mfma_f32_16x16x128_f8f6f4 v[134:137], v[128:133], v[8:13], v[134:137] cbsz:2 blgp:2
	v_mfma_f32_16x16x128_f8f6f4 v[204:207], v[128:133], v[44:49], v[204:207] cbsz:2 blgp:2
	v_mfma_f32_16x16x128_f8f6f4 v[138:141], v[128:133], v[20:25], v[138:141] cbsz:2 blgp:2
	v_mfma_f32_16x16x128_f8f6f4 v[208:211], v[128:133], v[56:61], v[208:211] cbsz:2 blgp:2
	v_mfma_f32_16x16x128_f8f6f4 v[142:145], v[128:133], v[32:37], v[142:145] cbsz:2 blgp:2
	v_mfma_f32_16x16x128_f8f6f4 v[212:215], v[128:133], v[68:73], v[212:215] cbsz:2 blgp:2
	v_cndmask_b32_e64 v158, v134, v204, s[0:1]
	v_cndmask_b32_e64 v159, v138, v208, s[0:1]
	v_fma_mix_f32 v158, v158, v100, v85 op_sel:[0,0,1] op_sel_hi:[0,0,1]
	v_fma_mix_f32 v159, v159, v101, v77 op_sel:[0,0,1] op_sel_hi:[0,0,1]
	v_exp_f32_e32 v158, v158
	v_exp_f32_e32 v159, v159
	v_fma_f32 v158, v158, v186, v186
	v_add_f32_e32 v159, 1.0, v159
	v_rcp_f32_e32 v158, v158
	v_rcp_f32_e32 v159, v159
	v_cndmask_b32_e64 v160, v142, v212, s[0:1]
	v_fma_mix_f32 v161, v158, v160, v81 op_sel:[0,0,1] op_sel_hi:[0,0,1]
	v_exp_f32_e32 v161, v161
	s_add_u32 s48, s48, s40
	v_add_f32_e32 v161, 1.0, v161
	v_rcp_f32_e32 v161, v161
	s_addc_u32 s49, s49, s41
	v_fma_f32 v162, v161, -2.0, 1.0
	v_sub_f32_e32 v163, v176, v162
	v_fma_f32 v176, v159, v163, v162
	v_fma_f32 v164, |v176|, s17, v113
	v_fma_f32 v165, |v176|, s18, v114
	v_fma_f32 v166, |v176|, s19, v115
	v_lshrrev_b32_e32 v167, 26, v176
	v_min3_u32 v164, v164, v165, v166
	v_bfi_b32 v168, 31, v164, v167
	s_nop 1
	v_mul_u32_u24_dpp v170, v168, v180 quad_perm:[1,2,3,3] row_mask:0xf bank_mask:0xf bound_ctrl:1
	v_mad_u32_u24 v171, v168, v181, v170
	ds_write_b8_d16_hi v184, v171
	s_barrier
	global_store_short_d16_hi v185, v176, s[48:49]
	s_waitcnt lgkmcnt(0)
	s_barrier
	ds_read_b64 v[122:123], v105 offset:0
	ds_read_b64 v[124:125], v105 offset:8
	ds_read_b64 v[126:127], v105 offset:16
	ds_read_b64 v[128:129], v105 offset:96
	ds_read_b64 v[130:131], v105 offset:104
	ds_read_b64 v[132:133], v105 offset:112
	s_waitcnt vmcnt(8)
	global_load_dwordx4 v[82:85], v[196:197], off
	global_load_dwordx4 v[74:77], v[196:197], off offset:512
	global_load_dwordx4 v[78:81], v[196:197], off offset:1024
	v_lshl_add_u64 v[196:197], v[196:197], 0, s[42:43]
	s_waitcnt lgkmcnt(3)
	v_mfma_f32_16x16x128_f8f6f4 v[134:137], v[122:127], v[2:7], 0 cbsz:2 blgp:2
	v_mfma_f32_16x16x128_f8f6f4 v[138:141], v[122:127], v[14:19], 0 cbsz:2 blgp:2
	v_mfma_f32_16x16x128_f8f6f4 v[142:145], v[122:127], v[26:31], v[188:191] cbsz:2 blgp:2
	v_mfma_f32_16x16x128_f8f6f4 v[204:207], v[122:127], v[38:43], 0 cbsz:2 blgp:2
	v_mfma_f32_16x16x128_f8f6f4 v[208:211], v[122:127], v[50:55], 0 cbsz:2 blgp:2
	v_mfma_f32_16x16x128_f8f6f4 v[212:215], v[122:127], v[62:67], v[188:191] cbsz:2 blgp:2
	s_waitcnt lgkmcnt(0)
	v_mfma_f32_16x16x128_f8f6f4 v[134:137], v[128:133], v[8:13], v[134:137] cbsz:2 blgp:2
	v_mfma_f32_16x16x128_f8f6f4 v[204:207], v[128:133], v[44:49], v[204:207] cbsz:2 blgp:2
	v_mfma_f32_16x16x128_f8f6f4 v[138:141], v[128:133], v[20:25], v[138:141] cbsz:2 blgp:2
	v_mfma_f32_16x16x128_f8f6f4 v[208:211], v[128:133], v[56:61], v[208:211] cbsz:2 blgp:2
	v_mfma_f32_16x16x128_f8f6f4 v[142:145], v[128:133], v[32:37], v[142:145] cbsz:2 blgp:2
	v_mfma_f32_16x16x128_f8f6f4 v[212:215], v[128:133], v[68:73], v[212:215] cbsz:2 blgp:2
	v_cndmask_b32_e64 v158, v134, v204, s[0:1]
	v_cndmask_b32_e64 v159, v138, v208, s[0:1]
	v_fma_mix_f32 v158, v158, v100, v146 op_sel_hi:[0,0,1]
	v_fma_mix_f32 v159, v159, v101, v150 op_sel_hi:[0,0,1]
	v_exp_f32_e32 v158, v158
	v_exp_f32_e32 v159, v159
	v_fma_f32 v158, v158, v186, v186
	v_add_f32_e32 v159, 1.0, v159
	v_rcp_f32_e32 v158, v158
	v_rcp_f32_e32 v159, v159
	v_cndmask_b32_e64 v160, v142, v212, s[0:1]
	v_fma_mix_f32 v161, v158, v160, v154 op_sel_hi:[0,0,1]
	v_exp_f32_e32 v161, v161
	s_add_u32 s48, s48, s40
	v_add_f32_e32 v161, 1.0, v161
	v_rcp_f32_e32 v161, v161
	s_addc_u32 s49, s49, s41
	v_fma_f32 v162, v161, -2.0, 1.0
	v_sub_f32_e32 v163, v176, v162
	v_fma_f32 v176, v159, v163, v162
	v_fma_f32 v164, |v176|, s17, v113
	v_fma_f32 v165, |v176|, s18, v114
	v_fma_f32 v166, |v176|, s19, v115
	v_lshrrev_b32_e32 v167, 26, v176
	v_min3_u32 v164, v164, v165, v166
	v_bfi_b32 v168, 31, v164, v167
	s_nop 1
	v_mul_u32_u24_dpp v170, v168, v180 quad_perm:[1,2,3,3] row_mask:0xf bank_mask:0xf bound_ctrl:1
	v_mad_u32_u24 v171, v168, v181, v170
	ds_write_b8_d16_hi v184, v171 offset:416
	s_barrier
	global_store_short_d16_hi v185, v176, s[48:49]
	s_waitcnt lgkmcnt(0)
	s_barrier
	ds_read_b64 v[122:123], v105 offset:416
	ds_read_b64 v[124:125], v105 offset:424
	ds_read_b64 v[126:127], v105 offset:432
	ds_read_b64 v[128:129], v105 offset:512
	ds_read_b64 v[130:131], v105 offset:520
	ds_read_b64 v[132:133], v105 offset:528
	s_waitcnt lgkmcnt(3)
	v_mfma_f32_16x16x128_f8f6f4 v[134:137], v[122:127], v[2:7], 0 cbsz:2 blgp:2
	v_mfma_f32_16x16x128_f8f6f4 v[138:141], v[122:127], v[14:19], 0 cbsz:2 blgp:2
	v_mfma_f32_16x16x128_f8f6f4 v[142:145], v[122:127], v[26:31], v[188:191] cbsz:2 blgp:2
	v_mfma_f32_16x16x128_f8f6f4 v[204:207], v[122:127], v[38:43], 0 cbsz:2 blgp:2
	v_mfma_f32_16x16x128_f8f6f4 v[208:211], v[122:127], v[50:55], 0 cbsz:2 blgp:2
	v_mfma_f32_16x16x128_f8f6f4 v[212:215], v[122:127], v[62:67], v[188:191] cbsz:2 blgp:2
	s_waitcnt lgkmcnt(0)
	v_mfma_f32_16x16x128_f8f6f4 v[134:137], v[128:133], v[8:13], v[134:137] cbsz:2 blgp:2
	v_mfma_f32_16x16x128_f8f6f4 v[204:207], v[128:133], v[44:49], v[204:207] cbsz:2 blgp:2
	v_mfma_f32_16x16x128_f8f6f4 v[138:141], v[128:133], v[20:25], v[138:141] cbsz:2 blgp:2
	v_mfma_f32_16x16x128_f8f6f4 v[208:211], v[128:133], v[56:61], v[208:211] cbsz:2 blgp:2
	v_mfma_f32_16x16x128_f8f6f4 v[142:145], v[128:133], v[32:37], v[142:145] cbsz:2 blgp:2
	v_mfma_f32_16x16x128_f8f6f4 v[212:215], v[128:133], v[68:73], v[212:215] cbsz:2 blgp:2
	v_cndmask_b32_e64 v158, v134, v204, s[0:1]
	v_cndmask_b32_e64 v159, v138, v208, s[0:1]
	v_fma_mix_f32 v158, v158, v100, v146 op_sel:[0,0,1] op_sel_hi:[0,0,1]
	v_fma_mix_f32 v159, v159, v101, v150 op_sel:[0,0,1] op_sel_hi:[0,0,1]
	v_exp_f32_e32 v158, v158
	v_exp_f32_e32 v159, v159
	v_fma_f32 v158, v158, v186, v186
	v_add_f32_e32 v159, 1.0, v159
	v_rcp_f32_e32 v158, v158
	v_rcp_f32_e32 v159, v159
	v_cndmask_b32_e64 v160, v142, v212, s[0:1]
	v_fma_mix_f32 v161, v158, v160, v154 op_sel:[0,0,1] op_sel_hi:[0,0,1]
	v_exp_f32_e32 v161, v161
	s_add_u32 s48, s48, s40
	v_add_f32_e32 v161, 1.0, v161
	v_rcp_f32_e32 v161, v161
	s_addc_u32 s49, s49, s41
	v_fma_f32 v162, v161, -2.0, 1.0
	v_sub_f32_e32 v163, v176, v162
	v_fma_f32 v176, v159, v163, v162
	v_fma_f32 v164, |v176|, s17, v113
	v_fma_f32 v165, |v176|, s18, v114
	v_fma_f32 v166, |v176|, s19, v115
	v_lshrrev_b32_e32 v167, 26, v176
	v_min3_u32 v164, v164, v165, v166
	v_bfi_b32 v168, 31, v164, v167
	s_nop 1
	v_mul_u32_u24_dpp v170, v168, v180 quad_perm:[1,2,3,3] row_mask:0xf bank_mask:0xf bound_ctrl:1
	v_mad_u32_u24 v171, v168, v181, v170
	ds_write_b8_d16_hi v184, v171
	s_barrier
	global_store_short_d16_hi v185, v176, s[48:49]
	s_waitcnt lgkmcnt(0)
	s_barrier
	ds_read_b64 v[122:123], v105 offset:0
	ds_read_b64 v[124:125], v105 offset:8
	ds_read_b64 v[126:127], v105 offset:16
	ds_read_b64 v[128:129], v105 offset:96
	ds_read_b64 v[130:131], v105 offset:104
	ds_read_b64 v[132:133], v105 offset:112
	s_waitcnt lgkmcnt(3)
	v_mfma_f32_16x16x128_f8f6f4 v[134:137], v[122:127], v[2:7], 0 cbsz:2 blgp:2
	v_mfma_f32_16x16x128_f8f6f4 v[138:141], v[122:127], v[14:19], 0 cbsz:2 blgp:2
	v_mfma_f32_16x16x128_f8f6f4 v[142:145], v[122:127], v[26:31], v[188:191] cbsz:2 blgp:2
	v_mfma_f32_16x16x128_f8f6f4 v[204:207], v[122:127], v[38:43], 0 cbsz:2 blgp:2
	v_mfma_f32_16x16x128_f8f6f4 v[208:211], v[122:127], v[50:55], 0 cbsz:2 blgp:2
	v_mfma_f32_16x16x128_f8f6f4 v[212:215], v[122:127], v[62:67], v[188:191] cbsz:2 blgp:2
	s_waitcnt lgkmcnt(0)
	v_mfma_f32_16x16x128_f8f6f4 v[134:137], v[128:133], v[8:13], v[134:137] cbsz:2 blgp:2
	v_mfma_f32_16x16x128_f8f6f4 v[204:207], v[128:133], v[44:49], v[204:207] cbsz:2 blgp:2
	v_mfma_f32_16x16x128_f8f6f4 v[138:141], v[128:133], v[20:25], v[138:141] cbsz:2 blgp:2
	v_mfma_f32_16x16x128_f8f6f4 v[208:211], v[128:133], v[56:61], v[208:211] cbsz:2 blgp:2
	v_mfma_f32_16x16x128_f8f6f4 v[142:145], v[128:133], v[32:37], v[142:145] cbsz:2 blgp:2
	v_mfma_f32_16x16x128_f8f6f4 v[212:215], v[128:133], v[68:73], v[212:215] cbsz:2 blgp:2
	v_cndmask_b32_e64 v158, v134, v204, s[0:1]
	v_cndmask_b32_e64 v159, v138, v208, s[0:1]
	v_fma_mix_f32 v158, v158, v100, v147 op_sel_hi:[0,0,1]
	v_fma_mix_f32 v159, v159, v101, v151 op_sel_hi:[0,0,1]
	v_exp_f32_e32 v158, v158
	v_exp_f32_e32 v159, v159
	v_fma_f32 v158, v158, v186, v186
	v_add_f32_e32 v159, 1.0, v159
	v_rcp_f32_e32 v158, v158
	v_rcp_f32_e32 v159, v159
	v_cndmask_b32_e64 v160, v142, v212, s[0:1]
	v_fma_mix_f32 v161, v158, v160, v155 op_sel_hi:[0,0,1]
	v_exp_f32_e32 v161, v161
	s_add_u32 s48, s48, s40
	v_add_f32_e32 v161, 1.0, v161
	v_rcp_f32_e32 v161, v161
	s_addc_u32 s49, s49, s41
	v_fma_f32 v162, v161, -2.0, 1.0
	v_sub_f32_e32 v163, v176, v162
	v_fma_f32 v176, v159, v163, v162
	v_fma_f32 v164, |v176|, s17, v113
	v_fma_f32 v165, |v176|, s18, v114
	v_fma_f32 v166, |v176|, s19, v115
	v_lshrrev_b32_e32 v167, 26, v176
	v_min3_u32 v164, v164, v165, v166
	v_bfi_b32 v168, 31, v164, v167
	s_nop 1
	v_mul_u32_u24_dpp v170, v168, v180 quad_perm:[1,2,3,3] row_mask:0xf bank_mask:0xf bound_ctrl:1
	v_mad_u32_u24 v171, v168, v181, v170
	ds_write_b8_d16_hi v184, v171 offset:416
	s_barrier
	global_store_short_d16_hi v185, v176, s[48:49]
	s_waitcnt lgkmcnt(0)
	s_barrier
	ds_read_b64 v[122:123], v105 offset:416
	ds_read_b64 v[124:125], v105 offset:424
	ds_read_b64 v[126:127], v105 offset:432
	ds_read_b64 v[128:129], v105 offset:512
	ds_read_b64 v[130:131], v105 offset:520
	ds_read_b64 v[132:133], v105 offset:528
	s_waitcnt lgkmcnt(3)
	v_mfma_f32_16x16x128_f8f6f4 v[134:137], v[122:127], v[2:7], 0 cbsz:2 blgp:2
	v_mfma_f32_16x16x128_f8f6f4 v[138:141], v[122:127], v[14:19], 0 cbsz:2 blgp:2
	v_mfma_f32_16x16x128_f8f6f4 v[142:145], v[122:127], v[26:31], v[188:191] cbsz:2 blgp:2
	v_mfma_f32_16x16x128_f8f6f4 v[204:207], v[122:127], v[38:43], 0 cbsz:2 blgp:2
	v_mfma_f32_16x16x128_f8f6f4 v[208:211], v[122:127], v[50:55], 0 cbsz:2 blgp:2
	v_mfma_f32_16x16x128_f8f6f4 v[212:215], v[122:127], v[62:67], v[188:191] cbsz:2 blgp:2
	s_waitcnt lgkmcnt(0)
	v_mfma_f32_16x16x128_f8f6f4 v[134:137], v[128:133], v[8:13], v[134:137] cbsz:2 blgp:2
	v_mfma_f32_16x16x128_f8f6f4 v[204:207], v[128:133], v[44:49], v[204:207] cbsz:2 blgp:2
	v_mfma_f32_16x16x128_f8f6f4 v[138:141], v[128:133], v[20:25], v[138:141] cbsz:2 blgp:2
	v_mfma_f32_16x16x128_f8f6f4 v[208:211], v[128:133], v[56:61], v[208:211] cbsz:2 blgp:2
	v_mfma_f32_16x16x128_f8f6f4 v[142:145], v[128:133], v[32:37], v[142:145] cbsz:2 blgp:2
	v_mfma_f32_16x16x128_f8f6f4 v[212:215], v[128:133], v[68:73], v[212:215] cbsz:2 blgp:2
	v_cndmask_b32_e64 v158, v134, v204, s[0:1]
	v_cndmask_b32_e64 v159, v138, v208, s[0:1]
	v_fma_mix_f32 v158, v158, v100, v147 op_sel:[0,0,1] op_sel_hi:[0,0,1]
	v_fma_mix_f32 v159, v159, v101, v151 op_sel:[0,0,1] op_sel_hi:[0,0,1]
	v_exp_f32_e32 v158, v158
	v_exp_f32_e32 v159, v159
	v_fma_f32 v158, v158, v186, v186
	v_add_f32_e32 v159, 1.0, v159
	v_rcp_f32_e32 v158, v158
	v_rcp_f32_e32 v159, v159
	v_cndmask_b32_e64 v160, v142, v212, s[0:1]
	v_fma_mix_f32 v161, v158, v160, v155 op_sel:[0,0,1] op_sel_hi:[0,0,1]
	v_exp_f32_e32 v161, v161
	s_add_u32 s48, s48, s40
	v_add_f32_e32 v161, 1.0, v161
	v_rcp_f32_e32 v161, v161
	s_addc_u32 s49, s49, s41
	v_fma_f32 v162, v161, -2.0, 1.0
	v_sub_f32_e32 v163, v176, v162
	v_fma_f32 v176, v159, v163, v162
	v_fma_f32 v164, |v176|, s17, v113
	v_fma_f32 v165, |v176|, s18, v114
	v_fma_f32 v166, |v176|, s19, v115
	v_lshrrev_b32_e32 v167, 26, v176
	v_min3_u32 v164, v164, v165, v166
	v_bfi_b32 v168, 31, v164, v167
	s_nop 1
	v_mul_u32_u24_dpp v170, v168, v180 quad_perm:[1,2,3,3] row_mask:0xf bank_mask:0xf bound_ctrl:1
	v_mad_u32_u24 v171, v168, v181, v170
	ds_write_b8_d16_hi v184, v171
	s_barrier
	global_store_short_d16_hi v185, v176, s[48:49]
	s_waitcnt lgkmcnt(0)
	s_barrier
	ds_read_b64 v[122:123], v105 offset:0
	ds_read_b64 v[124:125], v105 offset:8
	ds_read_b64 v[126:127], v105 offset:16
	ds_read_b64 v[128:129], v105 offset:96
	ds_read_b64 v[130:131], v105 offset:104
	ds_read_b64 v[132:133], v105 offset:112
	s_waitcnt lgkmcnt(3)
	v_mfma_f32_16x16x128_f8f6f4 v[134:137], v[122:127], v[2:7], 0 cbsz:2 blgp:2
	v_mfma_f32_16x16x128_f8f6f4 v[138:141], v[122:127], v[14:19], 0 cbsz:2 blgp:2
	v_mfma_f32_16x16x128_f8f6f4 v[142:145], v[122:127], v[26:31], v[188:191] cbsz:2 blgp:2
	v_mfma_f32_16x16x128_f8f6f4 v[204:207], v[122:127], v[38:43], 0 cbsz:2 blgp:2
	v_mfma_f32_16x16x128_f8f6f4 v[208:211], v[122:127], v[50:55], 0 cbsz:2 blgp:2
	v_mfma_f32_16x16x128_f8f6f4 v[212:215], v[122:127], v[62:67], v[188:191] cbsz:2 blgp:2
	s_waitcnt lgkmcnt(0)
	v_mfma_f32_16x16x128_f8f6f4 v[134:137], v[128:133], v[8:13], v[134:137] cbsz:2 blgp:2
	v_mfma_f32_16x16x128_f8f6f4 v[204:207], v[128:133], v[44:49], v[204:207] cbsz:2 blgp:2
	v_mfma_f32_16x16x128_f8f6f4 v[138:141], v[128:133], v[20:25], v[138:141] cbsz:2 blgp:2
	v_mfma_f32_16x16x128_f8f6f4 v[208:211], v[128:133], v[56:61], v[208:211] cbsz:2 blgp:2
	v_mfma_f32_16x16x128_f8f6f4 v[142:145], v[128:133], v[32:37], v[142:145] cbsz:2 blgp:2
	v_mfma_f32_16x16x128_f8f6f4 v[212:215], v[128:133], v[68:73], v[212:215] cbsz:2 blgp:2
	v_cndmask_b32_e64 v158, v134, v204, s[0:1]
	v_cndmask_b32_e64 v159, v138, v208, s[0:1]
	v_fma_mix_f32 v158, v158, v100, v148 op_sel_hi:[0,0,1]
	v_fma_mix_f32 v159, v159, v101, v152 op_sel_hi:[0,0,1]
	v_exp_f32_e32 v158, v158
	v_exp_f32_e32 v159, v159
	v_fma_f32 v158, v158, v186, v186
	v_add_f32_e32 v159, 1.0, v159
	v_rcp_f32_e32 v158, v158
	v_rcp_f32_e32 v159, v159
	v_cndmask_b32_e64 v160, v142, v212, s[0:1]
	v_fma_mix_f32 v161, v158, v160, v156 op_sel_hi:[0,0,1]
	v_exp_f32_e32 v161, v161
	s_add_u32 s48, s48, s40
	v_add_f32_e32 v161, 1.0, v161
	v_rcp_f32_e32 v161, v161
	s_addc_u32 s49, s49, s41
	v_fma_f32 v162, v161, -2.0, 1.0
	v_sub_f32_e32 v163, v176, v162
	v_fma_f32 v176, v159, v163, v162
	v_fma_f32 v164, |v176|, s17, v113
	v_fma_f32 v165, |v176|, s18, v114
	v_fma_f32 v166, |v176|, s19, v115
	v_lshrrev_b32_e32 v167, 26, v176
	v_min3_u32 v164, v164, v165, v166
	v_bfi_b32 v168, 31, v164, v167
	s_nop 1
	v_mul_u32_u24_dpp v170, v168, v180 quad_perm:[1,2,3,3] row_mask:0xf bank_mask:0xf bound_ctrl:1
	v_mad_u32_u24 v171, v168, v181, v170
	ds_write_b8_d16_hi v184, v171 offset:416
	s_barrier
	global_store_short_d16_hi v185, v176, s[48:49]
	s_waitcnt lgkmcnt(0)
	s_barrier
	ds_read_b64 v[122:123], v105 offset:416
	ds_read_b64 v[124:125], v105 offset:424
	ds_read_b64 v[126:127], v105 offset:432
	ds_read_b64 v[128:129], v105 offset:512
	ds_read_b64 v[130:131], v105 offset:520
	ds_read_b64 v[132:133], v105 offset:528
	s_waitcnt lgkmcnt(3)
	v_mfma_f32_16x16x128_f8f6f4 v[134:137], v[122:127], v[2:7], 0 cbsz:2 blgp:2
	v_mfma_f32_16x16x128_f8f6f4 v[138:141], v[122:127], v[14:19], 0 cbsz:2 blgp:2
	v_mfma_f32_16x16x128_f8f6f4 v[142:145], v[122:127], v[26:31], v[188:191] cbsz:2 blgp:2
	v_mfma_f32_16x16x128_f8f6f4 v[204:207], v[122:127], v[38:43], 0 cbsz:2 blgp:2
	v_mfma_f32_16x16x128_f8f6f4 v[208:211], v[122:127], v[50:55], 0 cbsz:2 blgp:2
	v_mfma_f32_16x16x128_f8f6f4 v[212:215], v[122:127], v[62:67], v[188:191] cbsz:2 blgp:2
	s_waitcnt lgkmcnt(0)
	v_mfma_f32_16x16x128_f8f6f4 v[134:137], v[128:133], v[8:13], v[134:137] cbsz:2 blgp:2
	v_mfma_f32_16x16x128_f8f6f4 v[204:207], v[128:133], v[44:49], v[204:207] cbsz:2 blgp:2
	v_mfma_f32_16x16x128_f8f6f4 v[138:141], v[128:133], v[20:25], v[138:141] cbsz:2 blgp:2
	v_mfma_f32_16x16x128_f8f6f4 v[208:211], v[128:133], v[56:61], v[208:211] cbsz:2 blgp:2
	v_mfma_f32_16x16x128_f8f6f4 v[142:145], v[128:133], v[32:37], v[142:145] cbsz:2 blgp:2
	v_mfma_f32_16x16x128_f8f6f4 v[212:215], v[128:133], v[68:73], v[212:215] cbsz:2 blgp:2
	v_cndmask_b32_e64 v158, v134, v204, s[0:1]
	v_cndmask_b32_e64 v159, v138, v208, s[0:1]
	v_fma_mix_f32 v158, v158, v100, v148 op_sel:[0,0,1] op_sel_hi:[0,0,1]
	v_fma_mix_f32 v159, v159, v101, v152 op_sel:[0,0,1] op_sel_hi:[0,0,1]
	v_exp_f32_e32 v158, v158
	v_exp_f32_e32 v159, v159
	v_fma_f32 v158, v158, v186, v186
	v_add_f32_e32 v159, 1.0, v159
	v_rcp_f32_e32 v158, v158
	v_rcp_f32_e32 v159, v159
	v_cndmask_b32_e64 v160, v142, v212, s[0:1]
	v_fma_mix_f32 v161, v158, v160, v156 op_sel:[0,0,1] op_sel_hi:[0,0,1]
	v_exp_f32_e32 v161, v161
	s_add_u32 s48, s48, s40
	v_add_f32_e32 v161, 1.0, v161
	v_rcp_f32_e32 v161, v161
	s_addc_u32 s49, s49, s41
	v_fma_f32 v162, v161, -2.0, 1.0
	v_sub_f32_e32 v163, v176, v162
	v_fma_f32 v176, v159, v163, v162
	v_fma_f32 v164, |v176|, s17, v113
	v_fma_f32 v165, |v176|, s18, v114
	v_fma_f32 v166, |v176|, s19, v115
	v_lshrrev_b32_e32 v167, 26, v176
	v_min3_u32 v164, v164, v165, v166
	v_bfi_b32 v168, 31, v164, v167
	s_nop 1
	v_mul_u32_u24_dpp v170, v168, v180 quad_perm:[1,2,3,3] row_mask:0xf bank_mask:0xf bound_ctrl:1
	v_mad_u32_u24 v171, v168, v181, v170
	ds_write_b8_d16_hi v184, v171
	s_barrier
	global_store_short_d16_hi v185, v176, s[48:49]
	s_waitcnt lgkmcnt(0)
	s_barrier
	ds_read_b64 v[122:123], v105 offset:0
	ds_read_b64 v[124:125], v105 offset:8
	ds_read_b64 v[126:127], v105 offset:16
	ds_read_b64 v[128:129], v105 offset:96
	ds_read_b64 v[130:131], v105 offset:104
	ds_read_b64 v[132:133], v105 offset:112
	s_waitcnt lgkmcnt(3)
	v_mfma_f32_16x16x128_f8f6f4 v[134:137], v[122:127], v[2:7], 0 cbsz:2 blgp:2
	v_mfma_f32_16x16x128_f8f6f4 v[138:141], v[122:127], v[14:19], 0 cbsz:2 blgp:2
	v_mfma_f32_16x16x128_f8f6f4 v[142:145], v[122:127], v[26:31], v[188:191] cbsz:2 blgp:2
	v_mfma_f32_16x16x128_f8f6f4 v[204:207], v[122:127], v[38:43], 0 cbsz:2 blgp:2
	v_mfma_f32_16x16x128_f8f6f4 v[208:211], v[122:127], v[50:55], 0 cbsz:2 blgp:2
	v_mfma_f32_16x16x128_f8f6f4 v[212:215], v[122:127], v[62:67], v[188:191] cbsz:2 blgp:2
	s_waitcnt lgkmcnt(0)
	v_mfma_f32_16x16x128_f8f6f4 v[134:137], v[128:133], v[8:13], v[134:137] cbsz:2 blgp:2
	v_mfma_f32_16x16x128_f8f6f4 v[204:207], v[128:133], v[44:49], v[204:207] cbsz:2 blgp:2
	v_mfma_f32_16x16x128_f8f6f4 v[138:141], v[128:133], v[20:25], v[138:141] cbsz:2 blgp:2
	v_mfma_f32_16x16x128_f8f6f4 v[208:211], v[128:133], v[56:61], v[208:211] cbsz:2 blgp:2
	v_mfma_f32_16x16x128_f8f6f4 v[142:145], v[128:133], v[32:37], v[142:145] cbsz:2 blgp:2
	v_mfma_f32_16x16x128_f8f6f4 v[212:215], v[128:133], v[68:73], v[212:215] cbsz:2 blgp:2
	v_cndmask_b32_e64 v158, v134, v204, s[0:1]
	v_cndmask_b32_e64 v159, v138, v208, s[0:1]
	v_fma_mix_f32 v158, v158, v100, v149 op_sel_hi:[0,0,1]
	v_fma_mix_f32 v159, v159, v101, v153 op_sel_hi:[0,0,1]
	v_exp_f32_e32 v158, v158
	v_exp_f32_e32 v159, v159
	v_fma_f32 v158, v158, v186, v186
	v_add_f32_e32 v159, 1.0, v159
	v_rcp_f32_e32 v158, v158
	v_rcp_f32_e32 v159, v159
	v_cndmask_b32_e64 v160, v142, v212, s[0:1]
	v_fma_mix_f32 v161, v158, v160, v157 op_sel_hi:[0,0,1]
	v_exp_f32_e32 v161, v161
	s_add_u32 s48, s48, s40
	v_add_f32_e32 v161, 1.0, v161
	v_rcp_f32_e32 v161, v161
	s_addc_u32 s49, s49, s41
	v_fma_f32 v162, v161, -2.0, 1.0
	v_sub_f32_e32 v163, v176, v162
	v_fma_f32 v176, v159, v163, v162
	v_fma_f32 v164, |v176|, s17, v113
	v_fma_f32 v165, |v176|, s18, v114
	v_fma_f32 v166, |v176|, s19, v115
	v_lshrrev_b32_e32 v167, 26, v176
	v_min3_u32 v164, v164, v165, v166
	v_bfi_b32 v168, 31, v164, v167
	s_nop 1
	v_mul_u32_u24_dpp v170, v168, v180 quad_perm:[1,2,3,3] row_mask:0xf bank_mask:0xf bound_ctrl:1
	v_mad_u32_u24 v171, v168, v181, v170
	ds_write_b8_d16_hi v184, v171 offset:416
	s_barrier
	global_store_short_d16_hi v185, v176, s[48:49]
	s_waitcnt lgkmcnt(0)
	s_barrier
	ds_read_b64 v[122:123], v105 offset:416
	ds_read_b64 v[124:125], v105 offset:424
	ds_read_b64 v[126:127], v105 offset:432
	ds_read_b64 v[128:129], v105 offset:512
	ds_read_b64 v[130:131], v105 offset:520
	ds_read_b64 v[132:133], v105 offset:528
	s_add_i32 s44, s44, 16
	s_waitcnt lgkmcnt(3)
	v_mfma_f32_16x16x128_f8f6f4 v[134:137], v[122:127], v[2:7], 0 cbsz:2 blgp:2
	v_mfma_f32_16x16x128_f8f6f4 v[138:141], v[122:127], v[14:19], 0 cbsz:2 blgp:2
	v_mfma_f32_16x16x128_f8f6f4 v[142:145], v[122:127], v[26:31], v[188:191] cbsz:2 blgp:2
	v_mfma_f32_16x16x128_f8f6f4 v[204:207], v[122:127], v[38:43], 0 cbsz:2 blgp:2
	v_mfma_f32_16x16x128_f8f6f4 v[208:211], v[122:127], v[50:55], 0 cbsz:2 blgp:2
	v_mfma_f32_16x16x128_f8f6f4 v[212:215], v[122:127], v[62:67], v[188:191] cbsz:2 blgp:2
	s_waitcnt lgkmcnt(0)
	v_mfma_f32_16x16x128_f8f6f4 v[134:137], v[128:133], v[8:13], v[134:137] cbsz:2 blgp:2
	v_mfma_f32_16x16x128_f8f6f4 v[204:207], v[128:133], v[44:49], v[204:207] cbsz:2 blgp:2
	v_mfma_f32_16x16x128_f8f6f4 v[138:141], v[128:133], v[20:25], v[138:141] cbsz:2 blgp:2
	v_mfma_f32_16x16x128_f8f6f4 v[208:211], v[128:133], v[56:61], v[208:211] cbsz:2 blgp:2
	v_mfma_f32_16x16x128_f8f6f4 v[142:145], v[128:133], v[32:37], v[142:145] cbsz:2 blgp:2
	v_mfma_f32_16x16x128_f8f6f4 v[212:215], v[128:133], v[68:73], v[212:215] cbsz:2 blgp:2
	v_cndmask_b32_e64 v158, v134, v204, s[0:1]
	v_cndmask_b32_e64 v159, v138, v208, s[0:1]
	v_fma_mix_f32 v158, v158, v100, v149 op_sel:[0,0,1] op_sel_hi:[0,0,1]
	v_fma_mix_f32 v159, v159, v101, v153 op_sel:[0,0,1] op_sel_hi:[0,0,1]
	v_exp_f32_e32 v158, v158
	v_exp_f32_e32 v159, v159
	v_fma_f32 v158, v158, v186, v186
	v_add_f32_e32 v159, 1.0, v159
	v_rcp_f32_e32 v158, v158
	v_rcp_f32_e32 v159, v159
	v_cndmask_b32_e64 v160, v142, v212, s[0:1]
	v_fma_mix_f32 v161, v158, v160, v157 op_sel:[0,0,1] op_sel_hi:[0,0,1]
	v_exp_f32_e32 v161, v161
	s_add_u32 s48, s48, s40
	v_add_f32_e32 v161, 1.0, v161
	v_rcp_f32_e32 v161, v161
	s_addc_u32 s49, s49, s41
	v_fma_f32 v162, v161, -2.0, 1.0
	v_sub_f32_e32 v163, v176, v162
	v_fma_f32 v176, v159, v163, v162
	v_fma_f32 v164, |v176|, s17, v113
	v_fma_f32 v165, |v176|, s18, v114
	v_fma_f32 v166, |v176|, s19, v115
	v_lshrrev_b32_e32 v167, 26, v176
	v_min3_u32 v164, v164, v165, v166
	v_bfi_b32 v168, 31, v164, v167
	s_nop 1
	v_mul_u32_u24_dpp v170, v168, v180 quad_perm:[1,2,3,3] row_mask:0xf bank_mask:0xf bound_ctrl:1
	v_mad_u32_u24 v171, v168, v181, v170
	ds_write_b8_d16_hi v184, v171
	s_barrier
	global_store_short_d16_hi v185, v176, s[48:49]
	s_cmp_lt_i32 s44, s45
	s_waitcnt lgkmcnt(0)
	s_barrier
	s_cbranch_scc1 .Lscan_loop_b_f2
